# GEMM LD segments: all fragment ds_reads issued first (before LDS-DMA issue and the streamer address math), on top of split lgkm waits (4 late reads on 16-read segments)
# baseline (speedup 1.0000x reference)
.LBB0_219:
	s_waitcnt lgkmcnt(0)
	s_add_i32 s4, s92, 0x180
	s_add_i32 s5, s93, 0x180
	s_barrier
	s_setprio 1
	s_waitcnt lgkmcnt(7)
	v_mfma_f32_16x16x32_bf16 v[60:63], v[156:159], v[188:191], 0
	s_waitcnt lgkmcnt(6)
	v_mfma_f32_16x16x32_bf16 v[60:63], v[152:155], v[184:187], v[60:63]
	v_mfma_f32_16x16x32_bf16 v[56:59], v[148:151], v[188:191], 0
	s_nop 0
	v_mfma_f32_16x16x32_bf16 v[56:59], v[144:147], v[184:187], v[56:59]
	s_waitcnt lgkmcnt(5)
	v_mfma_f32_16x16x32_bf16 v[52:55], v[156:159], v[180:183], 0
	s_waitcnt lgkmcnt(4)
	v_mfma_f32_16x16x32_bf16 v[52:55], v[152:155], v[176:179], v[52:55]
	v_mfma_f32_16x16x32_bf16 v[48:51], v[148:151], v[180:183], 0
	s_nop 0
	v_mfma_f32_16x16x32_bf16 v[48:51], v[144:147], v[176:179], v[48:51]
	s_waitcnt lgkmcnt(3)
	v_mfma_f32_16x16x32_bf16 v[44:47], v[156:159], v[172:175], 0
	s_waitcnt lgkmcnt(2)
	v_mfma_f32_16x16x32_bf16 v[44:47], v[152:155], v[168:171], v[44:47]
	v_mfma_f32_16x16x32_bf16 v[40:43], v[148:151], v[172:175], 0
	s_nop 0
	v_mfma_f32_16x16x32_bf16 v[40:43], v[144:147], v[168:171], v[40:43]
	s_waitcnt lgkmcnt(1)
	v_mfma_f32_16x16x32_bf16 v[36:39], v[156:159], v[164:167], 0
	s_waitcnt lgkmcnt(0)
	v_mfma_f32_16x16x32_bf16 v[36:39], v[152:155], v[160:163], v[36:39]
	v_mfma_f32_16x16x32_bf16 v[32:35], v[148:151], v[164:167], 0
	s_nop 0
	v_mfma_f32_16x16x32_bf16 v[32:35], v[144:147], v[160:163], v[32:35]
	s_setprio 0
	s_setprio 1
	v_mfma_f32_16x16x32_bf16 v[28:31], v[140:143], v[188:191], 0
	s_nop 0
	v_mfma_f32_16x16x32_bf16 v[28:31], v[136:139], v[184:187], v[28:31]
	v_mfma_f32_16x16x32_bf16 v[24:27], v[132:135], v[188:191], 0
	s_nop 0
	v_mfma_f32_16x16x32_bf16 v[24:27], v[128:131], v[184:187], v[24:27]
	v_mfma_f32_16x16x32_bf16 v[20:23], v[140:143], v[180:183], 0
	s_nop 0
	v_mfma_f32_16x16x32_bf16 v[20:23], v[136:139], v[176:179], v[20:23]
	v_mfma_f32_16x16x32_bf16 v[16:19], v[132:135], v[180:183], 0
	s_nop 0
	v_mfma_f32_16x16x32_bf16 v[16:19], v[128:131], v[176:179], v[16:19]
	v_mfma_f32_16x16x32_bf16 v[12:15], v[140:143], v[172:175], 0
	s_nop 0
	v_mfma_f32_16x16x32_bf16 v[12:15], v[136:139], v[168:171], v[12:15]
	v_mfma_f32_16x16x32_bf16 v[8:11], v[132:135], v[172:175], 0
	s_nop 0
	v_mfma_f32_16x16x32_bf16 v[8:11], v[128:131], v[168:171], v[8:11]
	v_mfma_f32_16x16x32_bf16 v[4:7], v[140:143], v[164:167], 0
	s_nop 0
	v_mfma_f32_16x16x32_bf16 v[4:7], v[136:139], v[160:163], v[4:7]
	v_mfma_f32_16x16x32_bf16 v[0:3], v[132:135], v[164:167], 0
	s_nop 0
	v_mfma_f32_16x16x32_bf16 v[0:3], v[128:131], v[160:163], v[0:3]
	s_setprio 0
	s_barrier
	ds_read_b128 v[156:159], v211
	ds_read_b128 v[152:155], v212
	ds_read_b128 v[148:151], v213
	ds_read_b128 v[144:147], v214
	ds_read_b128 v[140:143], v215
	ds_read_b128 v[136:139], v216
	ds_read_b128 v[132:135], v217
	ds_read_b128 v[128:131], v218
	ds_read_b128 v[160:163], v219 offset:32768
	ds_read_b128 v[164:167], v219 offset:33792
	ds_read_b128 v[168:171], v219 offset:34816
	ds_read_b128 v[172:175], v219 offset:35840
	ds_read_b128 v[176:179], v219 offset:36864
	ds_read_b128 v[180:183], v219 offset:37888
	ds_read_b128 v[184:187], v219 offset:38912
	ds_read_b128 v[188:191], v219 offset:39936
	s_mov_b32 m0, s69
	s_add_i32 s14, s92, 0x20100
	buffer_load_dwordx4 v196, s[8:11], s14 offen lds
	s_add_i32 s14, s92, 0x30100
	s_mov_b32 m0, s70
	s_nop 0
	buffer_load_dwordx4 v196, s[8:11], s14 offen lds
	s_waitcnt vmcnt(8)
	s_waitcnt lgkmcnt(4)
	s_barrier
	s_setprio 1
	s_waitcnt lgkmcnt(7)
	v_mfma_f32_16x16x32_bf16 v[124:127], v[156:159], v[160:163], v[124:127]
	s_waitcnt lgkmcnt(6)
	v_mfma_f32_16x16x32_bf16 v[124:127], v[152:155], v[164:167], v[124:127]
	v_mfma_f32_16x16x32_bf16 v[120:123], v[148:151], v[160:163], v[120:123]
	s_nop 0
	v_mfma_f32_16x16x32_bf16 v[120:123], v[144:147], v[164:167], v[120:123]
	s_waitcnt lgkmcnt(5)
	v_mfma_f32_16x16x32_bf16 v[116:119], v[156:159], v[168:171], v[116:119]
	s_waitcnt lgkmcnt(4)
	v_mfma_f32_16x16x32_bf16 v[116:119], v[152:155], v[172:175], v[116:119]
	v_mfma_f32_16x16x32_bf16 v[112:115], v[148:151], v[168:171], v[112:115]
	s_nop 0
	v_mfma_f32_16x16x32_bf16 v[112:115], v[144:147], v[172:175], v[112:115]
	s_waitcnt lgkmcnt(3)
	v_mfma_f32_16x16x32_bf16 v[108:111], v[156:159], v[176:179], v[108:111]
	s_waitcnt lgkmcnt(2)
	v_mfma_f32_16x16x32_bf16 v[108:111], v[152:155], v[180:183], v[108:111]
	v_mfma_f32_16x16x32_bf16 v[104:107], v[148:151], v[176:179], v[104:107]
	s_nop 0
	v_mfma_f32_16x16x32_bf16 v[104:107], v[144:147], v[180:183], v[104:107]
	s_waitcnt lgkmcnt(1)
	v_mfma_f32_16x16x32_bf16 v[100:103], v[156:159], v[184:187], v[100:103]
	s_waitcnt lgkmcnt(0)
	v_mfma_f32_16x16x32_bf16 v[100:103], v[152:155], v[188:191], v[100:103]
	v_mfma_f32_16x16x32_bf16 v[96:99], v[148:151], v[184:187], v[96:99]
	s_nop 0
	v_mfma_f32_16x16x32_bf16 v[96:99], v[144:147], v[188:191], v[96:99]
	s_setprio 0
	s_setprio 1
	v_mfma_f32_16x16x32_bf16 v[92:95], v[140:143], v[160:163], v[92:95]
	s_nop 0
	v_mfma_f32_16x16x32_bf16 v[92:95], v[136:139], v[164:167], v[92:95]
	v_mfma_f32_16x16x32_bf16 v[88:91], v[132:135], v[160:163], v[88:91]
	s_nop 0
	v_mfma_f32_16x16x32_bf16 v[88:91], v[128:131], v[164:167], v[88:91]
	v_mfma_f32_16x16x32_bf16 v[84:87], v[140:143], v[168:171], v[84:87]
	s_nop 0
	v_mfma_f32_16x16x32_bf16 v[84:87], v[136:139], v[172:175], v[84:87]
	v_mfma_f32_16x16x32_bf16 v[80:83], v[132:135], v[168:171], v[80:83]
	s_nop 0
	v_mfma_f32_16x16x32_bf16 v[80:83], v[128:131], v[172:175], v[80:83]
	v_mfma_f32_16x16x32_bf16 v[76:79], v[140:143], v[176:179], v[76:79]
	s_nop 0
	v_mfma_f32_16x16x32_bf16 v[76:79], v[136:139], v[180:183], v[76:79]
	v_mfma_f32_16x16x32_bf16 v[72:75], v[132:135], v[176:179], v[72:75]
	s_nop 0
	v_mfma_f32_16x16x32_bf16 v[72:75], v[128:131], v[180:183], v[72:75]
	v_mfma_f32_16x16x32_bf16 v[68:71], v[140:143], v[184:187], v[68:71]
	s_nop 0
	v_mfma_f32_16x16x32_bf16 v[68:71], v[136:139], v[188:191], v[68:71]
	v_mfma_f32_16x16x32_bf16 v[64:67], v[132:135], v[184:187], v[64:67]
	s_nop 0
	v_mfma_f32_16x16x32_bf16 v[64:67], v[128:131], v[188:191], v[64:67]
	s_setprio 0
	s_barrier
	ds_read_b128 v[160:163], v219 offset:49152
	ds_read_b128 v[164:167], v219 offset:50176
	ds_read_b128 v[168:171], v219 offset:51200
	ds_read_b128 v[172:175], v219 offset:52224
	ds_read_b128 v[176:179], v219 offset:53248
	ds_read_b128 v[180:183], v219 offset:54272
	ds_read_b128 v[184:187], v219 offset:55296
	ds_read_b128 v[188:191], v219 offset:56320
	s_mov_b32 m0, s73
	s_mov_b32 s14, s10
	s_mov_b32 s15, s11
	buffer_load_dwordx4 v202, s[12:15], s5 offen lds
	s_add_i32 s5, s93, 0x80180
	s_mov_b32 m0, s74
	s_nop 0
	buffer_load_dwordx4 v202, s[12:15], s5 offen lds
	s_add_i32 s5, s93, 0x8180
	s_mov_b32 m0, s77
	s_nop 0
	buffer_load_dwordx4 v202, s[12:15], s5 offen lds
	s_add_i32 s5, s93, 0x88180
	s_mov_b32 m0, s78
	s_nop 0
	buffer_load_dwordx4 v202, s[12:15], s5 offen lds
	s_mov_b32 m0, s75
	s_nop 0
	buffer_load_dwordx4 v196, s[8:11], s4 offen lds
	s_add_i32 s4, s92, 0x10180
	s_mov_b32 m0, s76
	s_nop 0
	buffer_load_dwordx4 v196, s[8:11], s4 offen lds
	s_waitcnt vmcnt(8)
	s_waitcnt lgkmcnt(0)
	s_barrier
	s_setprio 1
	s_waitcnt lgkmcnt(7)
	v_mfma_f32_16x16x32_bf16 v[60:63], v[156:159], v[160:163], v[60:63]
	s_waitcnt lgkmcnt(6)
	v_mfma_f32_16x16x32_bf16 v[60:63], v[152:155], v[164:167], v[60:63]
	v_mfma_f32_16x16x32_bf16 v[56:59], v[148:151], v[160:163], v[56:59]
	s_nop 0
	v_mfma_f32_16x16x32_bf16 v[56:59], v[144:147], v[164:167], v[56:59]
	s_waitcnt lgkmcnt(5)
	v_mfma_f32_16x16x32_bf16 v[52:55], v[156:159], v[168:171], v[52:55]
	s_waitcnt lgkmcnt(4)
	v_mfma_f32_16x16x32_bf16 v[52:55], v[152:155], v[172:175], v[52:55]
	v_mfma_f32_16x16x32_bf16 v[48:51], v[148:151], v[168:171], v[48:51]
	s_nop 0
	v_mfma_f32_16x16x32_bf16 v[48:51], v[144:147], v[172:175], v[48:51]
	s_waitcnt lgkmcnt(3)
	v_mfma_f32_16x16x32_bf16 v[44:47], v[156:159], v[176:179], v[44:47]
	s_waitcnt lgkmcnt(2)
	v_mfma_f32_16x16x32_bf16 v[44:47], v[152:155], v[180:183], v[44:47]
	v_mfma_f32_16x16x32_bf16 v[40:43], v[148:151], v[176:179], v[40:43]
	s_nop 0
	v_mfma_f32_16x16x32_bf16 v[40:43], v[144:147], v[180:183], v[40:43]
	s_waitcnt lgkmcnt(1)
	v_mfma_f32_16x16x32_bf16 v[36:39], v[156:159], v[184:187], v[36:39]
	s_waitcnt lgkmcnt(0)
	v_mfma_f32_16x16x32_bf16 v[36:39], v[152:155], v[188:191], v[36:39]
	v_mfma_f32_16x16x32_bf16 v[32:35], v[148:151], v[184:187], v[32:35]
	s_nop 0
	v_mfma_f32_16x16x32_bf16 v[32:35], v[144:147], v[188:191], v[32:35]
	s_setprio 0
	s_setprio 1
	v_mfma_f32_16x16x32_bf16 v[28:31], v[140:143], v[160:163], v[28:31]
	s_nop 0
	v_mfma_f32_16x16x32_bf16 v[28:31], v[136:139], v[164:167], v[28:31]
	v_mfma_f32_16x16x32_bf16 v[24:27], v[132:135], v[160:163], v[24:27]
	s_nop 0
	v_mfma_f32_16x16x32_bf16 v[24:27], v[128:131], v[164:167], v[24:27]
	v_mfma_f32_16x16x32_bf16 v[20:23], v[140:143], v[168:171], v[20:23]
	s_nop 0
	v_mfma_f32_16x16x32_bf16 v[20:23], v[136:139], v[172:175], v[20:23]
	v_mfma_f32_16x16x32_bf16 v[16:19], v[132:135], v[168:171], v[16:19]
	s_nop 0
	v_mfma_f32_16x16x32_bf16 v[16:19], v[128:131], v[172:175], v[16:19]
	v_mfma_f32_16x16x32_bf16 v[12:15], v[140:143], v[176:179], v[12:15]
	s_nop 0
	v_mfma_f32_16x16x32_bf16 v[12:15], v[136:139], v[180:183], v[12:15]
	v_mfma_f32_16x16x32_bf16 v[8:11], v[132:135], v[176:179], v[8:11]
	s_nop 0
	v_mfma_f32_16x16x32_bf16 v[8:11], v[128:131], v[180:183], v[8:11]
	v_mfma_f32_16x16x32_bf16 v[4:7], v[140:143], v[184:187], v[4:7]
	s_nop 0
	v_mfma_f32_16x16x32_bf16 v[4:7], v[136:139], v[188:191], v[4:7]
	v_mfma_f32_16x16x32_bf16 v[0:3], v[132:135], v[184:187], v[0:3]
	s_nop 0
	v_mfma_f32_16x16x32_bf16 v[0:3], v[128:131], v[188:191], v[0:3]
	s_setprio 0
	s_barrier
	s_add_i32 s4, s92, 0x30180
	s_add_i32 s5, s93, 0x200
	s_mov_b32 s33, 0
.LBB0_220:
	ds_read_b128 v[128:131], v203
	ds_read_b128 v[132:135], v204
	ds_read_b128 v[136:139], v205
	ds_read_b128 v[140:143], v206
	ds_read_b128 v[144:147], v207
	ds_read_b128 v[148:151], v208
	ds_read_b128 v[152:155], v209
	ds_read_b128 v[156:159], v210
	ds_read_b128 v[160:163], v219
	ds_read_b128 v[164:167], v219 offset:1024
	ds_read_b128 v[168:171], v219 offset:2048
	ds_read_b128 v[172:175], v219 offset:3072
	ds_read_b128 v[176:179], v219 offset:4096
	ds_read_b128 v[180:183], v219 offset:5120
	ds_read_b128 v[184:187], v219 offset:6144
	ds_read_b128 v[188:191], v219 offset:7168
	s_add_i32 s66, s4, 0xfffd0080
	s_cmp_eq_u32 s33, 4
	s_cselect_b32 s66, s90, s66
	s_cselect_b32 s92, s91, s5
	s_add_i32 s67, s66, 0x80
	s_mov_b32 m0, s79
	s_add_i32 s93, s4, 0xffff0000
	buffer_load_dwordx4 v196, s[8:11], s93 offen lds
	s_mov_b32 m0, s81
	s_nop 0
	buffer_load_dwordx4 v196, s[8:11], s4 offen lds
	s_waitcnt vmcnt(8)
	s_waitcnt lgkmcnt(4)
	s_barrier
	s_setprio 1
	s_waitcnt lgkmcnt(7)
	v_mfma_f32_16x16x32_bf16 v[124:127], v[128:131], v[160:163], v[124:127]
	s_waitcnt lgkmcnt(6)
	v_mfma_f32_16x16x32_bf16 v[124:127], v[132:135], v[164:167], v[124:127]
	v_mfma_f32_16x16x32_bf16 v[120:123], v[136:139], v[160:163], v[120:123]
	s_nop 0
	v_mfma_f32_16x16x32_bf16 v[120:123], v[140:143], v[164:167], v[120:123]
	s_waitcnt lgkmcnt(5)
	v_mfma_f32_16x16x32_bf16 v[116:119], v[128:131], v[168:171], v[116:119]
	s_waitcnt lgkmcnt(4)
	v_mfma_f32_16x16x32_bf16 v[116:119], v[132:135], v[172:175], v[116:119]
	v_mfma_f32_16x16x32_bf16 v[112:115], v[136:139], v[168:171], v[112:115]
	s_nop 0
	v_mfma_f32_16x16x32_bf16 v[112:115], v[140:143], v[172:175], v[112:115]
	s_waitcnt lgkmcnt(3)
	v_mfma_f32_16x16x32_bf16 v[108:111], v[128:131], v[176:179], v[108:111]
	s_waitcnt lgkmcnt(2)
	v_mfma_f32_16x16x32_bf16 v[108:111], v[132:135], v[180:183], v[108:111]
	v_mfma_f32_16x16x32_bf16 v[104:107], v[136:139], v[176:179], v[104:107]
	s_nop 0
	v_mfma_f32_16x16x32_bf16 v[104:107], v[140:143], v[180:183], v[104:107]
	s_waitcnt lgkmcnt(1)
	v_mfma_f32_16x16x32_bf16 v[100:103], v[128:131], v[184:187], v[100:103]
	s_waitcnt lgkmcnt(0)
	v_mfma_f32_16x16x32_bf16 v[100:103], v[132:135], v[188:191], v[100:103]
	v_mfma_f32_16x16x32_bf16 v[96:99], v[136:139], v[184:187], v[96:99]
	s_nop 0
	v_mfma_f32_16x16x32_bf16 v[96:99], v[140:143], v[188:191], v[96:99]
	s_setprio 0
	s_setprio 1
	v_mfma_f32_16x16x32_bf16 v[92:95], v[144:147], v[160:163], v[92:95]
	s_nop 0
	v_mfma_f32_16x16x32_bf16 v[92:95], v[148:151], v[164:167], v[92:95]
	v_mfma_f32_16x16x32_bf16 v[88:91], v[152:155], v[160:163], v[88:91]
	s_nop 0
	v_mfma_f32_16x16x32_bf16 v[88:91], v[156:159], v[164:167], v[88:91]
	v_mfma_f32_16x16x32_bf16 v[84:87], v[144:147], v[168:171], v[84:87]
	s_nop 0
	v_mfma_f32_16x16x32_bf16 v[84:87], v[148:151], v[172:175], v[84:87]
	v_mfma_f32_16x16x32_bf16 v[80:83], v[152:155], v[168:171], v[80:83]
	s_nop 0
	v_mfma_f32_16x16x32_bf16 v[80:83], v[156:159], v[172:175], v[80:83]
	v_mfma_f32_16x16x32_bf16 v[76:79], v[144:147], v[176:179], v[76:79]
	s_nop 0
	v_mfma_f32_16x16x32_bf16 v[76:79], v[148:151], v[180:183], v[76:79]
	v_mfma_f32_16x16x32_bf16 v[72:75], v[152:155], v[176:179], v[72:75]
	s_nop 0
	v_mfma_f32_16x16x32_bf16 v[72:75], v[156:159], v[180:183], v[72:75]
	v_mfma_f32_16x16x32_bf16 v[68:71], v[144:147], v[184:187], v[68:71]
	s_nop 0
	v_mfma_f32_16x16x32_bf16 v[68:71], v[148:151], v[188:191], v[68:71]
	v_mfma_f32_16x16x32_bf16 v[64:67], v[152:155], v[184:187], v[64:67]
	s_nop 0
	v_mfma_f32_16x16x32_bf16 v[64:67], v[156:159], v[188:191], v[64:67]
	s_setprio 0
	s_barrier
	ds_read_b128 v[160:163], v219 offset:16384
	ds_read_b128 v[164:167], v219 offset:17408
	ds_read_b128 v[168:171], v219 offset:18432
	ds_read_b128 v[172:175], v219 offset:19456
	ds_read_b128 v[176:179], v219 offset:20480
	ds_read_b128 v[180:183], v219 offset:21504
	ds_read_b128 v[184:187], v219 offset:22528
	ds_read_b128 v[188:191], v219 offset:23552
	s_mov_b32 m0, s62
	s_add_i32 s93, s92, 0x80000
	buffer_load_dwordx4 v202, s[12:15], s92 offen lds
	s_mov_b32 m0, s63
	s_nop 0
	buffer_load_dwordx4 v202, s[12:15], s93 offen lds
	s_add_i32 s93, s92, 0x8000
	s_mov_b32 m0, s64
	s_nop 0
	buffer_load_dwordx4 v202, s[12:15], s93 offen lds
	s_add_i32 s93, s92, 0x88000
	s_mov_b32 m0, s65
	s_nop 0
	buffer_load_dwordx4 v202, s[12:15], s93 offen lds
	s_mov_b32 m0, s45
	s_add_i32 s93, s66, 0x10000
	buffer_load_dwordx4 v196, s[8:11], s66 offen lds
	s_mov_b32 m0, s68
	s_nop 0
	buffer_load_dwordx4 v196, s[8:11], s93 offen lds
	s_waitcnt vmcnt(8)
	s_waitcnt lgkmcnt(0)
	s_barrier
	s_setprio 1
	s_waitcnt lgkmcnt(7)
	v_mfma_f32_16x16x32_bf16 v[60:63], v[128:131], v[160:163], v[60:63]
	s_waitcnt lgkmcnt(6)
	v_mfma_f32_16x16x32_bf16 v[60:63], v[132:135], v[164:167], v[60:63]
	v_mfma_f32_16x16x32_bf16 v[56:59], v[136:139], v[160:163], v[56:59]
	s_nop 0
	v_mfma_f32_16x16x32_bf16 v[56:59], v[140:143], v[164:167], v[56:59]
	s_waitcnt lgkmcnt(5)
	v_mfma_f32_16x16x32_bf16 v[52:55], v[128:131], v[168:171], v[52:55]
	s_waitcnt lgkmcnt(4)
	v_mfma_f32_16x16x32_bf16 v[52:55], v[132:135], v[172:175], v[52:55]
	v_mfma_f32_16x16x32_bf16 v[48:51], v[136:139], v[168:171], v[48:51]
	s_nop 0
	v_mfma_f32_16x16x32_bf16 v[48:51], v[140:143], v[172:175], v[48:51]
	s_waitcnt lgkmcnt(3)
	v_mfma_f32_16x16x32_bf16 v[44:47], v[128:131], v[176:179], v[44:47]
	s_waitcnt lgkmcnt(2)
	v_mfma_f32_16x16x32_bf16 v[44:47], v[132:135], v[180:183], v[44:47]
	v_mfma_f32_16x16x32_bf16 v[40:43], v[136:139], v[176:179], v[40:43]
	s_nop 0
	v_mfma_f32_16x16x32_bf16 v[40:43], v[140:143], v[180:183], v[40:43]
	s_waitcnt lgkmcnt(1)
	v_mfma_f32_16x16x32_bf16 v[36:39], v[128:131], v[184:187], v[36:39]
	s_waitcnt lgkmcnt(0)
	v_mfma_f32_16x16x32_bf16 v[36:39], v[132:135], v[188:191], v[36:39]
	v_mfma_f32_16x16x32_bf16 v[32:35], v[136:139], v[184:187], v[32:35]
	s_nop 0
	v_mfma_f32_16x16x32_bf16 v[32:35], v[140:143], v[188:191], v[32:35]
	s_setprio 0
	s_setprio 1
	v_mfma_f32_16x16x32_bf16 v[28:31], v[144:147], v[160:163], v[28:31]
	s_nop 0
	v_mfma_f32_16x16x32_bf16 v[28:31], v[148:151], v[164:167], v[28:31]
	v_mfma_f32_16x16x32_bf16 v[24:27], v[152:155], v[160:163], v[24:27]
	s_nop 0
	v_mfma_f32_16x16x32_bf16 v[24:27], v[156:159], v[164:167], v[24:27]
	v_mfma_f32_16x16x32_bf16 v[20:23], v[144:147], v[168:171], v[20:23]
	s_nop 0
	v_mfma_f32_16x16x32_bf16 v[20:23], v[148:151], v[172:175], v[20:23]
	v_mfma_f32_16x16x32_bf16 v[16:19], v[152:155], v[168:171], v[16:19]
	s_nop 0
	v_mfma_f32_16x16x32_bf16 v[16:19], v[156:159], v[172:175], v[16:19]
	v_mfma_f32_16x16x32_bf16 v[12:15], v[144:147], v[176:179], v[12:15]
	s_nop 0
	v_mfma_f32_16x16x32_bf16 v[12:15], v[148:151], v[180:183], v[12:15]
	v_mfma_f32_16x16x32_bf16 v[8:11], v[152:155], v[176:179], v[8:11]
	s_nop 0
	v_mfma_f32_16x16x32_bf16 v[8:11], v[156:159], v[180:183], v[8:11]
	v_mfma_f32_16x16x32_bf16 v[4:7], v[144:147], v[184:187], v[4:7]
	s_nop 0
	v_mfma_f32_16x16x32_bf16 v[4:7], v[148:151], v[188:191], v[4:7]
	v_mfma_f32_16x16x32_bf16 v[0:3], v[152:155], v[184:187], v[0:3]
	s_nop 0
	v_mfma_f32_16x16x32_bf16 v[0:3], v[156:159], v[188:191], v[0:3]
	s_setprio 0
	s_barrier
	ds_read_b128 v[140:143], v211
	ds_read_b128 v[144:147], v212
	ds_read_b128 v[148:151], v213
	ds_read_b128 v[152:155], v214
	ds_read_b128 v[156:159], v215
	ds_read_b128 v[136:139], v216
	ds_read_b128 v[132:135], v217
	ds_read_b128 v[128:131], v218
	ds_read_b128 v[160:163], v219 offset:32768
	ds_read_b128 v[164:167], v219 offset:33792
	ds_read_b128 v[168:171], v219 offset:34816
	ds_read_b128 v[172:175], v219 offset:35840
	ds_read_b128 v[176:179], v219 offset:36864
	ds_read_b128 v[180:183], v219 offset:37888
	ds_read_b128 v[184:187], v219 offset:38912
	ds_read_b128 v[188:191], v219 offset:39936
	s_mov_b32 m0, s69
	s_add_i32 s93, s66, 0x20000
	buffer_load_dwordx4 v196, s[8:11], s93 offen lds
	s_add_i32 s93, s66, 0x30000
	s_mov_b32 m0, s70
	s_nop 0
	buffer_load_dwordx4 v196, s[8:11], s93 offen lds
	s_waitcnt vmcnt(8)
	s_waitcnt lgkmcnt(4)
	s_barrier
	s_setprio 1
	s_waitcnt lgkmcnt(7)
	v_mfma_f32_16x16x32_bf16 v[124:127], v[140:143], v[160:163], v[124:127]
	s_waitcnt lgkmcnt(6)
	v_mfma_f32_16x16x32_bf16 v[124:127], v[144:147], v[164:167], v[124:127]
	v_mfma_f32_16x16x32_bf16 v[120:123], v[148:151], v[160:163], v[120:123]
	s_nop 0
	v_mfma_f32_16x16x32_bf16 v[120:123], v[152:155], v[164:167], v[120:123]
	s_waitcnt lgkmcnt(5)
	v_mfma_f32_16x16x32_bf16 v[116:119], v[140:143], v[168:171], v[116:119]
	s_waitcnt lgkmcnt(4)
	v_mfma_f32_16x16x32_bf16 v[116:119], v[144:147], v[172:175], v[116:119]
	v_mfma_f32_16x16x32_bf16 v[112:115], v[148:151], v[168:171], v[112:115]
	s_nop 0
	v_mfma_f32_16x16x32_bf16 v[112:115], v[152:155], v[172:175], v[112:115]
	s_waitcnt lgkmcnt(3)
	v_mfma_f32_16x16x32_bf16 v[108:111], v[140:143], v[176:179], v[108:111]
	s_waitcnt lgkmcnt(2)
	v_mfma_f32_16x16x32_bf16 v[108:111], v[144:147], v[180:183], v[108:111]
	v_mfma_f32_16x16x32_bf16 v[104:107], v[148:151], v[176:179], v[104:107]
	s_nop 0
	v_mfma_f32_16x16x32_bf16 v[104:107], v[152:155], v[180:183], v[104:107]
	s_waitcnt lgkmcnt(1)
	v_mfma_f32_16x16x32_bf16 v[100:103], v[140:143], v[184:187], v[100:103]
	s_waitcnt lgkmcnt(0)
	v_mfma_f32_16x16x32_bf16 v[100:103], v[144:147], v[188:191], v[100:103]
	v_mfma_f32_16x16x32_bf16 v[96:99], v[148:151], v[184:187], v[96:99]
	s_nop 0
	v_mfma_f32_16x16x32_bf16 v[96:99], v[152:155], v[188:191], v[96:99]
	s_setprio 0
	s_setprio 1
	v_mfma_f32_16x16x32_bf16 v[92:95], v[156:159], v[160:163], v[92:95]
	s_nop 0
	v_mfma_f32_16x16x32_bf16 v[92:95], v[136:139], v[164:167], v[92:95]
	v_mfma_f32_16x16x32_bf16 v[88:91], v[132:135], v[160:163], v[88:91]
	s_nop 0
	v_mfma_f32_16x16x32_bf16 v[88:91], v[128:131], v[164:167], v[88:91]
	v_mfma_f32_16x16x32_bf16 v[84:87], v[156:159], v[168:171], v[84:87]
	s_nop 0
	v_mfma_f32_16x16x32_bf16 v[84:87], v[136:139], v[172:175], v[84:87]
	v_mfma_f32_16x16x32_bf16 v[80:83], v[132:135], v[168:171], v[80:83]
	s_nop 0
	v_mfma_f32_16x16x32_bf16 v[80:83], v[128:131], v[172:175], v[80:83]
	v_mfma_f32_16x16x32_bf16 v[76:79], v[156:159], v[176:179], v[76:79]
	s_nop 0
	v_mfma_f32_16x16x32_bf16 v[76:79], v[136:139], v[180:183], v[76:79]
	v_mfma_f32_16x16x32_bf16 v[72:75], v[132:135], v[176:179], v[72:75]
	s_nop 0
	v_mfma_f32_16x16x32_bf16 v[72:75], v[128:131], v[180:183], v[72:75]
	v_mfma_f32_16x16x32_bf16 v[68:71], v[156:159], v[184:187], v[68:71]
	s_nop 0
	v_mfma_f32_16x16x32_bf16 v[68:71], v[136:139], v[188:191], v[68:71]
	v_mfma_f32_16x16x32_bf16 v[64:67], v[132:135], v[184:187], v[64:67]
	s_nop 0
	v_mfma_f32_16x16x32_bf16 v[64:67], v[128:131], v[188:191], v[64:67]
	s_setprio 0
	s_barrier
	ds_read_b128 v[160:163], v219 offset:49152
	ds_read_b128 v[164:167], v219 offset:50176
	ds_read_b128 v[168:171], v219 offset:51200
	ds_read_b128 v[172:175], v219 offset:52224
	ds_read_b128 v[176:179], v219 offset:53248
	ds_read_b128 v[180:183], v219 offset:54272
	ds_read_b128 v[184:187], v219 offset:55296
	ds_read_b128 v[188:191], v219 offset:56320
	s_mov_b32 m0, s73
	s_add_i32 s93, s92, 0x80
	buffer_load_dwordx4 v202, s[12:15], s93 offen lds
	s_add_i32 s93, s92, 0x80080
	s_mov_b32 m0, s74
	s_add_i32 s66, s66, 0x10080
	buffer_load_dwordx4 v202, s[12:15], s93 offen lds
	s_add_i32 s93, s92, 0x8080
	s_mov_b32 m0, s77
	s_add_i32 s92, s92, 0x88080
	buffer_load_dwordx4 v202, s[12:15], s93 offen lds
	s_mov_b32 m0, s78
	s_nop 0
	buffer_load_dwordx4 v202, s[12:15], s92 offen lds
	s_mov_b32 m0, s75
	s_nop 0
	buffer_load_dwordx4 v196, s[8:11], s67 offen lds
	s_mov_b32 m0, s76
	s_nop 0
	buffer_load_dwordx4 v196, s[8:11], s66 offen lds
	s_waitcnt vmcnt(8)
	s_waitcnt lgkmcnt(0)
	s_barrier
	s_setprio 1
	s_waitcnt lgkmcnt(7)
	v_mfma_f32_16x16x32_bf16 v[60:63], v[140:143], v[160:163], v[60:63]
	s_waitcnt lgkmcnt(6)
	v_mfma_f32_16x16x32_bf16 v[60:63], v[144:147], v[164:167], v[60:63]
	v_mfma_f32_16x16x32_bf16 v[56:59], v[148:151], v[160:163], v[56:59]
	s_nop 0
	v_mfma_f32_16x16x32_bf16 v[56:59], v[152:155], v[164:167], v[56:59]
	s_waitcnt lgkmcnt(5)
	v_mfma_f32_16x16x32_bf16 v[52:55], v[140:143], v[168:171], v[52:55]
	s_waitcnt lgkmcnt(4)
	v_mfma_f32_16x16x32_bf16 v[52:55], v[144:147], v[172:175], v[52:55]
	v_mfma_f32_16x16x32_bf16 v[48:51], v[148:151], v[168:171], v[48:51]
	s_nop 0
	v_mfma_f32_16x16x32_bf16 v[48:51], v[152:155], v[172:175], v[48:51]
	s_waitcnt lgkmcnt(3)
	v_mfma_f32_16x16x32_bf16 v[44:47], v[140:143], v[176:179], v[44:47]
	s_waitcnt lgkmcnt(2)
	v_mfma_f32_16x16x32_bf16 v[44:47], v[144:147], v[180:183], v[44:47]
	v_mfma_f32_16x16x32_bf16 v[40:43], v[148:151], v[176:179], v[40:43]
	s_nop 0
	v_mfma_f32_16x16x32_bf16 v[40:43], v[152:155], v[180:183], v[40:43]
	s_waitcnt lgkmcnt(1)
	v_mfma_f32_16x16x32_bf16 v[36:39], v[140:143], v[184:187], v[36:39]
	s_waitcnt lgkmcnt(0)
	v_mfma_f32_16x16x32_bf16 v[36:39], v[144:147], v[188:191], v[36:39]
	v_mfma_f32_16x16x32_bf16 v[32:35], v[148:151], v[184:187], v[32:35]
	s_nop 0
	v_mfma_f32_16x16x32_bf16 v[32:35], v[152:155], v[188:191], v[32:35]
	s_setprio 0
	s_setprio 1
	v_mfma_f32_16x16x32_bf16 v[28:31], v[156:159], v[160:163], v[28:31]
	s_nop 0
	v_mfma_f32_16x16x32_bf16 v[28:31], v[136:139], v[164:167], v[28:31]
	v_mfma_f32_16x16x32_bf16 v[24:27], v[132:135], v[160:163], v[24:27]
	s_nop 0
	v_mfma_f32_16x16x32_bf16 v[24:27], v[128:131], v[164:167], v[24:27]
	v_mfma_f32_16x16x32_bf16 v[20:23], v[156:159], v[168:171], v[20:23]
	s_nop 0
	v_mfma_f32_16x16x32_bf16 v[20:23], v[136:139], v[172:175], v[20:23]
	v_mfma_f32_16x16x32_bf16 v[16:19], v[132:135], v[168:171], v[16:19]
	s_nop 0
	v_mfma_f32_16x16x32_bf16 v[16:19], v[128:131], v[172:175], v[16:19]
	v_mfma_f32_16x16x32_bf16 v[12:15], v[156:159], v[176:179], v[12:15]
	s_nop 0
	v_mfma_f32_16x16x32_bf16 v[12:15], v[136:139], v[180:183], v[12:15]
	v_mfma_f32_16x16x32_bf16 v[8:11], v[132:135], v[176:179], v[8:11]
	s_nop 0
	v_mfma_f32_16x16x32_bf16 v[8:11], v[128:131], v[180:183], v[8:11]
	v_mfma_f32_16x16x32_bf16 v[4:7], v[156:159], v[184:187], v[4:7]
	s_nop 0
	v_mfma_f32_16x16x32_bf16 v[4:7], v[136:139], v[188:191], v[4:7]
	v_mfma_f32_16x16x32_bf16 v[0:3], v[132:135], v[184:187], v[0:3]
	s_nop 0
	v_mfma_f32_16x16x32_bf16 v[0:3], v[128:131], v[188:191], v[0:3]
	s_setprio 0
	s_barrier
	s_add_i32 s33, s33, 2
	s_addk_i32 s4, 0x100
	s_addk_i32 s5, 0x100
	s_cmp_gt_u32 s33, 5
	s_cbranch_scc0 .LBB0_220
	s_and_b64 vcc, exec, s[16:17]
	s_cbranch_vccz .LBB0_223
	s_barrier

.LBB0_253:
	s_waitcnt lgkmcnt(0)
	s_add_i32 s33, s91, 0x180
	s_add_i32 s42, s90, 0x180
	s_barrier
	s_setprio 1
	s_waitcnt lgkmcnt(7)
	v_mfma_f32_16x16x32_bf16 v[60:63], v[156:159], v[188:191], 0
	s_waitcnt lgkmcnt(6)
	v_mfma_f32_16x16x32_bf16 v[60:63], v[152:155], v[184:187], v[60:63]
	v_mfma_f32_16x16x32_bf16 v[56:59], v[148:151], v[188:191], 0
	s_nop 0
	v_mfma_f32_16x16x32_bf16 v[56:59], v[144:147], v[184:187], v[56:59]
	s_waitcnt lgkmcnt(5)
	v_mfma_f32_16x16x32_bf16 v[52:55], v[156:159], v[180:183], 0
	s_waitcnt lgkmcnt(4)
	v_mfma_f32_16x16x32_bf16 v[52:55], v[152:155], v[176:179], v[52:55]
	v_mfma_f32_16x16x32_bf16 v[48:51], v[148:151], v[180:183], 0
	s_nop 0
	v_mfma_f32_16x16x32_bf16 v[48:51], v[144:147], v[176:179], v[48:51]
	s_waitcnt lgkmcnt(3)
	v_mfma_f32_16x16x32_bf16 v[44:47], v[156:159], v[172:175], 0
	s_waitcnt lgkmcnt(2)
	v_mfma_f32_16x16x32_bf16 v[44:47], v[152:155], v[168:171], v[44:47]
	v_mfma_f32_16x16x32_bf16 v[40:43], v[148:151], v[172:175], 0
	s_nop 0
	v_mfma_f32_16x16x32_bf16 v[40:43], v[144:147], v[168:171], v[40:43]
	s_waitcnt lgkmcnt(1)
	v_mfma_f32_16x16x32_bf16 v[36:39], v[156:159], v[164:167], 0
	s_waitcnt lgkmcnt(0)
	v_mfma_f32_16x16x32_bf16 v[36:39], v[152:155], v[160:163], v[36:39]
	v_mfma_f32_16x16x32_bf16 v[32:35], v[148:151], v[164:167], 0
	s_nop 0
	v_mfma_f32_16x16x32_bf16 v[32:35], v[144:147], v[160:163], v[32:35]
	s_setprio 0
	s_setprio 1
	v_mfma_f32_16x16x32_bf16 v[28:31], v[140:143], v[188:191], 0
	s_nop 0
	v_mfma_f32_16x16x32_bf16 v[28:31], v[136:139], v[184:187], v[28:31]
	v_mfma_f32_16x16x32_bf16 v[24:27], v[132:135], v[188:191], 0
	s_nop 0
	v_mfma_f32_16x16x32_bf16 v[24:27], v[128:131], v[184:187], v[24:27]
	v_mfma_f32_16x16x32_bf16 v[20:23], v[140:143], v[180:183], 0
	s_nop 0
	v_mfma_f32_16x16x32_bf16 v[20:23], v[136:139], v[176:179], v[20:23]
	v_mfma_f32_16x16x32_bf16 v[16:19], v[132:135], v[180:183], 0
	s_nop 0
	v_mfma_f32_16x16x32_bf16 v[16:19], v[128:131], v[176:179], v[16:19]
	v_mfma_f32_16x16x32_bf16 v[12:15], v[140:143], v[172:175], 0
	s_nop 0
	v_mfma_f32_16x16x32_bf16 v[12:15], v[136:139], v[168:171], v[12:15]
	v_mfma_f32_16x16x32_bf16 v[8:11], v[132:135], v[172:175], 0
	s_nop 0
	v_mfma_f32_16x16x32_bf16 v[8:11], v[128:131], v[168:171], v[8:11]
	v_mfma_f32_16x16x32_bf16 v[4:7], v[140:143], v[164:167], 0
	s_nop 0
	v_mfma_f32_16x16x32_bf16 v[4:7], v[136:139], v[160:163], v[4:7]
	v_mfma_f32_16x16x32_bf16 v[0:3], v[132:135], v[164:167], 0
	s_nop 0
	v_mfma_f32_16x16x32_bf16 v[0:3], v[128:131], v[160:163], v[0:3]
	s_setprio 0
	s_barrier
	ds_read_b128 v[156:159], v203
	ds_read_b128 v[152:155], v204
	ds_read_b128 v[148:151], v205
	ds_read_b128 v[144:147], v206
	ds_read_b128 v[140:143], v207
	ds_read_b128 v[136:139], v208
	ds_read_b128 v[132:135], v209
	ds_read_b128 v[128:131], v210
	ds_read_b128 v[160:163], v197 offset:32768
	ds_read_b128 v[164:167], v197 offset:33792
	ds_read_b128 v[168:171], v197 offset:34816
	ds_read_b128 v[172:175], v197 offset:35840
	ds_read_b128 v[176:179], v197 offset:36864
	ds_read_b128 v[180:183], v197 offset:37888
	ds_read_b128 v[184:187], v197 offset:38912
	ds_read_b128 v[188:191], v197 offset:39936
	s_mov_b32 m0, s69
	s_add_i32 s10, s91, 0x20100
	buffer_load_dwordx4 v196, s[4:7], s10 offen lds
	s_add_i32 s10, s91, 0x30100
	s_mov_b32 m0, s70
	s_nop 0
	buffer_load_dwordx4 v196, s[4:7], s10 offen lds
	s_waitcnt vmcnt(8)
	s_waitcnt lgkmcnt(4)
	s_barrier
	s_setprio 1
	s_waitcnt lgkmcnt(7)
	v_mfma_f32_16x16x32_bf16 v[124:127], v[156:159], v[160:163], v[124:127]
	s_waitcnt lgkmcnt(6)
	v_mfma_f32_16x16x32_bf16 v[124:127], v[152:155], v[164:167], v[124:127]
	v_mfma_f32_16x16x32_bf16 v[120:123], v[148:151], v[160:163], v[120:123]
	s_nop 0
	v_mfma_f32_16x16x32_bf16 v[120:123], v[144:147], v[164:167], v[120:123]
	s_waitcnt lgkmcnt(5)
	v_mfma_f32_16x16x32_bf16 v[116:119], v[156:159], v[168:171], v[116:119]
	s_waitcnt lgkmcnt(4)
	v_mfma_f32_16x16x32_bf16 v[116:119], v[152:155], v[172:175], v[116:119]
	v_mfma_f32_16x16x32_bf16 v[112:115], v[148:151], v[168:171], v[112:115]
	s_nop 0
	v_mfma_f32_16x16x32_bf16 v[112:115], v[144:147], v[172:175], v[112:115]
	s_waitcnt lgkmcnt(3)
	v_mfma_f32_16x16x32_bf16 v[108:111], v[156:159], v[176:179], v[108:111]
	s_waitcnt lgkmcnt(2)
	v_mfma_f32_16x16x32_bf16 v[108:111], v[152:155], v[180:183], v[108:111]
	v_mfma_f32_16x16x32_bf16 v[104:107], v[148:151], v[176:179], v[104:107]
	s_nop 0
	v_mfma_f32_16x16x32_bf16 v[104:107], v[144:147], v[180:183], v[104:107]
	s_waitcnt lgkmcnt(1)
	v_mfma_f32_16x16x32_bf16 v[100:103], v[156:159], v[184:187], v[100:103]
	s_waitcnt lgkmcnt(0)
	v_mfma_f32_16x16x32_bf16 v[100:103], v[152:155], v[188:191], v[100:103]
	v_mfma_f32_16x16x32_bf16 v[96:99], v[148:151], v[184:187], v[96:99]
	s_nop 0
	v_mfma_f32_16x16x32_bf16 v[96:99], v[144:147], v[188:191], v[96:99]
	s_setprio 0
	s_setprio 1
	v_mfma_f32_16x16x32_bf16 v[92:95], v[140:143], v[160:163], v[92:95]
	s_nop 0
	v_mfma_f32_16x16x32_bf16 v[92:95], v[136:139], v[164:167], v[92:95]
	v_mfma_f32_16x16x32_bf16 v[88:91], v[132:135], v[160:163], v[88:91]
	s_nop 0
	v_mfma_f32_16x16x32_bf16 v[88:91], v[128:131], v[164:167], v[88:91]
	v_mfma_f32_16x16x32_bf16 v[84:87], v[140:143], v[168:171], v[84:87]
	s_nop 0
	v_mfma_f32_16x16x32_bf16 v[84:87], v[136:139], v[172:175], v[84:87]
	v_mfma_f32_16x16x32_bf16 v[80:83], v[132:135], v[168:171], v[80:83]
	s_nop 0
	v_mfma_f32_16x16x32_bf16 v[80:83], v[128:131], v[172:175], v[80:83]
	v_mfma_f32_16x16x32_bf16 v[76:79], v[140:143], v[176:179], v[76:79]
	s_nop 0
	v_mfma_f32_16x16x32_bf16 v[76:79], v[136:139], v[180:183], v[76:79]
	v_mfma_f32_16x16x32_bf16 v[72:75], v[132:135], v[176:179], v[72:75]
	s_nop 0
	v_mfma_f32_16x16x32_bf16 v[72:75], v[128:131], v[180:183], v[72:75]
	v_mfma_f32_16x16x32_bf16 v[68:71], v[140:143], v[184:187], v[68:71]
	s_nop 0
	v_mfma_f32_16x16x32_bf16 v[68:71], v[136:139], v[188:191], v[68:71]
	v_mfma_f32_16x16x32_bf16 v[64:67], v[132:135], v[184:187], v[64:67]
	s_nop 0
	v_mfma_f32_16x16x32_bf16 v[64:67], v[128:131], v[188:191], v[64:67]
	s_setprio 0
	s_barrier
	ds_read_b128 v[160:163], v197 offset:49152
	ds_read_b128 v[164:167], v197 offset:50176
	ds_read_b128 v[168:171], v197 offset:51200
	ds_read_b128 v[172:175], v197 offset:52224
	ds_read_b128 v[176:179], v197 offset:53248
	ds_read_b128 v[180:183], v197 offset:54272
	ds_read_b128 v[184:187], v197 offset:55296
	ds_read_b128 v[188:191], v197 offset:56320
	s_mov_b32 m0, s72
	s_mov_b32 s10, s6
	s_mov_b32 s11, s7
	buffer_load_dwordx4 v192, s[8:11], s42 offen lds
	s_add_i32 s42, s90, 0x20180
	s_mov_b32 m0, s73
	s_nop 0
	buffer_load_dwordx4 v192, s[8:11], s42 offen lds
	s_add_i32 s42, s90, 0x2180
	s_mov_b32 m0, s76
	s_nop 0
	buffer_load_dwordx4 v192, s[8:11], s42 offen lds
	s_add_i32 s42, s90, 0x22180
	s_mov_b32 m0, s77
	s_nop 0
	buffer_load_dwordx4 v192, s[8:11], s42 offen lds
	s_mov_b32 m0, s74
	s_nop 0
	buffer_load_dwordx4 v196, s[4:7], s33 offen lds
	s_add_i32 s33, s91, 0x10180
	s_mov_b32 m0, s75
	s_nop 0
	buffer_load_dwordx4 v196, s[4:7], s33 offen lds
	s_waitcnt vmcnt(8)
	s_waitcnt lgkmcnt(0)
	s_barrier
	s_setprio 1
	s_waitcnt lgkmcnt(7)
	v_mfma_f32_16x16x32_bf16 v[60:63], v[156:159], v[160:163], v[60:63]
	s_waitcnt lgkmcnt(6)
	v_mfma_f32_16x16x32_bf16 v[60:63], v[152:155], v[164:167], v[60:63]
	v_mfma_f32_16x16x32_bf16 v[56:59], v[148:151], v[160:163], v[56:59]
	s_nop 0
	v_mfma_f32_16x16x32_bf16 v[56:59], v[144:147], v[164:167], v[56:59]
	s_waitcnt lgkmcnt(5)
	v_mfma_f32_16x16x32_bf16 v[52:55], v[156:159], v[168:171], v[52:55]
	s_waitcnt lgkmcnt(4)
	v_mfma_f32_16x16x32_bf16 v[52:55], v[152:155], v[172:175], v[52:55]
	v_mfma_f32_16x16x32_bf16 v[48:51], v[148:151], v[168:171], v[48:51]
	s_nop 0
	v_mfma_f32_16x16x32_bf16 v[48:51], v[144:147], v[172:175], v[48:51]
	s_waitcnt lgkmcnt(3)
	v_mfma_f32_16x16x32_bf16 v[44:47], v[156:159], v[176:179], v[44:47]
	s_waitcnt lgkmcnt(2)
	v_mfma_f32_16x16x32_bf16 v[44:47], v[152:155], v[180:183], v[44:47]
	v_mfma_f32_16x16x32_bf16 v[40:43], v[148:151], v[176:179], v[40:43]
	s_nop 0
	v_mfma_f32_16x16x32_bf16 v[40:43], v[144:147], v[180:183], v[40:43]
	s_waitcnt lgkmcnt(1)
	v_mfma_f32_16x16x32_bf16 v[36:39], v[156:159], v[184:187], v[36:39]
	s_waitcnt lgkmcnt(0)
	v_mfma_f32_16x16x32_bf16 v[36:39], v[152:155], v[188:191], v[36:39]
	v_mfma_f32_16x16x32_bf16 v[32:35], v[148:151], v[184:187], v[32:35]
	s_nop 0
	v_mfma_f32_16x16x32_bf16 v[32:35], v[144:147], v[188:191], v[32:35]
	s_setprio 0
	s_setprio 1
	v_mfma_f32_16x16x32_bf16 v[28:31], v[140:143], v[160:163], v[28:31]
	s_nop 0
	v_mfma_f32_16x16x32_bf16 v[28:31], v[136:139], v[164:167], v[28:31]
	v_mfma_f32_16x16x32_bf16 v[24:27], v[132:135], v[160:163], v[24:27]
	s_nop 0
	v_mfma_f32_16x16x32_bf16 v[24:27], v[128:131], v[164:167], v[24:27]
	v_mfma_f32_16x16x32_bf16 v[20:23], v[140:143], v[168:171], v[20:23]
	s_nop 0
	v_mfma_f32_16x16x32_bf16 v[20:23], v[136:139], v[172:175], v[20:23]
	v_mfma_f32_16x16x32_bf16 v[16:19], v[132:135], v[168:171], v[16:19]
	s_nop 0
	v_mfma_f32_16x16x32_bf16 v[16:19], v[128:131], v[172:175], v[16:19]
	v_mfma_f32_16x16x32_bf16 v[12:15], v[140:143], v[176:179], v[12:15]
	s_nop 0
	v_mfma_f32_16x16x32_bf16 v[12:15], v[136:139], v[180:183], v[12:15]
	v_mfma_f32_16x16x32_bf16 v[8:11], v[132:135], v[176:179], v[8:11]
	s_nop 0
	v_mfma_f32_16x16x32_bf16 v[8:11], v[128:131], v[180:183], v[8:11]
	v_mfma_f32_16x16x32_bf16 v[4:7], v[140:143], v[184:187], v[4:7]
	s_nop 0
	v_mfma_f32_16x16x32_bf16 v[4:7], v[136:139], v[188:191], v[4:7]
	v_mfma_f32_16x16x32_bf16 v[0:3], v[132:135], v[184:187], v[0:3]
	s_nop 0
	v_mfma_f32_16x16x32_bf16 v[0:3], v[128:131], v[188:191], v[0:3]
	s_setprio 0
	s_barrier
	s_add_i32 s33, s91, 0x30180
	s_add_i32 s42, s90, 0x200
	s_mov_b32 s43, 0
.LBB0_254:
	ds_read_b128 v[128:131], v193
	ds_read_b128 v[132:135], v194
	ds_read_b128 v[136:139], v195
	ds_read_b128 v[140:143], v198
	ds_read_b128 v[144:147], v199
	ds_read_b128 v[148:151], v200
	ds_read_b128 v[152:155], v201
	ds_read_b128 v[156:159], v202
	ds_read_b128 v[160:163], v197
	ds_read_b128 v[164:167], v197 offset:1024
	ds_read_b128 v[168:171], v197 offset:2048
	ds_read_b128 v[172:175], v197 offset:3072
	ds_read_b128 v[176:179], v197 offset:4096
	ds_read_b128 v[180:183], v197 offset:5120
	ds_read_b128 v[184:187], v197 offset:6144
	ds_read_b128 v[188:191], v197 offset:7168
	s_add_i32 s66, s33, 0xfffd0080
	s_cmp_eq_u32 s43, 4
	s_cselect_b32 s66, s88, s66
	s_cselect_b32 s90, s89, s42
	s_add_i32 s67, s66, 0x80
	s_mov_b32 m0, s78
	s_add_i32 s91, s33, 0xffff0000
	buffer_load_dwordx4 v196, s[4:7], s91 offen lds
	s_mov_b32 m0, s79
	s_nop 0
	buffer_load_dwordx4 v196, s[4:7], s33 offen lds
	s_waitcnt vmcnt(8)
	s_waitcnt lgkmcnt(4)
	s_barrier
	s_setprio 1
	s_waitcnt lgkmcnt(7)
	v_mfma_f32_16x16x32_bf16 v[124:127], v[128:131], v[160:163], v[124:127]
	s_waitcnt lgkmcnt(6)
	v_mfma_f32_16x16x32_bf16 v[124:127], v[132:135], v[164:167], v[124:127]
	v_mfma_f32_16x16x32_bf16 v[120:123], v[136:139], v[160:163], v[120:123]
	s_nop 0
	v_mfma_f32_16x16x32_bf16 v[120:123], v[140:143], v[164:167], v[120:123]
	s_waitcnt lgkmcnt(5)
	v_mfma_f32_16x16x32_bf16 v[116:119], v[128:131], v[168:171], v[116:119]
	s_waitcnt lgkmcnt(4)
	v_mfma_f32_16x16x32_bf16 v[116:119], v[132:135], v[172:175], v[116:119]
	v_mfma_f32_16x16x32_bf16 v[112:115], v[136:139], v[168:171], v[112:115]
	s_nop 0
	v_mfma_f32_16x16x32_bf16 v[112:115], v[140:143], v[172:175], v[112:115]
	s_waitcnt lgkmcnt(3)
	v_mfma_f32_16x16x32_bf16 v[108:111], v[128:131], v[176:179], v[108:111]
	s_waitcnt lgkmcnt(2)
	v_mfma_f32_16x16x32_bf16 v[108:111], v[132:135], v[180:183], v[108:111]
	v_mfma_f32_16x16x32_bf16 v[104:107], v[136:139], v[176:179], v[104:107]
	s_nop 0
	v_mfma_f32_16x16x32_bf16 v[104:107], v[140:143], v[180:183], v[104:107]
	s_waitcnt lgkmcnt(1)
	v_mfma_f32_16x16x32_bf16 v[100:103], v[128:131], v[184:187], v[100:103]
	s_waitcnt lgkmcnt(0)
	v_mfma_f32_16x16x32_bf16 v[100:103], v[132:135], v[188:191], v[100:103]
	v_mfma_f32_16x16x32_bf16 v[96:99], v[136:139], v[184:187], v[96:99]
	s_nop 0
	v_mfma_f32_16x16x32_bf16 v[96:99], v[140:143], v[188:191], v[96:99]
	s_setprio 0
	s_setprio 1
	v_mfma_f32_16x16x32_bf16 v[92:95], v[144:147], v[160:163], v[92:95]
	s_nop 0
	v_mfma_f32_16x16x32_bf16 v[92:95], v[148:151], v[164:167], v[92:95]
	v_mfma_f32_16x16x32_bf16 v[88:91], v[152:155], v[160:163], v[88:91]
	s_nop 0
	v_mfma_f32_16x16x32_bf16 v[88:91], v[156:159], v[164:167], v[88:91]
	v_mfma_f32_16x16x32_bf16 v[84:87], v[144:147], v[168:171], v[84:87]
	s_nop 0
	v_mfma_f32_16x16x32_bf16 v[84:87], v[148:151], v[172:175], v[84:87]
	v_mfma_f32_16x16x32_bf16 v[80:83], v[152:155], v[168:171], v[80:83]
	s_nop 0
	v_mfma_f32_16x16x32_bf16 v[80:83], v[156:159], v[172:175], v[80:83]
	v_mfma_f32_16x16x32_bf16 v[76:79], v[144:147], v[176:179], v[76:79]
	s_nop 0
	v_mfma_f32_16x16x32_bf16 v[76:79], v[148:151], v[180:183], v[76:79]
	v_mfma_f32_16x16x32_bf16 v[72:75], v[152:155], v[176:179], v[72:75]
	s_nop 0
	v_mfma_f32_16x16x32_bf16 v[72:75], v[156:159], v[180:183], v[72:75]
	v_mfma_f32_16x16x32_bf16 v[68:71], v[144:147], v[184:187], v[68:71]
	s_nop 0
	v_mfma_f32_16x16x32_bf16 v[68:71], v[148:151], v[188:191], v[68:71]
	v_mfma_f32_16x16x32_bf16 v[64:67], v[152:155], v[184:187], v[64:67]
	s_nop 0
	v_mfma_f32_16x16x32_bf16 v[64:67], v[156:159], v[188:191], v[64:67]
	s_setprio 0
	s_barrier
	ds_read_b128 v[160:163], v197 offset:16384
	ds_read_b128 v[164:167], v197 offset:17408
	ds_read_b128 v[168:171], v197 offset:18432
	ds_read_b128 v[172:175], v197 offset:19456
	ds_read_b128 v[176:179], v197 offset:20480
	ds_read_b128 v[180:183], v197 offset:21504
	ds_read_b128 v[184:187], v197 offset:22528
	ds_read_b128 v[188:191], v197 offset:23552
	s_mov_b32 m0, s62
	s_add_i32 s91, s90, 0x20000
	buffer_load_dwordx4 v192, s[8:11], s90 offen lds
	s_mov_b32 m0, s63
	s_nop 0
	buffer_load_dwordx4 v192, s[8:11], s91 offen lds
	s_add_i32 s91, s90, 0x2000
	s_mov_b32 m0, s64
	s_nop 0
	buffer_load_dwordx4 v192, s[8:11], s91 offen lds
	s_add_i32 s91, s90, 0x22000
	s_mov_b32 m0, s65
	s_nop 0
	buffer_load_dwordx4 v192, s[8:11], s91 offen lds
	s_mov_b32 m0, s47
	s_add_i32 s91, s66, 0x10000
	buffer_load_dwordx4 v196, s[4:7], s66 offen lds
	s_mov_b32 m0, s68
	s_nop 0
	buffer_load_dwordx4 v196, s[4:7], s91 offen lds
	s_waitcnt vmcnt(8)
	s_waitcnt lgkmcnt(0)
	s_barrier
	s_setprio 1
	s_waitcnt lgkmcnt(7)
	v_mfma_f32_16x16x32_bf16 v[60:63], v[128:131], v[160:163], v[60:63]
	s_waitcnt lgkmcnt(6)
	v_mfma_f32_16x16x32_bf16 v[60:63], v[132:135], v[164:167], v[60:63]
	v_mfma_f32_16x16x32_bf16 v[56:59], v[136:139], v[160:163], v[56:59]
	s_nop 0
	v_mfma_f32_16x16x32_bf16 v[56:59], v[140:143], v[164:167], v[56:59]
	s_waitcnt lgkmcnt(5)
	v_mfma_f32_16x16x32_bf16 v[52:55], v[128:131], v[168:171], v[52:55]
	s_waitcnt lgkmcnt(4)
	v_mfma_f32_16x16x32_bf16 v[52:55], v[132:135], v[172:175], v[52:55]
	v_mfma_f32_16x16x32_bf16 v[48:51], v[136:139], v[168:171], v[48:51]
	s_nop 0
	v_mfma_f32_16x16x32_bf16 v[48:51], v[140:143], v[172:175], v[48:51]
	s_waitcnt lgkmcnt(3)
	v_mfma_f32_16x16x32_bf16 v[44:47], v[128:131], v[176:179], v[44:47]
	s_waitcnt lgkmcnt(2)
	v_mfma_f32_16x16x32_bf16 v[44:47], v[132:135], v[180:183], v[44:47]
	v_mfma_f32_16x16x32_bf16 v[40:43], v[136:139], v[176:179], v[40:43]
	s_nop 0
	v_mfma_f32_16x16x32_bf16 v[40:43], v[140:143], v[180:183], v[40:43]
	s_waitcnt lgkmcnt(1)
	v_mfma_f32_16x16x32_bf16 v[36:39], v[128:131], v[184:187], v[36:39]
	s_waitcnt lgkmcnt(0)
	v_mfma_f32_16x16x32_bf16 v[36:39], v[132:135], v[188:191], v[36:39]
	v_mfma_f32_16x16x32_bf16 v[32:35], v[136:139], v[184:187], v[32:35]
	s_nop 0
	v_mfma_f32_16x16x32_bf16 v[32:35], v[140:143], v[188:191], v[32:35]
	s_setprio 0
	s_setprio 1
	v_mfma_f32_16x16x32_bf16 v[28:31], v[144:147], v[160:163], v[28:31]
	s_nop 0
	v_mfma_f32_16x16x32_bf16 v[28:31], v[148:151], v[164:167], v[28:31]
	v_mfma_f32_16x16x32_bf16 v[24:27], v[152:155], v[160:163], v[24:27]
	s_nop 0
	v_mfma_f32_16x16x32_bf16 v[24:27], v[156:159], v[164:167], v[24:27]
	v_mfma_f32_16x16x32_bf16 v[20:23], v[144:147], v[168:171], v[20:23]
	s_nop 0
	v_mfma_f32_16x16x32_bf16 v[20:23], v[148:151], v[172:175], v[20:23]
	v_mfma_f32_16x16x32_bf16 v[16:19], v[152:155], v[168:171], v[16:19]
	s_nop 0
	v_mfma_f32_16x16x32_bf16 v[16:19], v[156:159], v[172:175], v[16:19]
	v_mfma_f32_16x16x32_bf16 v[12:15], v[144:147], v[176:179], v[12:15]
	s_nop 0
	v_mfma_f32_16x16x32_bf16 v[12:15], v[148:151], v[180:183], v[12:15]
	v_mfma_f32_16x16x32_bf16 v[8:11], v[152:155], v[176:179], v[8:11]
	s_nop 0
	v_mfma_f32_16x16x32_bf16 v[8:11], v[156:159], v[180:183], v[8:11]
	v_mfma_f32_16x16x32_bf16 v[4:7], v[144:147], v[184:187], v[4:7]
	s_nop 0
	v_mfma_f32_16x16x32_bf16 v[4:7], v[148:151], v[188:191], v[4:7]
	v_mfma_f32_16x16x32_bf16 v[0:3], v[152:155], v[184:187], v[0:3]
	s_nop 0
	v_mfma_f32_16x16x32_bf16 v[0:3], v[156:159], v[188:191], v[0:3]
	s_setprio 0
	s_barrier
	ds_read_b128 v[140:143], v203
	ds_read_b128 v[144:147], v204
	ds_read_b128 v[148:151], v205
	ds_read_b128 v[152:155], v206
	ds_read_b128 v[156:159], v207
	ds_read_b128 v[136:139], v208
	ds_read_b128 v[132:135], v209
	ds_read_b128 v[128:131], v210
	ds_read_b128 v[160:163], v197 offset:32768
	ds_read_b128 v[164:167], v197 offset:33792
	ds_read_b128 v[168:171], v197 offset:34816
	ds_read_b128 v[172:175], v197 offset:35840
	ds_read_b128 v[176:179], v197 offset:36864
	ds_read_b128 v[180:183], v197 offset:37888
	ds_read_b128 v[184:187], v197 offset:38912
	ds_read_b128 v[188:191], v197 offset:39936
	s_mov_b32 m0, s69
	s_add_i32 s91, s66, 0x20000
	buffer_load_dwordx4 v196, s[4:7], s91 offen lds
	s_add_i32 s91, s66, 0x30000
	s_mov_b32 m0, s70
	s_nop 0
	buffer_load_dwordx4 v196, s[4:7], s91 offen lds
	s_waitcnt vmcnt(8)
	s_waitcnt lgkmcnt(4)
	s_barrier
	s_setprio 1
	s_waitcnt lgkmcnt(7)
	v_mfma_f32_16x16x32_bf16 v[124:127], v[140:143], v[160:163], v[124:127]
	s_waitcnt lgkmcnt(6)
	v_mfma_f32_16x16x32_bf16 v[124:127], v[144:147], v[164:167], v[124:127]
	v_mfma_f32_16x16x32_bf16 v[120:123], v[148:151], v[160:163], v[120:123]
	s_nop 0
	v_mfma_f32_16x16x32_bf16 v[120:123], v[152:155], v[164:167], v[120:123]
	s_waitcnt lgkmcnt(5)
	v_mfma_f32_16x16x32_bf16 v[116:119], v[140:143], v[168:171], v[116:119]
	s_waitcnt lgkmcnt(4)
	v_mfma_f32_16x16x32_bf16 v[116:119], v[144:147], v[172:175], v[116:119]
	v_mfma_f32_16x16x32_bf16 v[112:115], v[148:151], v[168:171], v[112:115]
	s_nop 0
	v_mfma_f32_16x16x32_bf16 v[112:115], v[152:155], v[172:175], v[112:115]
	s_waitcnt lgkmcnt(3)
	v_mfma_f32_16x16x32_bf16 v[108:111], v[140:143], v[176:179], v[108:111]
	s_waitcnt lgkmcnt(2)
	v_mfma_f32_16x16x32_bf16 v[108:111], v[144:147], v[180:183], v[108:111]
	v_mfma_f32_16x16x32_bf16 v[104:107], v[148:151], v[176:179], v[104:107]
	s_nop 0
	v_mfma_f32_16x16x32_bf16 v[104:107], v[152:155], v[180:183], v[104:107]
	s_waitcnt lgkmcnt(1)
	v_mfma_f32_16x16x32_bf16 v[100:103], v[140:143], v[184:187], v[100:103]
	s_waitcnt lgkmcnt(0)
	v_mfma_f32_16x16x32_bf16 v[100:103], v[144:147], v[188:191], v[100:103]
	v_mfma_f32_16x16x32_bf16 v[96:99], v[148:151], v[184:187], v[96:99]
	s_nop 0
	v_mfma_f32_16x16x32_bf16 v[96:99], v[152:155], v[188:191], v[96:99]
	s_setprio 0
	s_setprio 1
	v_mfma_f32_16x16x32_bf16 v[92:95], v[156:159], v[160:163], v[92:95]
	s_nop 0
	v_mfma_f32_16x16x32_bf16 v[92:95], v[136:139], v[164:167], v[92:95]
	v_mfma_f32_16x16x32_bf16 v[88:91], v[132:135], v[160:163], v[88:91]
	s_nop 0
	v_mfma_f32_16x16x32_bf16 v[88:91], v[128:131], v[164:167], v[88:91]
	v_mfma_f32_16x16x32_bf16 v[84:87], v[156:159], v[168:171], v[84:87]
	s_nop 0
	v_mfma_f32_16x16x32_bf16 v[84:87], v[136:139], v[172:175], v[84:87]
	v_mfma_f32_16x16x32_bf16 v[80:83], v[132:135], v[168:171], v[80:83]
	s_nop 0
	v_mfma_f32_16x16x32_bf16 v[80:83], v[128:131], v[172:175], v[80:83]
	v_mfma_f32_16x16x32_bf16 v[76:79], v[156:159], v[176:179], v[76:79]
	s_nop 0
	v_mfma_f32_16x16x32_bf16 v[76:79], v[136:139], v[180:183], v[76:79]
	v_mfma_f32_16x16x32_bf16 v[72:75], v[132:135], v[176:179], v[72:75]
	s_nop 0
	v_mfma_f32_16x16x32_bf16 v[72:75], v[128:131], v[180:183], v[72:75]
	v_mfma_f32_16x16x32_bf16 v[68:71], v[156:159], v[184:187], v[68:71]
	s_nop 0
	v_mfma_f32_16x16x32_bf16 v[68:71], v[136:139], v[188:191], v[68:71]
	v_mfma_f32_16x16x32_bf16 v[64:67], v[132:135], v[184:187], v[64:67]
	s_nop 0
	v_mfma_f32_16x16x32_bf16 v[64:67], v[128:131], v[188:191], v[64:67]
	s_setprio 0
	s_barrier
	ds_read_b128 v[160:163], v197 offset:49152
	ds_read_b128 v[164:167], v197 offset:50176
	ds_read_b128 v[168:171], v197 offset:51200
	ds_read_b128 v[172:175], v197 offset:52224
	ds_read_b128 v[176:179], v197 offset:53248
	ds_read_b128 v[180:183], v197 offset:54272
	ds_read_b128 v[184:187], v197 offset:55296
	ds_read_b128 v[188:191], v197 offset:56320
	s_mov_b32 m0, s72
	s_add_i32 s91, s90, 0x80
	buffer_load_dwordx4 v192, s[8:11], s91 offen lds
	s_add_i32 s91, s90, 0x20080
	s_mov_b32 m0, s73
	s_add_i32 s66, s66, 0x10080
	buffer_load_dwordx4 v192, s[8:11], s91 offen lds
	s_add_i32 s91, s90, 0x2080
	s_mov_b32 m0, s76
	s_add_i32 s90, s90, 0x22080
	buffer_load_dwordx4 v192, s[8:11], s91 offen lds
	s_mov_b32 m0, s77
	s_nop 0
	buffer_load_dwordx4 v192, s[8:11], s90 offen lds
	s_mov_b32 m0, s74
	s_nop 0
	buffer_load_dwordx4 v196, s[4:7], s67 offen lds
	s_mov_b32 m0, s75
	s_nop 0
	buffer_load_dwordx4 v196, s[4:7], s66 offen lds
	s_waitcnt vmcnt(8)
	s_waitcnt lgkmcnt(0)
	s_barrier
	s_setprio 1
	s_waitcnt lgkmcnt(7)
	v_mfma_f32_16x16x32_bf16 v[60:63], v[140:143], v[160:163], v[60:63]
	s_waitcnt lgkmcnt(6)
	v_mfma_f32_16x16x32_bf16 v[60:63], v[144:147], v[164:167], v[60:63]
	v_mfma_f32_16x16x32_bf16 v[56:59], v[148:151], v[160:163], v[56:59]
	s_nop 0
	v_mfma_f32_16x16x32_bf16 v[56:59], v[152:155], v[164:167], v[56:59]
	s_waitcnt lgkmcnt(5)
	v_mfma_f32_16x16x32_bf16 v[52:55], v[140:143], v[168:171], v[52:55]
	s_waitcnt lgkmcnt(4)
	v_mfma_f32_16x16x32_bf16 v[52:55], v[144:147], v[172:175], v[52:55]
	v_mfma_f32_16x16x32_bf16 v[48:51], v[148:151], v[168:171], v[48:51]
	s_nop 0
	v_mfma_f32_16x16x32_bf16 v[48:51], v[152:155], v[172:175], v[48:51]
	s_waitcnt lgkmcnt(3)
	v_mfma_f32_16x16x32_bf16 v[44:47], v[140:143], v[176:179], v[44:47]
	s_waitcnt lgkmcnt(2)
	v_mfma_f32_16x16x32_bf16 v[44:47], v[144:147], v[180:183], v[44:47]
	v_mfma_f32_16x16x32_bf16 v[40:43], v[148:151], v[176:179], v[40:43]
	s_nop 0
	v_mfma_f32_16x16x32_bf16 v[40:43], v[152:155], v[180:183], v[40:43]
	s_waitcnt lgkmcnt(1)
	v_mfma_f32_16x16x32_bf16 v[36:39], v[140:143], v[184:187], v[36:39]
	s_waitcnt lgkmcnt(0)
	v_mfma_f32_16x16x32_bf16 v[36:39], v[144:147], v[188:191], v[36:39]
	v_mfma_f32_16x16x32_bf16 v[32:35], v[148:151], v[184:187], v[32:35]
	s_nop 0
	v_mfma_f32_16x16x32_bf16 v[32:35], v[152:155], v[188:191], v[32:35]
	s_setprio 0
	s_setprio 1
	v_mfma_f32_16x16x32_bf16 v[28:31], v[156:159], v[160:163], v[28:31]
	s_nop 0
	v_mfma_f32_16x16x32_bf16 v[28:31], v[136:139], v[164:167], v[28:31]
	v_mfma_f32_16x16x32_bf16 v[24:27], v[132:135], v[160:163], v[24:27]
	s_nop 0
	v_mfma_f32_16x16x32_bf16 v[24:27], v[128:131], v[164:167], v[24:27]
	v_mfma_f32_16x16x32_bf16 v[20:23], v[156:159], v[168:171], v[20:23]
	s_nop 0
	v_mfma_f32_16x16x32_bf16 v[20:23], v[136:139], v[172:175], v[20:23]
	v_mfma_f32_16x16x32_bf16 v[16:19], v[132:135], v[168:171], v[16:19]
	s_nop 0
	v_mfma_f32_16x16x32_bf16 v[16:19], v[128:131], v[172:175], v[16:19]
	v_mfma_f32_16x16x32_bf16 v[12:15], v[156:159], v[176:179], v[12:15]
	s_nop 0
	v_mfma_f32_16x16x32_bf16 v[12:15], v[136:139], v[180:183], v[12:15]
	v_mfma_f32_16x16x32_bf16 v[8:11], v[132:135], v[176:179], v[8:11]
	s_nop 0
	v_mfma_f32_16x16x32_bf16 v[8:11], v[128:131], v[180:183], v[8:11]
	v_mfma_f32_16x16x32_bf16 v[4:7], v[156:159], v[184:187], v[4:7]
	s_nop 0
	v_mfma_f32_16x16x32_bf16 v[4:7], v[136:139], v[188:191], v[4:7]
	v_mfma_f32_16x16x32_bf16 v[0:3], v[132:135], v[184:187], v[0:3]
	s_nop 0
	v_mfma_f32_16x16x32_bf16 v[0:3], v[128:131], v[188:191], v[0:3]
	s_setprio 0
	s_barrier
	s_add_i32 s43, s43, 2
	s_addk_i32 s33, 0x100
	s_addk_i32 s42, 0x100
	s_cmp_gt_u32 s43, 5
	s_cbranch_scc0 .LBB0_254
	s_and_b64 vcc, exec, s[14:15]
	s_cbranch_vccz .LBB0_257
	s_barrier

.LBB0_344:
	s_waitcnt lgkmcnt(0)
	s_add_i32 s4, s60, 0x180
	s_add_i32 s5, s36, 0x180
	s_barrier
	s_setprio 1
	s_waitcnt lgkmcnt(7)
	v_mfma_f32_16x16x32_bf16 v[60:63], v[164:167], v[196:199], 0
	s_waitcnt lgkmcnt(6)
	v_mfma_f32_16x16x32_bf16 v[60:63], v[160:163], v[192:195], v[60:63]
	v_mfma_f32_16x16x32_bf16 v[56:59], v[156:159], v[196:199], 0
	s_nop 0
	v_mfma_f32_16x16x32_bf16 v[56:59], v[152:155], v[192:195], v[56:59]
	s_waitcnt lgkmcnt(5)
	v_mfma_f32_16x16x32_bf16 v[52:55], v[164:167], v[188:191], 0
	s_waitcnt lgkmcnt(4)
	v_mfma_f32_16x16x32_bf16 v[52:55], v[160:163], v[184:187], v[52:55]
	v_mfma_f32_16x16x32_bf16 v[48:51], v[156:159], v[188:191], 0
	s_nop 0
	v_mfma_f32_16x16x32_bf16 v[48:51], v[152:155], v[184:187], v[48:51]
	s_waitcnt lgkmcnt(3)
	v_mfma_f32_16x16x32_bf16 v[44:47], v[164:167], v[180:183], 0
	s_waitcnt lgkmcnt(2)
	v_mfma_f32_16x16x32_bf16 v[44:47], v[160:163], v[176:179], v[44:47]
	v_mfma_f32_16x16x32_bf16 v[40:43], v[156:159], v[180:183], 0
	s_nop 0
	v_mfma_f32_16x16x32_bf16 v[40:43], v[152:155], v[176:179], v[40:43]
	s_waitcnt lgkmcnt(1)
	v_mfma_f32_16x16x32_bf16 v[36:39], v[164:167], v[172:175], 0
	s_waitcnt lgkmcnt(0)
	v_mfma_f32_16x16x32_bf16 v[36:39], v[160:163], v[168:171], v[36:39]
	v_mfma_f32_16x16x32_bf16 v[32:35], v[156:159], v[172:175], 0
	s_nop 0
	v_mfma_f32_16x16x32_bf16 v[32:35], v[152:155], v[168:171], v[32:35]
	s_setprio 0
	s_setprio 1
	v_mfma_f32_16x16x32_bf16 v[28:31], v[148:151], v[196:199], 0
	s_nop 0
	v_mfma_f32_16x16x32_bf16 v[28:31], v[144:147], v[192:195], v[28:31]
	v_mfma_f32_16x16x32_bf16 v[24:27], v[140:143], v[196:199], 0
	s_nop 0
	v_mfma_f32_16x16x32_bf16 v[24:27], v[136:139], v[192:195], v[24:27]
	v_mfma_f32_16x16x32_bf16 v[20:23], v[148:151], v[188:191], 0
	s_nop 0
	v_mfma_f32_16x16x32_bf16 v[20:23], v[144:147], v[184:187], v[20:23]
	v_mfma_f32_16x16x32_bf16 v[16:19], v[140:143], v[188:191], 0
	s_nop 0
	v_mfma_f32_16x16x32_bf16 v[16:19], v[136:139], v[184:187], v[16:19]
	v_mfma_f32_16x16x32_bf16 v[12:15], v[148:151], v[180:183], 0
	s_nop 0
	v_mfma_f32_16x16x32_bf16 v[12:15], v[144:147], v[176:179], v[12:15]
	v_mfma_f32_16x16x32_bf16 v[8:11], v[140:143], v[180:183], 0
	s_nop 0
	v_mfma_f32_16x16x32_bf16 v[8:11], v[136:139], v[176:179], v[8:11]
	v_mfma_f32_16x16x32_bf16 v[4:7], v[148:151], v[172:175], 0
	s_nop 0
	v_mfma_f32_16x16x32_bf16 v[4:7], v[144:147], v[168:171], v[4:7]
	v_mfma_f32_16x16x32_bf16 v[0:3], v[140:143], v[172:175], 0
	s_nop 0
	v_mfma_f32_16x16x32_bf16 v[0:3], v[136:139], v[168:171], v[0:3]
	s_setprio 0
	s_barrier
	ds_read_b128 v[164:167], v225
	ds_read_b128 v[160:163], v226
	ds_read_b128 v[156:159], v227
	ds_read_b128 v[152:155], v228
	ds_read_b128 v[148:151], v229
	ds_read_b128 v[144:147], v230
	ds_read_b128 v[140:143], v231
	ds_read_b128 v[136:139], v232
	ds_read_b128 v[168:171], v233 offset:32768
	ds_read_b128 v[172:175], v233 offset:33792
	ds_read_b128 v[176:179], v233 offset:34816
	ds_read_b128 v[180:183], v233 offset:35840
	ds_read_b128 v[184:187], v233 offset:36864
	ds_read_b128 v[188:191], v233 offset:37888
	ds_read_b128 v[192:195], v233 offset:38912
	ds_read_b128 v[196:199], v233 offset:39936
	s_mov_b32 m0, s72
	s_add_i32 s14, s60, 0x100100
	buffer_load_dwordx4 v214, s[8:11], s14 offen lds
	s_add_i32 s14, s60, 0x180100
	s_mov_b32 m0, s73
	s_nop 0
	buffer_load_dwordx4 v214, s[8:11], s14 offen lds
	s_waitcnt vmcnt(10)
	s_waitcnt lgkmcnt(4)
	s_barrier
	s_setprio 1
	s_waitcnt lgkmcnt(7)
	v_mfma_f32_16x16x32_bf16 v[124:127], v[164:167], v[168:171], v[124:127]
	s_waitcnt lgkmcnt(6)
	v_mfma_f32_16x16x32_bf16 v[124:127], v[160:163], v[172:175], v[124:127]
	v_mfma_f32_16x16x32_bf16 v[120:123], v[156:159], v[168:171], v[120:123]
	s_nop 0
	v_mfma_f32_16x16x32_bf16 v[120:123], v[152:155], v[172:175], v[120:123]
	s_waitcnt lgkmcnt(5)
	v_mfma_f32_16x16x32_bf16 v[116:119], v[164:167], v[176:179], v[116:119]
	s_waitcnt lgkmcnt(4)
	v_mfma_f32_16x16x32_bf16 v[116:119], v[160:163], v[180:183], v[116:119]
	v_mfma_f32_16x16x32_bf16 v[112:115], v[156:159], v[176:179], v[112:115]
	s_nop 0
	v_mfma_f32_16x16x32_bf16 v[112:115], v[152:155], v[180:183], v[112:115]
	s_waitcnt lgkmcnt(3)
	v_mfma_f32_16x16x32_bf16 v[108:111], v[164:167], v[184:187], v[108:111]
	s_waitcnt lgkmcnt(2)
	v_mfma_f32_16x16x32_bf16 v[108:111], v[160:163], v[188:191], v[108:111]
	v_mfma_f32_16x16x32_bf16 v[104:107], v[156:159], v[184:187], v[104:107]
	s_nop 0
	v_mfma_f32_16x16x32_bf16 v[104:107], v[152:155], v[188:191], v[104:107]
	s_waitcnt lgkmcnt(1)
	v_mfma_f32_16x16x32_bf16 v[100:103], v[164:167], v[192:195], v[100:103]
	s_waitcnt lgkmcnt(0)
	v_mfma_f32_16x16x32_bf16 v[100:103], v[160:163], v[196:199], v[100:103]
	v_mfma_f32_16x16x32_bf16 v[96:99], v[156:159], v[192:195], v[96:99]
	s_nop 0
	v_mfma_f32_16x16x32_bf16 v[96:99], v[152:155], v[196:199], v[96:99]
	s_setprio 0
	s_setprio 1
	v_mfma_f32_16x16x32_bf16 v[92:95], v[148:151], v[168:171], v[92:95]
	s_nop 0
	v_mfma_f32_16x16x32_bf16 v[92:95], v[144:147], v[172:175], v[92:95]
	v_mfma_f32_16x16x32_bf16 v[88:91], v[140:143], v[168:171], v[88:91]
	s_nop 0
	v_mfma_f32_16x16x32_bf16 v[88:91], v[136:139], v[172:175], v[88:91]
	v_mfma_f32_16x16x32_bf16 v[84:87], v[148:151], v[176:179], v[84:87]
	s_nop 0
	v_mfma_f32_16x16x32_bf16 v[84:87], v[144:147], v[180:183], v[84:87]
	v_mfma_f32_16x16x32_bf16 v[80:83], v[140:143], v[176:179], v[80:83]
	s_nop 0
	v_mfma_f32_16x16x32_bf16 v[80:83], v[136:139], v[180:183], v[80:83]
	v_mfma_f32_16x16x32_bf16 v[76:79], v[148:151], v[184:187], v[76:79]
	s_nop 0
	v_mfma_f32_16x16x32_bf16 v[76:79], v[144:147], v[188:191], v[76:79]
	v_mfma_f32_16x16x32_bf16 v[72:75], v[140:143], v[184:187], v[72:75]
	s_nop 0
	v_mfma_f32_16x16x32_bf16 v[72:75], v[136:139], v[188:191], v[72:75]
	v_mfma_f32_16x16x32_bf16 v[68:71], v[148:151], v[192:195], v[68:71]
	s_nop 0
	v_mfma_f32_16x16x32_bf16 v[68:71], v[144:147], v[196:199], v[68:71]
	v_mfma_f32_16x16x32_bf16 v[64:67], v[140:143], v[192:195], v[64:67]
	s_nop 0
	v_mfma_f32_16x16x32_bf16 v[64:67], v[136:139], v[196:199], v[64:67]
	s_setprio 0
	s_barrier
	ds_read_b128 v[168:171], v233 offset:49152
	ds_read_b128 v[172:175], v233 offset:50176
	ds_read_b128 v[176:179], v233 offset:51200
	ds_read_b128 v[180:183], v233 offset:52224
	ds_read_b128 v[184:187], v233 offset:53248
	ds_read_b128 v[188:191], v233 offset:54272
	ds_read_b128 v[192:195], v233 offset:55296
	ds_read_b128 v[196:199], v233 offset:56320
	s_mov_b32 m0, s76
	s_mov_b32 s14, s10
	s_mov_b32 s15, s11
	buffer_load_dwordx4 v215, s[12:15], s5 offen lds
	s_add_i32 s5, s36, 0x100180
	s_mov_b32 m0, s77
	s_nop 0
	buffer_load_dwordx4 v215, s[12:15], s5 offen lds
	s_add_i32 s5, s36, 0x10180
	s_mov_b32 m0, s80
	s_nop 0
	buffer_load_dwordx4 v215, s[12:15], s5 offen lds
	s_add_i32 s5, s36, 0x110180
	s_mov_b32 m0, s81
	s_nop 0
	buffer_load_dwordx4 v215, s[12:15], s5 offen lds
	s_mov_b32 m0, s78
	s_nop 0
	buffer_load_dwordx4 v214, s[8:11], s4 offen lds
	s_add_i32 s4, s60, 0x80180
	s_mov_b32 m0, s79
	s_nop 0
	buffer_load_dwordx4 v214, s[8:11], s4 offen lds
	s_waitcnt vmcnt(8)
	s_waitcnt lgkmcnt(0)
	s_barrier
	s_setprio 1
	s_waitcnt lgkmcnt(7)
	v_mfma_f32_16x16x32_bf16 v[60:63], v[164:167], v[168:171], v[60:63]
	s_waitcnt lgkmcnt(6)
	v_mfma_f32_16x16x32_bf16 v[60:63], v[160:163], v[172:175], v[60:63]
	v_mfma_f32_16x16x32_bf16 v[56:59], v[156:159], v[168:171], v[56:59]
	s_nop 0
	v_mfma_f32_16x16x32_bf16 v[56:59], v[152:155], v[172:175], v[56:59]
	s_waitcnt lgkmcnt(5)
	v_mfma_f32_16x16x32_bf16 v[52:55], v[164:167], v[176:179], v[52:55]
	s_waitcnt lgkmcnt(4)
	v_mfma_f32_16x16x32_bf16 v[52:55], v[160:163], v[180:183], v[52:55]
	v_mfma_f32_16x16x32_bf16 v[48:51], v[156:159], v[176:179], v[48:51]
	s_nop 0
	v_mfma_f32_16x16x32_bf16 v[48:51], v[152:155], v[180:183], v[48:51]
	s_waitcnt lgkmcnt(3)
	v_mfma_f32_16x16x32_bf16 v[44:47], v[164:167], v[184:187], v[44:47]
	s_waitcnt lgkmcnt(2)
	v_mfma_f32_16x16x32_bf16 v[44:47], v[160:163], v[188:191], v[44:47]
	v_mfma_f32_16x16x32_bf16 v[40:43], v[156:159], v[184:187], v[40:43]
	s_nop 0
	v_mfma_f32_16x16x32_bf16 v[40:43], v[152:155], v[188:191], v[40:43]
	s_waitcnt lgkmcnt(1)
	v_mfma_f32_16x16x32_bf16 v[36:39], v[164:167], v[192:195], v[36:39]
	s_waitcnt lgkmcnt(0)
	v_mfma_f32_16x16x32_bf16 v[36:39], v[160:163], v[196:199], v[36:39]
	v_mfma_f32_16x16x32_bf16 v[32:35], v[156:159], v[192:195], v[32:35]
	s_nop 0
	v_mfma_f32_16x16x32_bf16 v[32:35], v[152:155], v[196:199], v[32:35]
	s_setprio 0
	s_setprio 1
	v_mfma_f32_16x16x32_bf16 v[28:31], v[148:151], v[168:171], v[28:31]
	s_nop 0
	v_mfma_f32_16x16x32_bf16 v[28:31], v[144:147], v[172:175], v[28:31]
	v_mfma_f32_16x16x32_bf16 v[24:27], v[140:143], v[168:171], v[24:27]
	s_nop 0
	v_mfma_f32_16x16x32_bf16 v[24:27], v[136:139], v[172:175], v[24:27]
	v_mfma_f32_16x16x32_bf16 v[20:23], v[148:151], v[176:179], v[20:23]
	s_nop 0
	v_mfma_f32_16x16x32_bf16 v[20:23], v[144:147], v[180:183], v[20:23]
	v_mfma_f32_16x16x32_bf16 v[16:19], v[140:143], v[176:179], v[16:19]
	s_nop 0
	v_mfma_f32_16x16x32_bf16 v[16:19], v[136:139], v[180:183], v[16:19]
	v_mfma_f32_16x16x32_bf16 v[12:15], v[148:151], v[184:187], v[12:15]
	s_nop 0
	v_mfma_f32_16x16x32_bf16 v[12:15], v[144:147], v[188:191], v[12:15]
	v_mfma_f32_16x16x32_bf16 v[8:11], v[140:143], v[184:187], v[8:11]
	s_nop 0
	v_mfma_f32_16x16x32_bf16 v[8:11], v[136:139], v[188:191], v[8:11]
	v_mfma_f32_16x16x32_bf16 v[4:7], v[148:151], v[192:195], v[4:7]
	s_nop 0
	v_mfma_f32_16x16x32_bf16 v[4:7], v[144:147], v[196:199], v[4:7]
	v_mfma_f32_16x16x32_bf16 v[0:3], v[140:143], v[192:195], v[0:3]
	s_nop 0
	v_mfma_f32_16x16x32_bf16 v[0:3], v[136:139], v[196:199], v[0:3]
	s_setprio 0
	s_barrier
	s_waitcnt vmcnt(14)
	v_mul_f32_e32 v132, 0x42800000, v132
	v_mul_f32_e32 v128, 0x42800000, v128
	v_mul_f32_e32 v133, 0x42800000, v133
	v_mul_f32_e32 v129, 0x42800000, v129
	v_mul_f32_e32 v134, 0x42800000, v134
	v_mul_f32_e32 v130, 0x42800000, v130
	v_mul_f32_e32 v135, 0x42800000, v135
	v_mul_f32_e32 v131, 0x42800000, v131
	v_cvt_pk_fp8_f32 v204, v128, v132
	v_cvt_pk_fp8_f32 v234, v129, v133
	v_cvt_pk_fp8_f32 v235, v130, v134
	v_cvt_pk_fp8_f32 v236, v131, v135
	s_add_i32 s33, s36, 0x200
	s_mov_b32 s61, 0
	s_mov_b32 s66, s75
	s_mov_b32 s94, s86
	s_branch .LBB0_347

.LBB0_347:
	v_mov_b32_e32 v152, v204
	v_mov_b32_e32 v153, v234
	v_mov_b32_e32 v154, v235
	v_mov_b32_e32 v155, v236
	ds_read_b128 v[158:161], v217
	ds_read_b128 v[162:165], v218
	ds_read_b128 v[166:169], v219
	ds_read_b128 v[170:173], v220
	ds_read_b128 v[148:151], v221
	ds_read_b128 v[144:147], v222
	ds_read_b128 v[140:143], v223
	ds_read_b128 v[136:139], v224
	ds_read_b128 v[174:177], v233
	ds_read_b128 v[178:181], v233 offset:1024
	ds_read_b128 v[182:185], v233 offset:2048
	ds_read_b128 v[186:189], v233 offset:3072
	ds_read_b128 v[190:193], v233 offset:4096
	ds_read_b128 v[194:197], v233 offset:5120
	ds_read_b128 v[234:237], v233 offset:6144
	ds_read_b128 v[238:241], v233 offset:7168
	s_add_i32 s4, s60, s61
	s_mov_b32 s46, s94
	s_add_i32 s94, s94, 1
	s_add_i32 s5, s4, 0x200
	s_add_i32 s16, s33, s61
	s_cmpk_eq_i32 s61, 0x1e00
	s_cselect_b32 s47, s90, s5
	s_cselect_b32 s97, s91, s16
	s_add_i32 s96, s47, 0x80
	s_mov_b32 m0, s82
	s_add_i32 s5, s4, 0x100180
	buffer_load_dwordx4 v214, s[8:11], s5 offen lds
	s_add_i32 s4, s4, 0x180180
	s_mov_b32 m0, s85
	s_add_i32 vcc_lo, s97, 0x80
	buffer_load_dwordx4 v214, s[8:11], s4 offen lds
	s_lshr_b32 s4, s94, 2
	s_mul_i32 s5, s4, s34
	s_add_i32 s16, s5, s2
	s_cmp_lt_i32 s4, s3
	s_cselect_b64 s[4:5], -1, 0
	s_and_b64 s[44:45], s[4:5], exec
	s_cselect_b32 s16, s16, 0
	s_bfe_u32 s17, s94, 0x10001
	s_or_b32 s17, s17, s83
	s_bfe_u32 s67, s16, 0x50007
	s_bfe_u32 s36, s16, 0x50002
	s_and_b32 s95, s16, 3
	s_cmpk_gt_i32 s16, 0xfff
	s_cselect_b64 s[44:45], -1, 0
	v_lshl_or_b32 v156, s17, 3, v216
	s_and_b64 s[16:17], s[44:45], exec
	s_cselect_b32 s16, s25, s21
	s_cselect_b32 s17, s24, s20
	s_lshl_b32 vcc_hi, s67, 23
	s_add_u32 s17, s17, vcc_hi
	s_addc_u32 s16, s16, 0
	s_lshl_b32 vcc_hi, s36, 18
	s_add_u32 s17, s17, vcc_hi
	s_addc_u32 vcc_hi, s16, 0
	s_lshl_b32 s16, s95, 9
	s_add_u32 s16, s17, s16
	v_and_or_b32 v204, s66, 2, v200
	s_addc_u32 s17, vcc_hi, 0
	v_lshlrev_b64 v[128:129], 11, v[204:205]
	v_lshl_add_u64 v[128:129], s[16:17], 0, v[128:129]
	v_lshlrev_b32_e32 v204, 4, v156
	v_lshl_add_u64 v[132:133], v[128:129], 0, v[204:205]
	global_load_dwordx4 v[128:131], v[132:133], off nt
	s_nop 0
	global_load_dwordx4 v[132:135], v[132:133], off offset:2048 nt
	s_waitcnt vmcnt(10)
	s_waitcnt lgkmcnt(4)
	s_barrier
	s_setprio 1
	s_waitcnt lgkmcnt(7)
	v_mfma_f32_16x16x32_bf16 v[124:127], v[158:161], v[174:177], v[124:127]
	s_waitcnt lgkmcnt(6)
	v_mfma_f32_16x16x32_bf16 v[124:127], v[162:165], v[178:181], v[124:127]
	v_mfma_f32_16x16x32_bf16 v[120:123], v[166:169], v[174:177], v[120:123]
	s_nop 0
	v_mfma_f32_16x16x32_bf16 v[120:123], v[170:173], v[178:181], v[120:123]
	s_waitcnt lgkmcnt(5)
	v_mfma_f32_16x16x32_bf16 v[116:119], v[158:161], v[182:185], v[116:119]
	s_waitcnt lgkmcnt(4)
	v_mfma_f32_16x16x32_bf16 v[116:119], v[162:165], v[186:189], v[116:119]
	v_mfma_f32_16x16x32_bf16 v[112:115], v[166:169], v[182:185], v[112:115]
	s_nop 0
	v_mfma_f32_16x16x32_bf16 v[112:115], v[170:173], v[186:189], v[112:115]
	s_waitcnt lgkmcnt(3)
	v_mfma_f32_16x16x32_bf16 v[108:111], v[158:161], v[190:193], v[108:111]
	s_waitcnt lgkmcnt(2)
	v_mfma_f32_16x16x32_bf16 v[108:111], v[162:165], v[194:197], v[108:111]
	v_mfma_f32_16x16x32_bf16 v[104:107], v[166:169], v[190:193], v[104:107]
	s_nop 0
	v_mfma_f32_16x16x32_bf16 v[104:107], v[170:173], v[194:197], v[104:107]
	s_waitcnt lgkmcnt(1)
	v_mfma_f32_16x16x32_bf16 v[100:103], v[158:161], v[234:237], v[100:103]
	s_waitcnt lgkmcnt(0)
	v_mfma_f32_16x16x32_bf16 v[100:103], v[162:165], v[238:241], v[100:103]
	v_mfma_f32_16x16x32_bf16 v[96:99], v[166:169], v[234:237], v[96:99]
	s_nop 0
	v_mfma_f32_16x16x32_bf16 v[96:99], v[170:173], v[238:241], v[96:99]
	s_setprio 0
	s_setprio 1
	v_mfma_f32_16x16x32_bf16 v[92:95], v[148:151], v[174:177], v[92:95]
	s_nop 0
	v_mfma_f32_16x16x32_bf16 v[92:95], v[144:147], v[178:181], v[92:95]
	v_mfma_f32_16x16x32_bf16 v[88:91], v[140:143], v[174:177], v[88:91]
	s_nop 0
	v_mfma_f32_16x16x32_bf16 v[88:91], v[136:139], v[178:181], v[88:91]
	v_mfma_f32_16x16x32_bf16 v[84:87], v[148:151], v[182:185], v[84:87]
	s_nop 0
	v_mfma_f32_16x16x32_bf16 v[84:87], v[144:147], v[186:189], v[84:87]
	v_mfma_f32_16x16x32_bf16 v[80:83], v[140:143], v[182:185], v[80:83]
	s_nop 0
	v_mfma_f32_16x16x32_bf16 v[80:83], v[136:139], v[186:189], v[80:83]
	v_mfma_f32_16x16x32_bf16 v[76:79], v[148:151], v[190:193], v[76:79]
	s_nop 0
	v_mfma_f32_16x16x32_bf16 v[76:79], v[144:147], v[194:197], v[76:79]
	v_mfma_f32_16x16x32_bf16 v[72:75], v[140:143], v[190:193], v[72:75]
	s_nop 0
	v_mfma_f32_16x16x32_bf16 v[72:75], v[136:139], v[194:197], v[72:75]
	v_mfma_f32_16x16x32_bf16 v[68:71], v[148:151], v[234:237], v[68:71]
	s_nop 0
	v_mfma_f32_16x16x32_bf16 v[68:71], v[144:147], v[238:241], v[68:71]
	v_mfma_f32_16x16x32_bf16 v[64:67], v[140:143], v[234:237], v[64:67]
	s_nop 0
	v_mfma_f32_16x16x32_bf16 v[64:67], v[136:139], v[238:241], v[64:67]
	s_setprio 0
	s_barrier
	ds_read_b128 v[174:177], v233 offset:16384
	ds_read_b128 v[178:181], v233 offset:17408
	ds_read_b128 v[182:185], v233 offset:18432
	ds_read_b128 v[186:189], v233 offset:19456
	ds_read_b128 v[190:193], v233 offset:20480
	ds_read_b128 v[194:197], v233 offset:21504
	ds_read_b128 v[234:237], v233 offset:22528
	ds_read_b128 v[238:241], v233 offset:23552
	s_mov_b32 m0, s65
	s_add_i32 s16, s97, 0x100000
	buffer_load_dwordx4 v215, s[12:15], s97 offen lds
	s_mov_b32 m0, s68
	s_nop 0
	buffer_load_dwordx4 v215, s[12:15], s16 offen lds
	s_add_i32 s16, s97, 0x10000
	s_mov_b32 m0, s69
	s_nop 0
	buffer_load_dwordx4 v215, s[12:15], s16 offen lds
	s_add_i32 s16, s97, 0x110000
	s_mov_b32 m0, s70
	s_nop 0
	buffer_load_dwordx4 v215, s[12:15], s16 offen lds
	s_mov_b32 m0, s64
	s_add_i32 s16, s47, 0x80000
	buffer_load_dwordx4 v214, s[8:11], s47 offen lds
	s_mov_b32 m0, s71
	s_nop 0
	buffer_load_dwordx4 v214, s[8:11], s16 offen lds
	s_waitcnt vmcnt(10)
	s_waitcnt lgkmcnt(0)
	s_barrier
	s_setprio 1
	s_waitcnt lgkmcnt(7)
	v_mfma_f32_16x16x32_bf16 v[60:63], v[158:161], v[174:177], v[60:63]
	s_waitcnt lgkmcnt(6)
	v_mfma_f32_16x16x32_bf16 v[60:63], v[162:165], v[178:181], v[60:63]
	v_mfma_f32_16x16x32_bf16 v[56:59], v[166:169], v[174:177], v[56:59]
	s_nop 0
	v_mfma_f32_16x16x32_bf16 v[56:59], v[170:173], v[178:181], v[56:59]
	s_waitcnt lgkmcnt(5)
	v_mfma_f32_16x16x32_bf16 v[52:55], v[158:161], v[182:185], v[52:55]
	s_waitcnt lgkmcnt(4)
	v_mfma_f32_16x16x32_bf16 v[52:55], v[162:165], v[186:189], v[52:55]
	v_mfma_f32_16x16x32_bf16 v[48:51], v[166:169], v[182:185], v[48:51]
	s_nop 0
	v_mfma_f32_16x16x32_bf16 v[48:51], v[170:173], v[186:189], v[48:51]
	s_waitcnt lgkmcnt(3)
	v_mfma_f32_16x16x32_bf16 v[44:47], v[158:161], v[190:193], v[44:47]
	s_waitcnt lgkmcnt(2)
	v_mfma_f32_16x16x32_bf16 v[44:47], v[162:165], v[194:197], v[44:47]
	v_mfma_f32_16x16x32_bf16 v[40:43], v[166:169], v[190:193], v[40:43]
	s_nop 0
	v_mfma_f32_16x16x32_bf16 v[40:43], v[170:173], v[194:197], v[40:43]
	s_waitcnt lgkmcnt(1)
	v_mfma_f32_16x16x32_bf16 v[36:39], v[158:161], v[234:237], v[36:39]
	s_waitcnt lgkmcnt(0)
	v_mfma_f32_16x16x32_bf16 v[36:39], v[162:165], v[238:241], v[36:39]
	v_mfma_f32_16x16x32_bf16 v[32:35], v[166:169], v[234:237], v[32:35]
	s_nop 0
	v_mfma_f32_16x16x32_bf16 v[32:35], v[170:173], v[238:241], v[32:35]
	s_setprio 0
	s_setprio 1
	v_mfma_f32_16x16x32_bf16 v[28:31], v[148:151], v[174:177], v[28:31]
	s_nop 0
	v_mfma_f32_16x16x32_bf16 v[28:31], v[144:147], v[178:181], v[28:31]
	v_mfma_f32_16x16x32_bf16 v[24:27], v[140:143], v[174:177], v[24:27]
	s_nop 0
	v_mfma_f32_16x16x32_bf16 v[24:27], v[136:139], v[178:181], v[24:27]
	v_mfma_f32_16x16x32_bf16 v[20:23], v[148:151], v[182:185], v[20:23]
	s_nop 0
	v_mfma_f32_16x16x32_bf16 v[20:23], v[144:147], v[186:189], v[20:23]
	v_mfma_f32_16x16x32_bf16 v[16:19], v[140:143], v[182:185], v[16:19]
	s_nop 0
	v_mfma_f32_16x16x32_bf16 v[16:19], v[136:139], v[186:189], v[16:19]
	v_mfma_f32_16x16x32_bf16 v[12:15], v[148:151], v[190:193], v[12:15]
	s_nop 0
	v_mfma_f32_16x16x32_bf16 v[12:15], v[144:147], v[194:197], v[12:15]
	v_mfma_f32_16x16x32_bf16 v[8:11], v[140:143], v[190:193], v[8:11]
	s_nop 0
	v_mfma_f32_16x16x32_bf16 v[8:11], v[136:139], v[194:197], v[8:11]
	v_mfma_f32_16x16x32_bf16 v[4:7], v[148:151], v[234:237], v[4:7]
	s_nop 0
	v_mfma_f32_16x16x32_bf16 v[4:7], v[144:147], v[238:241], v[4:7]
	v_mfma_f32_16x16x32_bf16 v[0:3], v[140:143], v[234:237], v[0:3]
	s_nop 0
	v_mfma_f32_16x16x32_bf16 v[0:3], v[136:139], v[238:241], v[0:3]
	s_setprio 0
	s_barrier
	ds_read_b128 v[136:139], v225
	ds_read_b128 v[140:143], v226
	ds_read_b128 v[144:147], v227
	ds_read_b128 v[148:151], v228
	ds_read_b128 v[158:161], v229
	ds_read_b128 v[162:165], v230
	ds_read_b128 v[166:169], v231
	ds_read_b128 v[170:173], v232
	ds_read_b128 v[174:177], v233 offset:32768
	ds_read_b128 v[178:181], v233 offset:33792
	ds_read_b128 v[182:185], v233 offset:34816
	ds_read_b128 v[186:189], v233 offset:35840
	ds_read_b128 v[190:193], v233 offset:36864
	ds_read_b128 v[194:197], v233 offset:37888
	ds_read_b128 v[234:237], v233 offset:38912
	ds_read_b128 v[238:241], v233 offset:39936
	s_mov_b32 m0, s72
	s_add_i32 s16, s47, 0x100000
	buffer_load_dwordx4 v214, s[8:11], s16 offen lds
	s_add_i32 s16, s47, 0x180000
	s_mov_b32 m0, s73
	s_nop 0
	buffer_load_dwordx4 v214, s[8:11], s16 offen lds
	s_waitcnt vmcnt(10)
	s_waitcnt lgkmcnt(4)
	s_barrier
	s_setprio 1
	s_waitcnt lgkmcnt(7)
	v_mfma_f32_16x16x32_bf16 v[124:127], v[136:139], v[174:177], v[124:127]
	s_waitcnt lgkmcnt(6)
	v_mfma_f32_16x16x32_bf16 v[124:127], v[140:143], v[178:181], v[124:127]
	v_mfma_f32_16x16x32_bf16 v[120:123], v[144:147], v[174:177], v[120:123]
	s_nop 0
	v_mfma_f32_16x16x32_bf16 v[120:123], v[148:151], v[178:181], v[120:123]
	s_waitcnt lgkmcnt(5)
	v_mfma_f32_16x16x32_bf16 v[116:119], v[136:139], v[182:185], v[116:119]
	s_waitcnt lgkmcnt(4)
	v_mfma_f32_16x16x32_bf16 v[116:119], v[140:143], v[186:189], v[116:119]
	v_mfma_f32_16x16x32_bf16 v[112:115], v[144:147], v[182:185], v[112:115]
	s_nop 0
	v_mfma_f32_16x16x32_bf16 v[112:115], v[148:151], v[186:189], v[112:115]
	s_waitcnt lgkmcnt(3)
	v_mfma_f32_16x16x32_bf16 v[108:111], v[136:139], v[190:193], v[108:111]
	s_waitcnt lgkmcnt(2)
	v_mfma_f32_16x16x32_bf16 v[108:111], v[140:143], v[194:197], v[108:111]
	v_mfma_f32_16x16x32_bf16 v[104:107], v[144:147], v[190:193], v[104:107]
	s_nop 0
	v_mfma_f32_16x16x32_bf16 v[104:107], v[148:151], v[194:197], v[104:107]
	s_waitcnt lgkmcnt(1)
	v_mfma_f32_16x16x32_bf16 v[100:103], v[136:139], v[234:237], v[100:103]
	s_waitcnt lgkmcnt(0)
	v_mfma_f32_16x16x32_bf16 v[100:103], v[140:143], v[238:241], v[100:103]
	v_mfma_f32_16x16x32_bf16 v[96:99], v[144:147], v[234:237], v[96:99]
	s_nop 0
	v_mfma_f32_16x16x32_bf16 v[96:99], v[148:151], v[238:241], v[96:99]
	s_setprio 0
	s_setprio 1
	v_mfma_f32_16x16x32_bf16 v[92:95], v[158:161], v[174:177], v[92:95]
	s_nop 0
	v_mfma_f32_16x16x32_bf16 v[92:95], v[162:165], v[178:181], v[92:95]
	v_mfma_f32_16x16x32_bf16 v[88:91], v[166:169], v[174:177], v[88:91]
	s_nop 0
	v_mfma_f32_16x16x32_bf16 v[88:91], v[170:173], v[178:181], v[88:91]
	v_mfma_f32_16x16x32_bf16 v[84:87], v[158:161], v[182:185], v[84:87]
	s_nop 0
	v_mfma_f32_16x16x32_bf16 v[84:87], v[162:165], v[186:189], v[84:87]
	v_mfma_f32_16x16x32_bf16 v[80:83], v[166:169], v[182:185], v[80:83]
	s_nop 0
	v_mfma_f32_16x16x32_bf16 v[80:83], v[170:173], v[186:189], v[80:83]
	v_mfma_f32_16x16x32_bf16 v[76:79], v[158:161], v[190:193], v[76:79]
	s_nop 0
	v_mfma_f32_16x16x32_bf16 v[76:79], v[162:165], v[194:197], v[76:79]
	v_mfma_f32_16x16x32_bf16 v[72:75], v[166:169], v[190:193], v[72:75]
	s_nop 0
	v_mfma_f32_16x16x32_bf16 v[72:75], v[170:173], v[194:197], v[72:75]
	v_mfma_f32_16x16x32_bf16 v[68:71], v[158:161], v[234:237], v[68:71]
	s_nop 0
	v_mfma_f32_16x16x32_bf16 v[68:71], v[162:165], v[238:241], v[68:71]
	v_mfma_f32_16x16x32_bf16 v[64:67], v[166:169], v[234:237], v[64:67]
	s_nop 0
	v_mfma_f32_16x16x32_bf16 v[64:67], v[170:173], v[238:241], v[64:67]
	s_setprio 0
	s_barrier
	ds_read_b128 v[174:177], v233 offset:49152
	ds_read_b128 v[178:181], v233 offset:50176
	ds_read_b128 v[182:185], v233 offset:51200
	ds_read_b128 v[186:189], v233 offset:52224
	ds_read_b128 v[190:193], v233 offset:53248
	ds_read_b128 v[194:197], v233 offset:54272
	ds_read_b128 v[234:237], v233 offset:55296
	ds_read_b128 v[238:241], v233 offset:56320
	s_mov_b32 m0, s76
	s_add_i32 s16, s97, 0x100080
	buffer_load_dwordx4 v215, s[12:15], vcc_lo offen lds
	s_mov_b32 m0, s77
	s_add_i32 s47, s47, 0x80080
	buffer_load_dwordx4 v215, s[12:15], s16 offen lds
	s_add_i32 s16, s97, 0x10080
	s_mov_b32 m0, s80
	s_add_i32 s97, s97, 0x110080
	buffer_load_dwordx4 v215, s[12:15], s16 offen lds
	s_mov_b32 m0, s81
	s_nop 0
	buffer_load_dwordx4 v215, s[12:15], s97 offen lds
	s_mov_b32 m0, s78
	s_nop 0
	buffer_load_dwordx4 v214, s[8:11], s96 offen lds
	s_mov_b32 m0, s79
	s_nop 0
	buffer_load_dwordx4 v214, s[8:11], s47 offen lds
	s_waitcnt vmcnt(8)
	s_waitcnt lgkmcnt(0)
	s_barrier
	s_setprio 1
	s_waitcnt lgkmcnt(7)
	v_mfma_f32_16x16x32_bf16 v[60:63], v[136:139], v[174:177], v[60:63]
	s_waitcnt lgkmcnt(6)
	v_mfma_f32_16x16x32_bf16 v[60:63], v[140:143], v[178:181], v[60:63]
	v_mfma_f32_16x16x32_bf16 v[56:59], v[144:147], v[174:177], v[56:59]
	s_nop 0
	v_mfma_f32_16x16x32_bf16 v[56:59], v[148:151], v[178:181], v[56:59]
	s_waitcnt lgkmcnt(5)
	v_mfma_f32_16x16x32_bf16 v[52:55], v[136:139], v[182:185], v[52:55]
	s_waitcnt lgkmcnt(4)
	v_mfma_f32_16x16x32_bf16 v[52:55], v[140:143], v[186:189], v[52:55]
	v_mfma_f32_16x16x32_bf16 v[48:51], v[144:147], v[182:185], v[48:51]
	s_nop 0
	v_mfma_f32_16x16x32_bf16 v[48:51], v[148:151], v[186:189], v[48:51]
	s_waitcnt lgkmcnt(3)
	v_mfma_f32_16x16x32_bf16 v[44:47], v[136:139], v[190:193], v[44:47]
	s_waitcnt lgkmcnt(2)
	v_mfma_f32_16x16x32_bf16 v[44:47], v[140:143], v[194:197], v[44:47]
	v_mfma_f32_16x16x32_bf16 v[40:43], v[144:147], v[190:193], v[40:43]
	s_nop 0
	v_mfma_f32_16x16x32_bf16 v[40:43], v[148:151], v[194:197], v[40:43]
	s_waitcnt lgkmcnt(1)
	v_mfma_f32_16x16x32_bf16 v[36:39], v[136:139], v[234:237], v[36:39]
	s_waitcnt lgkmcnt(0)
	v_mfma_f32_16x16x32_bf16 v[36:39], v[140:143], v[238:241], v[36:39]
	v_mfma_f32_16x16x32_bf16 v[32:35], v[144:147], v[234:237], v[32:35]
	s_nop 0
	v_mfma_f32_16x16x32_bf16 v[32:35], v[148:151], v[238:241], v[32:35]
	s_setprio 0
	s_setprio 1
	v_mfma_f32_16x16x32_bf16 v[28:31], v[158:161], v[174:177], v[28:31]
	s_nop 0
	v_mfma_f32_16x16x32_bf16 v[28:31], v[162:165], v[178:181], v[28:31]
	v_mfma_f32_16x16x32_bf16 v[24:27], v[166:169], v[174:177], v[24:27]
	s_nop 0
	v_mfma_f32_16x16x32_bf16 v[24:27], v[170:173], v[178:181], v[24:27]
	v_mfma_f32_16x16x32_bf16 v[20:23], v[158:161], v[182:185], v[20:23]
	s_nop 0
	v_mfma_f32_16x16x32_bf16 v[20:23], v[162:165], v[186:189], v[20:23]
	v_mfma_f32_16x16x32_bf16 v[16:19], v[166:169], v[182:185], v[16:19]
	s_nop 0
	v_mfma_f32_16x16x32_bf16 v[16:19], v[170:173], v[186:189], v[16:19]
	v_mfma_f32_16x16x32_bf16 v[12:15], v[158:161], v[190:193], v[12:15]
	s_nop 0
	v_mfma_f32_16x16x32_bf16 v[12:15], v[162:165], v[194:197], v[12:15]
	v_mfma_f32_16x16x32_bf16 v[8:11], v[166:169], v[190:193], v[8:11]
	s_nop 0
	v_mfma_f32_16x16x32_bf16 v[8:11], v[170:173], v[194:197], v[8:11]
	v_mfma_f32_16x16x32_bf16 v[4:7], v[158:161], v[234:237], v[4:7]
	s_nop 0
	v_mfma_f32_16x16x32_bf16 v[4:7], v[162:165], v[238:241], v[4:7]
	v_mfma_f32_16x16x32_bf16 v[0:3], v[166:169], v[234:237], v[0:3]
	s_nop 0
	v_mfma_f32_16x16x32_bf16 v[0:3], v[170:173], v[238:241], v[0:3]
	s_setprio 0
	s_barrier
	s_bitcmp0_b32 s46, 0
	s_waitcnt vmcnt(15)
	v_mul_f32_e32 v128, 0x42800000, v128
	s_waitcnt vmcnt(14)
	v_mul_f32_e32 v132, 0x42800000, v132
	v_mul_f32_e32 v129, 0x42800000, v129
	v_mul_f32_e32 v133, 0x42800000, v133
	v_mul_f32_e32 v130, 0x42800000, v130
	v_mul_f32_e32 v134, 0x42800000, v134
	v_mul_f32_e32 v131, 0x42800000, v131
	v_mul_f32_e32 v135, 0x42800000, v135
	s_mov_b64 s[46:47], -1
	s_cbranch_scc0 .LBB0_350
	s_andn2_b64 vcc, exec, s[46:47]
	s_cbranch_vccnz .LBB0_346
	s_branch .LBB0_351

.LBB0_592:
	s_waitcnt lgkmcnt(0)
	s_add_i32 s4, s60, 0x180
	s_add_i32 s5, s42, 0x180
	s_barrier
	s_setprio 1
	s_waitcnt lgkmcnt(7)
	v_mfma_f32_16x16x32_bf16 v[60:63], v[164:167], v[196:199], 0
	s_waitcnt lgkmcnt(6)
	v_mfma_f32_16x16x32_bf16 v[60:63], v[160:163], v[192:195], v[60:63]
	v_mfma_f32_16x16x32_bf16 v[56:59], v[156:159], v[196:199], 0
	s_nop 0
	v_mfma_f32_16x16x32_bf16 v[56:59], v[152:155], v[192:195], v[56:59]
	s_waitcnt lgkmcnt(5)
	v_mfma_f32_16x16x32_bf16 v[52:55], v[164:167], v[188:191], 0
	s_waitcnt lgkmcnt(4)
	v_mfma_f32_16x16x32_bf16 v[52:55], v[160:163], v[184:187], v[52:55]
	v_mfma_f32_16x16x32_bf16 v[48:51], v[156:159], v[188:191], 0
	s_nop 0
	v_mfma_f32_16x16x32_bf16 v[48:51], v[152:155], v[184:187], v[48:51]
	s_waitcnt lgkmcnt(3)
	v_mfma_f32_16x16x32_bf16 v[44:47], v[164:167], v[180:183], 0
	s_waitcnt lgkmcnt(2)
	v_mfma_f32_16x16x32_bf16 v[44:47], v[160:163], v[176:179], v[44:47]
	v_mfma_f32_16x16x32_bf16 v[40:43], v[156:159], v[180:183], 0
	s_nop 0
	v_mfma_f32_16x16x32_bf16 v[40:43], v[152:155], v[176:179], v[40:43]
	s_waitcnt lgkmcnt(1)
	v_mfma_f32_16x16x32_bf16 v[36:39], v[164:167], v[172:175], 0
	s_waitcnt lgkmcnt(0)
	v_mfma_f32_16x16x32_bf16 v[36:39], v[160:163], v[168:171], v[36:39]
	v_mfma_f32_16x16x32_bf16 v[32:35], v[156:159], v[172:175], 0
	s_nop 0
	v_mfma_f32_16x16x32_bf16 v[32:35], v[152:155], v[168:171], v[32:35]
	s_setprio 0
	s_setprio 1
	v_mfma_f32_16x16x32_bf16 v[28:31], v[148:151], v[196:199], 0
	s_nop 0
	v_mfma_f32_16x16x32_bf16 v[28:31], v[144:147], v[192:195], v[28:31]
	v_mfma_f32_16x16x32_bf16 v[24:27], v[140:143], v[196:199], 0
	s_nop 0
	v_mfma_f32_16x16x32_bf16 v[24:27], v[136:139], v[192:195], v[24:27]
	v_mfma_f32_16x16x32_bf16 v[20:23], v[148:151], v[188:191], 0
	s_nop 0
	v_mfma_f32_16x16x32_bf16 v[20:23], v[144:147], v[184:187], v[20:23]
	v_mfma_f32_16x16x32_bf16 v[16:19], v[140:143], v[188:191], 0
	s_nop 0
	v_mfma_f32_16x16x32_bf16 v[16:19], v[136:139], v[184:187], v[16:19]
	v_mfma_f32_16x16x32_bf16 v[12:15], v[148:151], v[180:183], 0
	s_nop 0
	v_mfma_f32_16x16x32_bf16 v[12:15], v[144:147], v[176:179], v[12:15]
	v_mfma_f32_16x16x32_bf16 v[8:11], v[140:143], v[180:183], 0
	s_nop 0
	v_mfma_f32_16x16x32_bf16 v[8:11], v[136:139], v[176:179], v[8:11]
	v_mfma_f32_16x16x32_bf16 v[4:7], v[148:151], v[172:175], 0
	s_nop 0
	v_mfma_f32_16x16x32_bf16 v[4:7], v[144:147], v[168:171], v[4:7]
	v_mfma_f32_16x16x32_bf16 v[0:3], v[140:143], v[172:175], 0
	s_nop 0
	v_mfma_f32_16x16x32_bf16 v[0:3], v[136:139], v[168:171], v[0:3]
	s_setprio 0
	s_barrier
	ds_read_b128 v[164:167], v224
	ds_read_b128 v[160:163], v225
	ds_read_b128 v[156:159], v226
	ds_read_b128 v[152:155], v227
	ds_read_b128 v[148:151], v228
	ds_read_b128 v[144:147], v229
	ds_read_b128 v[140:143], v230
	ds_read_b128 v[136:139], v231
	ds_read_b128 v[168:171], v232 offset:32768
	ds_read_b128 v[172:175], v232 offset:33792
	ds_read_b128 v[176:179], v232 offset:34816
	ds_read_b128 v[180:183], v232 offset:35840
	ds_read_b128 v[184:187], v232 offset:36864
	ds_read_b128 v[188:191], v232 offset:37888
	ds_read_b128 v[192:195], v232 offset:38912
	ds_read_b128 v[196:199], v232 offset:39936
	s_mov_b32 m0, s68
	s_add_i32 s10, s60, 0x100100
	buffer_load_dwordx4 v213, s[12:15], s10 offen lds
	s_add_i32 s10, s60, 0x180100
	s_mov_b32 m0, s69
	s_nop 0
	buffer_load_dwordx4 v213, s[12:15], s10 offen lds
	s_waitcnt vmcnt(10)
	s_waitcnt lgkmcnt(4)
	s_barrier
	s_setprio 1
	s_waitcnt lgkmcnt(7)
	v_mfma_f32_16x16x32_bf16 v[124:127], v[164:167], v[168:171], v[124:127]
	s_waitcnt lgkmcnt(6)
	v_mfma_f32_16x16x32_bf16 v[124:127], v[160:163], v[172:175], v[124:127]
	v_mfma_f32_16x16x32_bf16 v[120:123], v[156:159], v[168:171], v[120:123]
	s_nop 0
	v_mfma_f32_16x16x32_bf16 v[120:123], v[152:155], v[172:175], v[120:123]
	s_waitcnt lgkmcnt(5)
	v_mfma_f32_16x16x32_bf16 v[116:119], v[164:167], v[176:179], v[116:119]
	s_waitcnt lgkmcnt(4)
	v_mfma_f32_16x16x32_bf16 v[116:119], v[160:163], v[180:183], v[116:119]
	v_mfma_f32_16x16x32_bf16 v[112:115], v[156:159], v[176:179], v[112:115]
	s_nop 0
	v_mfma_f32_16x16x32_bf16 v[112:115], v[152:155], v[180:183], v[112:115]
	s_waitcnt lgkmcnt(3)
	v_mfma_f32_16x16x32_bf16 v[108:111], v[164:167], v[184:187], v[108:111]
	s_waitcnt lgkmcnt(2)
	v_mfma_f32_16x16x32_bf16 v[108:111], v[160:163], v[188:191], v[108:111]
	v_mfma_f32_16x16x32_bf16 v[104:107], v[156:159], v[184:187], v[104:107]
	s_nop 0
	v_mfma_f32_16x16x32_bf16 v[104:107], v[152:155], v[188:191], v[104:107]
	s_waitcnt lgkmcnt(1)
	v_mfma_f32_16x16x32_bf16 v[100:103], v[164:167], v[192:195], v[100:103]
	s_waitcnt lgkmcnt(0)
	v_mfma_f32_16x16x32_bf16 v[100:103], v[160:163], v[196:199], v[100:103]
	v_mfma_f32_16x16x32_bf16 v[96:99], v[156:159], v[192:195], v[96:99]
	s_nop 0
	v_mfma_f32_16x16x32_bf16 v[96:99], v[152:155], v[196:199], v[96:99]
	s_setprio 0
	s_setprio 1
	v_mfma_f32_16x16x32_bf16 v[92:95], v[148:151], v[168:171], v[92:95]
	s_nop 0
	v_mfma_f32_16x16x32_bf16 v[92:95], v[144:147], v[172:175], v[92:95]
	v_mfma_f32_16x16x32_bf16 v[88:91], v[140:143], v[168:171], v[88:91]
	s_nop 0
	v_mfma_f32_16x16x32_bf16 v[88:91], v[136:139], v[172:175], v[88:91]
	v_mfma_f32_16x16x32_bf16 v[84:87], v[148:151], v[176:179], v[84:87]
	s_nop 0
	v_mfma_f32_16x16x32_bf16 v[84:87], v[144:147], v[180:183], v[84:87]
	v_mfma_f32_16x16x32_bf16 v[80:83], v[140:143], v[176:179], v[80:83]
	s_nop 0
	v_mfma_f32_16x16x32_bf16 v[80:83], v[136:139], v[180:183], v[80:83]
	v_mfma_f32_16x16x32_bf16 v[76:79], v[148:151], v[184:187], v[76:79]
	s_nop 0
	v_mfma_f32_16x16x32_bf16 v[76:79], v[144:147], v[188:191], v[76:79]
	v_mfma_f32_16x16x32_bf16 v[72:75], v[140:143], v[184:187], v[72:75]
	s_nop 0
	v_mfma_f32_16x16x32_bf16 v[72:75], v[136:139], v[188:191], v[72:75]
	v_mfma_f32_16x16x32_bf16 v[68:71], v[148:151], v[192:195], v[68:71]
	s_nop 0
	v_mfma_f32_16x16x32_bf16 v[68:71], v[144:147], v[196:199], v[68:71]
	v_mfma_f32_16x16x32_bf16 v[64:67], v[140:143], v[192:195], v[64:67]
	s_nop 0
	v_mfma_f32_16x16x32_bf16 v[64:67], v[136:139], v[196:199], v[64:67]
	s_setprio 0
	s_barrier
	ds_read_b128 v[168:171], v232 offset:49152
	ds_read_b128 v[172:175], v232 offset:50176
	ds_read_b128 v[176:179], v232 offset:51200
	ds_read_b128 v[180:183], v232 offset:52224
	ds_read_b128 v[184:187], v232 offset:53248
	ds_read_b128 v[188:191], v232 offset:54272
	ds_read_b128 v[192:195], v232 offset:55296
	ds_read_b128 v[196:199], v232 offset:56320
	s_mov_b32 m0, s72
	s_mov_b32 s10, s14
	s_mov_b32 s11, s15
	buffer_load_dwordx4 v214, s[8:11], s5 offen lds
	s_add_i32 s5, s42, 0x40180
	s_mov_b32 m0, s73
	s_nop 0
	buffer_load_dwordx4 v214, s[8:11], s5 offen lds
	s_add_i32 s5, s42, 0x4180
	s_mov_b32 m0, s76
	s_nop 0
	buffer_load_dwordx4 v214, s[8:11], s5 offen lds
	s_add_i32 s5, s42, 0x44180
	s_mov_b32 m0, s77
	s_nop 0
	buffer_load_dwordx4 v214, s[8:11], s5 offen lds
	s_mov_b32 m0, s74
	s_nop 0
	buffer_load_dwordx4 v213, s[12:15], s4 offen lds
	s_add_i32 s4, s60, 0x80180
	s_mov_b32 m0, s75
	s_nop 0
	buffer_load_dwordx4 v213, s[12:15], s4 offen lds
	s_waitcnt vmcnt(8)
	s_waitcnt lgkmcnt(0)
	s_barrier
	s_setprio 1
	s_waitcnt lgkmcnt(7)
	v_mfma_f32_16x16x32_bf16 v[60:63], v[164:167], v[168:171], v[60:63]
	s_waitcnt lgkmcnt(6)
	v_mfma_f32_16x16x32_bf16 v[60:63], v[160:163], v[172:175], v[60:63]
	v_mfma_f32_16x16x32_bf16 v[56:59], v[156:159], v[168:171], v[56:59]
	s_nop 0
	v_mfma_f32_16x16x32_bf16 v[56:59], v[152:155], v[172:175], v[56:59]
	s_waitcnt lgkmcnt(5)
	v_mfma_f32_16x16x32_bf16 v[52:55], v[164:167], v[176:179], v[52:55]
	s_waitcnt lgkmcnt(4)
	v_mfma_f32_16x16x32_bf16 v[52:55], v[160:163], v[180:183], v[52:55]
	v_mfma_f32_16x16x32_bf16 v[48:51], v[156:159], v[176:179], v[48:51]
	s_nop 0
	v_mfma_f32_16x16x32_bf16 v[48:51], v[152:155], v[180:183], v[48:51]
	s_waitcnt lgkmcnt(3)
	v_mfma_f32_16x16x32_bf16 v[44:47], v[164:167], v[184:187], v[44:47]
	s_waitcnt lgkmcnt(2)
	v_mfma_f32_16x16x32_bf16 v[44:47], v[160:163], v[188:191], v[44:47]
	v_mfma_f32_16x16x32_bf16 v[40:43], v[156:159], v[184:187], v[40:43]
	s_nop 0
	v_mfma_f32_16x16x32_bf16 v[40:43], v[152:155], v[188:191], v[40:43]
	s_waitcnt lgkmcnt(1)
	v_mfma_f32_16x16x32_bf16 v[36:39], v[164:167], v[192:195], v[36:39]
	s_waitcnt lgkmcnt(0)
	v_mfma_f32_16x16x32_bf16 v[36:39], v[160:163], v[196:199], v[36:39]
	v_mfma_f32_16x16x32_bf16 v[32:35], v[156:159], v[192:195], v[32:35]
	s_nop 0
	v_mfma_f32_16x16x32_bf16 v[32:35], v[152:155], v[196:199], v[32:35]
	s_setprio 0
	s_setprio 1
	v_mfma_f32_16x16x32_bf16 v[28:31], v[148:151], v[168:171], v[28:31]
	s_nop 0
	v_mfma_f32_16x16x32_bf16 v[28:31], v[144:147], v[172:175], v[28:31]
	v_mfma_f32_16x16x32_bf16 v[24:27], v[140:143], v[168:171], v[24:27]
	s_nop 0
	v_mfma_f32_16x16x32_bf16 v[24:27], v[136:139], v[172:175], v[24:27]
	v_mfma_f32_16x16x32_bf16 v[20:23], v[148:151], v[176:179], v[20:23]
	s_nop 0
	v_mfma_f32_16x16x32_bf16 v[20:23], v[144:147], v[180:183], v[20:23]
	v_mfma_f32_16x16x32_bf16 v[16:19], v[140:143], v[176:179], v[16:19]
	s_nop 0
	v_mfma_f32_16x16x32_bf16 v[16:19], v[136:139], v[180:183], v[16:19]
	v_mfma_f32_16x16x32_bf16 v[12:15], v[148:151], v[184:187], v[12:15]
	s_nop 0
	v_mfma_f32_16x16x32_bf16 v[12:15], v[144:147], v[188:191], v[12:15]
	v_mfma_f32_16x16x32_bf16 v[8:11], v[140:143], v[184:187], v[8:11]
	s_nop 0
	v_mfma_f32_16x16x32_bf16 v[8:11], v[136:139], v[188:191], v[8:11]
	v_mfma_f32_16x16x32_bf16 v[4:7], v[148:151], v[192:195], v[4:7]
	s_nop 0
	v_mfma_f32_16x16x32_bf16 v[4:7], v[144:147], v[196:199], v[4:7]
	v_mfma_f32_16x16x32_bf16 v[0:3], v[140:143], v[192:195], v[0:3]
	s_nop 0
	v_mfma_f32_16x16x32_bf16 v[0:3], v[136:139], v[196:199], v[0:3]
	s_setprio 0
	s_barrier
	s_waitcnt vmcnt(14)
	v_mul_f32_e32 v132, 0x42800000, v132
	v_mul_f32_e32 v128, 0x42800000, v128
	v_mul_f32_e32 v133, 0x42800000, v133
	v_mul_f32_e32 v129, 0x42800000, v129
	v_mul_f32_e32 v134, 0x42800000, v134
	v_mul_f32_e32 v130, 0x42800000, v130
	v_mul_f32_e32 v135, 0x42800000, v135
	v_mul_f32_e32 v131, 0x42800000, v131
	v_cvt_pk_fp8_f32 v202, v128, v132
	v_cvt_pk_fp8_f32 v233, v129, v133
	v_cvt_pk_fp8_f32 v234, v130, v134
	v_cvt_pk_fp8_f32 v235, v131, v135
	s_add_i32 s33, s42, 0x200
	s_mov_b32 s66, 0
	s_mov_b32 s89, s70
	s_mov_b32 s90, s71
	s_branch .LBB0_595

.LBB0_595:
	v_mov_b32_e32 v152, v202
	v_mov_b32_e32 v153, v233
	v_mov_b32_e32 v154, v234
	v_mov_b32_e32 v155, v235
	ds_read_b128 v[158:161], v216
	ds_read_b128 v[162:165], v217
	ds_read_b128 v[166:169], v218
	ds_read_b128 v[170:173], v219
	ds_read_b128 v[148:151], v220
	ds_read_b128 v[144:147], v221
	ds_read_b128 v[140:143], v222
	ds_read_b128 v[136:139], v223
	ds_read_b128 v[174:177], v232
	ds_read_b128 v[178:181], v232 offset:1024
	ds_read_b128 v[182:185], v232 offset:2048
	ds_read_b128 v[186:189], v232 offset:3072
	ds_read_b128 v[190:193], v232 offset:4096
	ds_read_b128 v[194:197], v232 offset:5120
	ds_read_b128 v[234:237], v232 offset:6144
	ds_read_b128 v[238:241], v232 offset:7168
	s_add_i32 s4, s60, s66
	s_mov_b32 s42, s90
	s_add_i32 s90, s90, 1
	s_add_i32 s5, s4, 0x200
	s_add_i32 s67, s33, s66
	s_cmpk_eq_i32 s66, 0x200
	s_cselect_b32 s43, s87, s5
	s_cselect_b32 s93, s88, s67
	s_add_i32 s92, s43, 0x80
	s_mov_b32 m0, s78
	s_add_i32 s5, s4, 0x100180
	buffer_load_dwordx4 v213, s[12:15], s5 offen lds
	s_add_i32 s4, s4, 0x180180
	s_mov_b32 m0, s81
	s_add_i32 s94, s93, 0x80
	buffer_load_dwordx4 v213, s[12:15], s4 offen lds
	s_lshr_b32 s4, s90, 2
	s_mul_i32 s67, s4, s34
	s_add_i32 s67, s67, s2
	s_cmp_lt_i32 s4, s3
	s_cselect_b64 s[4:5], -1, 0
	s_and_b64 s[96:97], s[4:5], exec
	s_cselect_b32 s91, s67, 0
	s_ashr_i32 s96, s91, 7
	s_bfe_u32 s95, s90, 0x10001
	s_ashr_i32 s97, s96, 31
	s_or_b32 s95, s95, s79
	s_lshl_b64 s[96:97], s[96:97], 23
	s_add_u32 s96, s48, s96
	s_addc_u32 s97, s49, s97
	s_lshl_b32 vcc_lo, s91, 16
	s_and_b32 vcc_lo, vcc_lo, 0x600000
	s_add_u32 s96, s96, vcc_lo
	s_addc_u32 s97, s97, 0
	s_lshl_b32 s91, s91, 7
	s_and_b32 s91, s91, 0xf80
	s_lshl_b32 vcc_lo, s91, 2
	s_add_u32 s96, s96, vcc_lo
	v_and_or_b32 v202, s89, 2, v200
	s_addc_u32 s97, s97, 0
	v_lshl_or_b32 v156, s95, 5, v215
	v_lshlrev_b64 v[128:129], 14, v[202:203]
	v_lshl_add_u64 v[128:129], s[96:97], 0, v[128:129]
	v_lshlrev_b32_e32 v202, 2, v156
	v_lshl_add_u64 v[128:129], v[128:129], 0, v[202:203]
	s_movk_i32 s95, 0x4000
	v_add_co_u32_e32 v132, vcc, s95, v128
	s_nop 1
	v_addc_co_u32_e32 v133, vcc, 0, v129, vcc
	global_load_dwordx4 v[128:131], v[128:129], off nt
	s_nop 0
	global_load_dwordx4 v[132:135], v[132:133], off nt
	s_waitcnt vmcnt(10)
	s_waitcnt lgkmcnt(4)
	s_barrier
	s_setprio 1
	s_waitcnt lgkmcnt(7)
	v_mfma_f32_16x16x32_bf16 v[124:127], v[158:161], v[174:177], v[124:127]
	s_waitcnt lgkmcnt(6)
	v_mfma_f32_16x16x32_bf16 v[124:127], v[162:165], v[178:181], v[124:127]
	v_mfma_f32_16x16x32_bf16 v[120:123], v[166:169], v[174:177], v[120:123]
	s_nop 0
	v_mfma_f32_16x16x32_bf16 v[120:123], v[170:173], v[178:181], v[120:123]
	s_waitcnt lgkmcnt(5)
	v_mfma_f32_16x16x32_bf16 v[116:119], v[158:161], v[182:185], v[116:119]
	s_waitcnt lgkmcnt(4)
	v_mfma_f32_16x16x32_bf16 v[116:119], v[162:165], v[186:189], v[116:119]
	v_mfma_f32_16x16x32_bf16 v[112:115], v[166:169], v[182:185], v[112:115]
	s_nop 0
	v_mfma_f32_16x16x32_bf16 v[112:115], v[170:173], v[186:189], v[112:115]
	s_waitcnt lgkmcnt(3)
	v_mfma_f32_16x16x32_bf16 v[108:111], v[158:161], v[190:193], v[108:111]
	s_waitcnt lgkmcnt(2)
	v_mfma_f32_16x16x32_bf16 v[108:111], v[162:165], v[194:197], v[108:111]
	v_mfma_f32_16x16x32_bf16 v[104:107], v[166:169], v[190:193], v[104:107]
	s_nop 0
	v_mfma_f32_16x16x32_bf16 v[104:107], v[170:173], v[194:197], v[104:107]
	s_waitcnt lgkmcnt(1)
	v_mfma_f32_16x16x32_bf16 v[100:103], v[158:161], v[234:237], v[100:103]
	s_waitcnt lgkmcnt(0)
	v_mfma_f32_16x16x32_bf16 v[100:103], v[162:165], v[238:241], v[100:103]
	v_mfma_f32_16x16x32_bf16 v[96:99], v[166:169], v[234:237], v[96:99]
	s_nop 0
	v_mfma_f32_16x16x32_bf16 v[96:99], v[170:173], v[238:241], v[96:99]
	s_setprio 0
	s_setprio 1
	v_mfma_f32_16x16x32_bf16 v[92:95], v[148:151], v[174:177], v[92:95]
	s_nop 0
	v_mfma_f32_16x16x32_bf16 v[92:95], v[144:147], v[178:181], v[92:95]
	v_mfma_f32_16x16x32_bf16 v[88:91], v[140:143], v[174:177], v[88:91]
	s_nop 0
	v_mfma_f32_16x16x32_bf16 v[88:91], v[136:139], v[178:181], v[88:91]
	v_mfma_f32_16x16x32_bf16 v[84:87], v[148:151], v[182:185], v[84:87]
	s_nop 0
	v_mfma_f32_16x16x32_bf16 v[84:87], v[144:147], v[186:189], v[84:87]
	v_mfma_f32_16x16x32_bf16 v[80:83], v[140:143], v[182:185], v[80:83]
	s_nop 0
	v_mfma_f32_16x16x32_bf16 v[80:83], v[136:139], v[186:189], v[80:83]
	v_mfma_f32_16x16x32_bf16 v[76:79], v[148:151], v[190:193], v[76:79]
	s_nop 0
	v_mfma_f32_16x16x32_bf16 v[76:79], v[144:147], v[194:197], v[76:79]
	v_mfma_f32_16x16x32_bf16 v[72:75], v[140:143], v[190:193], v[72:75]
	s_nop 0
	v_mfma_f32_16x16x32_bf16 v[72:75], v[136:139], v[194:197], v[72:75]
	v_mfma_f32_16x16x32_bf16 v[68:71], v[148:151], v[234:237], v[68:71]
	s_nop 0
	v_mfma_f32_16x16x32_bf16 v[68:71], v[144:147], v[238:241], v[68:71]
	v_mfma_f32_16x16x32_bf16 v[64:67], v[140:143], v[234:237], v[64:67]
	s_nop 0
	v_mfma_f32_16x16x32_bf16 v[64:67], v[136:139], v[238:241], v[64:67]
	s_setprio 0
	s_barrier
	ds_read_b128 v[174:177], v232 offset:16384
	ds_read_b128 v[178:181], v232 offset:17408
	ds_read_b128 v[182:185], v232 offset:18432
	ds_read_b128 v[186:189], v232 offset:19456
	ds_read_b128 v[190:193], v232 offset:20480
	ds_read_b128 v[194:197], v232 offset:21504
	ds_read_b128 v[234:237], v232 offset:22528
	ds_read_b128 v[238:241], v232 offset:23552
	s_mov_b32 m0, s47
	s_add_i32 s95, s93, 0x40000
	buffer_load_dwordx4 v214, s[8:11], s93 offen lds
	s_mov_b32 m0, s62
	s_nop 0
	buffer_load_dwordx4 v214, s[8:11], s95 offen lds
	s_add_i32 s95, s93, 0x4000
	s_mov_b32 m0, s63
	s_nop 0
	buffer_load_dwordx4 v214, s[8:11], s95 offen lds
	s_add_i32 s95, s93, 0x44000
	s_mov_b32 m0, s64
	s_nop 0
	buffer_load_dwordx4 v214, s[8:11], s95 offen lds
	s_mov_b32 m0, s46
	s_add_i32 s95, s43, 0x80000
	buffer_load_dwordx4 v213, s[12:15], s43 offen lds
	s_mov_b32 m0, s65
	s_nop 0
	buffer_load_dwordx4 v213, s[12:15], s95 offen lds
	s_waitcnt vmcnt(10)
	s_waitcnt lgkmcnt(0)
	s_barrier
	s_setprio 1
	s_waitcnt lgkmcnt(7)
	v_mfma_f32_16x16x32_bf16 v[60:63], v[158:161], v[174:177], v[60:63]
	s_waitcnt lgkmcnt(6)
	v_mfma_f32_16x16x32_bf16 v[60:63], v[162:165], v[178:181], v[60:63]
	v_mfma_f32_16x16x32_bf16 v[56:59], v[166:169], v[174:177], v[56:59]
	s_nop 0
	v_mfma_f32_16x16x32_bf16 v[56:59], v[170:173], v[178:181], v[56:59]
	s_waitcnt lgkmcnt(5)
	v_mfma_f32_16x16x32_bf16 v[52:55], v[158:161], v[182:185], v[52:55]
	s_waitcnt lgkmcnt(4)
	v_mfma_f32_16x16x32_bf16 v[52:55], v[162:165], v[186:189], v[52:55]
	v_mfma_f32_16x16x32_bf16 v[48:51], v[166:169], v[182:185], v[48:51]
	s_nop 0
	v_mfma_f32_16x16x32_bf16 v[48:51], v[170:173], v[186:189], v[48:51]
	s_waitcnt lgkmcnt(3)
	v_mfma_f32_16x16x32_bf16 v[44:47], v[158:161], v[190:193], v[44:47]
	s_waitcnt lgkmcnt(2)
	v_mfma_f32_16x16x32_bf16 v[44:47], v[162:165], v[194:197], v[44:47]
	v_mfma_f32_16x16x32_bf16 v[40:43], v[166:169], v[190:193], v[40:43]
	s_nop 0
	v_mfma_f32_16x16x32_bf16 v[40:43], v[170:173], v[194:197], v[40:43]
	s_waitcnt lgkmcnt(1)
	v_mfma_f32_16x16x32_bf16 v[36:39], v[158:161], v[234:237], v[36:39]
	s_waitcnt lgkmcnt(0)
	v_mfma_f32_16x16x32_bf16 v[36:39], v[162:165], v[238:241], v[36:39]
	v_mfma_f32_16x16x32_bf16 v[32:35], v[166:169], v[234:237], v[32:35]
	s_nop 0
	v_mfma_f32_16x16x32_bf16 v[32:35], v[170:173], v[238:241], v[32:35]
	s_setprio 0
	s_setprio 1
	v_mfma_f32_16x16x32_bf16 v[28:31], v[148:151], v[174:177], v[28:31]
	s_nop 0
	v_mfma_f32_16x16x32_bf16 v[28:31], v[144:147], v[178:181], v[28:31]
	v_mfma_f32_16x16x32_bf16 v[24:27], v[140:143], v[174:177], v[24:27]
	s_nop 0
	v_mfma_f32_16x16x32_bf16 v[24:27], v[136:139], v[178:181], v[24:27]
	v_mfma_f32_16x16x32_bf16 v[20:23], v[148:151], v[182:185], v[20:23]
	s_nop 0
	v_mfma_f32_16x16x32_bf16 v[20:23], v[144:147], v[186:189], v[20:23]
	v_mfma_f32_16x16x32_bf16 v[16:19], v[140:143], v[182:185], v[16:19]
	s_nop 0
	v_mfma_f32_16x16x32_bf16 v[16:19], v[136:139], v[186:189], v[16:19]
	v_mfma_f32_16x16x32_bf16 v[12:15], v[148:151], v[190:193], v[12:15]
	s_nop 0
	v_mfma_f32_16x16x32_bf16 v[12:15], v[144:147], v[194:197], v[12:15]
	v_mfma_f32_16x16x32_bf16 v[8:11], v[140:143], v[190:193], v[8:11]
	s_nop 0
	v_mfma_f32_16x16x32_bf16 v[8:11], v[136:139], v[194:197], v[8:11]
	v_mfma_f32_16x16x32_bf16 v[4:7], v[148:151], v[234:237], v[4:7]
	s_nop 0
	v_mfma_f32_16x16x32_bf16 v[4:7], v[144:147], v[238:241], v[4:7]
	v_mfma_f32_16x16x32_bf16 v[0:3], v[140:143], v[234:237], v[0:3]
	s_nop 0
	v_mfma_f32_16x16x32_bf16 v[0:3], v[136:139], v[238:241], v[0:3]
	s_setprio 0
	s_barrier
	ds_read_b128 v[136:139], v224
	ds_read_b128 v[140:143], v225
	ds_read_b128 v[144:147], v226
	ds_read_b128 v[148:151], v227
	ds_read_b128 v[158:161], v228
	ds_read_b128 v[162:165], v229
	ds_read_b128 v[166:169], v230
	ds_read_b128 v[170:173], v231
	ds_read_b128 v[174:177], v232 offset:32768
	ds_read_b128 v[178:181], v232 offset:33792
	ds_read_b128 v[182:185], v232 offset:34816
	ds_read_b128 v[186:189], v232 offset:35840
	ds_read_b128 v[190:193], v232 offset:36864
	ds_read_b128 v[194:197], v232 offset:37888
	ds_read_b128 v[234:237], v232 offset:38912
	ds_read_b128 v[238:241], v232 offset:39936
	s_mov_b32 m0, s68
	s_add_i32 s95, s43, 0x100000
	buffer_load_dwordx4 v213, s[12:15], s95 offen lds
	s_add_i32 s95, s43, 0x180000
	s_mov_b32 m0, s69
	s_nop 0
	buffer_load_dwordx4 v213, s[12:15], s95 offen lds
	s_waitcnt vmcnt(10)
	s_waitcnt lgkmcnt(4)
	s_barrier
	s_setprio 1
	s_waitcnt lgkmcnt(7)
	v_mfma_f32_16x16x32_bf16 v[124:127], v[136:139], v[174:177], v[124:127]
	s_waitcnt lgkmcnt(6)
	v_mfma_f32_16x16x32_bf16 v[124:127], v[140:143], v[178:181], v[124:127]
	v_mfma_f32_16x16x32_bf16 v[120:123], v[144:147], v[174:177], v[120:123]
	s_nop 0
	v_mfma_f32_16x16x32_bf16 v[120:123], v[148:151], v[178:181], v[120:123]
	s_waitcnt lgkmcnt(5)
	v_mfma_f32_16x16x32_bf16 v[116:119], v[136:139], v[182:185], v[116:119]
	s_waitcnt lgkmcnt(4)
	v_mfma_f32_16x16x32_bf16 v[116:119], v[140:143], v[186:189], v[116:119]
	v_mfma_f32_16x16x32_bf16 v[112:115], v[144:147], v[182:185], v[112:115]
	s_nop 0
	v_mfma_f32_16x16x32_bf16 v[112:115], v[148:151], v[186:189], v[112:115]
	s_waitcnt lgkmcnt(3)
	v_mfma_f32_16x16x32_bf16 v[108:111], v[136:139], v[190:193], v[108:111]
	s_waitcnt lgkmcnt(2)
	v_mfma_f32_16x16x32_bf16 v[108:111], v[140:143], v[194:197], v[108:111]
	v_mfma_f32_16x16x32_bf16 v[104:107], v[144:147], v[190:193], v[104:107]
	s_nop 0
	v_mfma_f32_16x16x32_bf16 v[104:107], v[148:151], v[194:197], v[104:107]
	s_waitcnt lgkmcnt(1)
	v_mfma_f32_16x16x32_bf16 v[100:103], v[136:139], v[234:237], v[100:103]
	s_waitcnt lgkmcnt(0)
	v_mfma_f32_16x16x32_bf16 v[100:103], v[140:143], v[238:241], v[100:103]
	v_mfma_f32_16x16x32_bf16 v[96:99], v[144:147], v[234:237], v[96:99]
	s_nop 0
	v_mfma_f32_16x16x32_bf16 v[96:99], v[148:151], v[238:241], v[96:99]
	s_setprio 0
	s_setprio 1
	v_mfma_f32_16x16x32_bf16 v[92:95], v[158:161], v[174:177], v[92:95]
	s_nop 0
	v_mfma_f32_16x16x32_bf16 v[92:95], v[162:165], v[178:181], v[92:95]
	v_mfma_f32_16x16x32_bf16 v[88:91], v[166:169], v[174:177], v[88:91]
	s_nop 0
	v_mfma_f32_16x16x32_bf16 v[88:91], v[170:173], v[178:181], v[88:91]
	v_mfma_f32_16x16x32_bf16 v[84:87], v[158:161], v[182:185], v[84:87]
	s_nop 0
	v_mfma_f32_16x16x32_bf16 v[84:87], v[162:165], v[186:189], v[84:87]
	v_mfma_f32_16x16x32_bf16 v[80:83], v[166:169], v[182:185], v[80:83]
	s_nop 0
	v_mfma_f32_16x16x32_bf16 v[80:83], v[170:173], v[186:189], v[80:83]
	v_mfma_f32_16x16x32_bf16 v[76:79], v[158:161], v[190:193], v[76:79]
	s_nop 0
	v_mfma_f32_16x16x32_bf16 v[76:79], v[162:165], v[194:197], v[76:79]
	v_mfma_f32_16x16x32_bf16 v[72:75], v[166:169], v[190:193], v[72:75]
	s_nop 0
	v_mfma_f32_16x16x32_bf16 v[72:75], v[170:173], v[194:197], v[72:75]
	v_mfma_f32_16x16x32_bf16 v[68:71], v[158:161], v[234:237], v[68:71]
	s_nop 0
	v_mfma_f32_16x16x32_bf16 v[68:71], v[162:165], v[238:241], v[68:71]
	v_mfma_f32_16x16x32_bf16 v[64:67], v[166:169], v[234:237], v[64:67]
	s_nop 0
	v_mfma_f32_16x16x32_bf16 v[64:67], v[170:173], v[238:241], v[64:67]
	s_setprio 0
	s_barrier
	ds_read_b128 v[174:177], v232 offset:49152
	ds_read_b128 v[178:181], v232 offset:50176
	ds_read_b128 v[182:185], v232 offset:51200
	ds_read_b128 v[186:189], v232 offset:52224
	ds_read_b128 v[190:193], v232 offset:53248
	ds_read_b128 v[194:197], v232 offset:54272
	ds_read_b128 v[234:237], v232 offset:55296
	ds_read_b128 v[238:241], v232 offset:56320
	s_mov_b32 m0, s72
	s_add_i32 s43, s43, 0x80080
	buffer_load_dwordx4 v214, s[8:11], s94 offen lds
	s_add_i32 s94, s93, 0x40080
	s_mov_b32 m0, s73
	s_nop 0
	buffer_load_dwordx4 v214, s[8:11], s94 offen lds
	s_add_i32 s94, s93, 0x4080
	s_mov_b32 m0, s76
	s_add_i32 s93, s93, 0x44080
	buffer_load_dwordx4 v214, s[8:11], s94 offen lds
	s_mov_b32 m0, s77
	s_nop 0
	buffer_load_dwordx4 v214, s[8:11], s93 offen lds
	s_mov_b32 m0, s74
	s_nop 0
	buffer_load_dwordx4 v213, s[12:15], s92 offen lds
	s_mov_b32 m0, s75
	s_nop 0
	buffer_load_dwordx4 v213, s[12:15], s43 offen lds
	s_waitcnt vmcnt(8)
	s_waitcnt lgkmcnt(0)
	s_barrier
	s_setprio 1
	s_waitcnt lgkmcnt(7)
	v_mfma_f32_16x16x32_bf16 v[60:63], v[136:139], v[174:177], v[60:63]
	s_waitcnt lgkmcnt(6)
	v_mfma_f32_16x16x32_bf16 v[60:63], v[140:143], v[178:181], v[60:63]
	v_mfma_f32_16x16x32_bf16 v[56:59], v[144:147], v[174:177], v[56:59]
	s_nop 0
	v_mfma_f32_16x16x32_bf16 v[56:59], v[148:151], v[178:181], v[56:59]
	s_waitcnt lgkmcnt(5)
	v_mfma_f32_16x16x32_bf16 v[52:55], v[136:139], v[182:185], v[52:55]
	s_waitcnt lgkmcnt(4)
	v_mfma_f32_16x16x32_bf16 v[52:55], v[140:143], v[186:189], v[52:55]
	v_mfma_f32_16x16x32_bf16 v[48:51], v[144:147], v[182:185], v[48:51]
	s_nop 0
	v_mfma_f32_16x16x32_bf16 v[48:51], v[148:151], v[186:189], v[48:51]
	s_waitcnt lgkmcnt(3)
	v_mfma_f32_16x16x32_bf16 v[44:47], v[136:139], v[190:193], v[44:47]
	s_waitcnt lgkmcnt(2)
	v_mfma_f32_16x16x32_bf16 v[44:47], v[140:143], v[194:197], v[44:47]
	v_mfma_f32_16x16x32_bf16 v[40:43], v[144:147], v[190:193], v[40:43]
	s_nop 0
	v_mfma_f32_16x16x32_bf16 v[40:43], v[148:151], v[194:197], v[40:43]
	s_waitcnt lgkmcnt(1)
	v_mfma_f32_16x16x32_bf16 v[36:39], v[136:139], v[234:237], v[36:39]
	s_waitcnt lgkmcnt(0)
	v_mfma_f32_16x16x32_bf16 v[36:39], v[140:143], v[238:241], v[36:39]
	v_mfma_f32_16x16x32_bf16 v[32:35], v[144:147], v[234:237], v[32:35]
	s_nop 0
	v_mfma_f32_16x16x32_bf16 v[32:35], v[148:151], v[238:241], v[32:35]
	s_setprio 0
	s_setprio 1
	v_mfma_f32_16x16x32_bf16 v[28:31], v[158:161], v[174:177], v[28:31]
	s_nop 0
	v_mfma_f32_16x16x32_bf16 v[28:31], v[162:165], v[178:181], v[28:31]
	v_mfma_f32_16x16x32_bf16 v[24:27], v[166:169], v[174:177], v[24:27]
	s_nop 0
	v_mfma_f32_16x16x32_bf16 v[24:27], v[170:173], v[178:181], v[24:27]
	v_mfma_f32_16x16x32_bf16 v[20:23], v[158:161], v[182:185], v[20:23]
	s_nop 0
	v_mfma_f32_16x16x32_bf16 v[20:23], v[162:165], v[186:189], v[20:23]
	v_mfma_f32_16x16x32_bf16 v[16:19], v[166:169], v[182:185], v[16:19]
	s_nop 0
	v_mfma_f32_16x16x32_bf16 v[16:19], v[170:173], v[186:189], v[16:19]
	v_mfma_f32_16x16x32_bf16 v[12:15], v[158:161], v[190:193], v[12:15]
	s_nop 0
	v_mfma_f32_16x16x32_bf16 v[12:15], v[162:165], v[194:197], v[12:15]
	v_mfma_f32_16x16x32_bf16 v[8:11], v[166:169], v[190:193], v[8:11]
	s_nop 0
	v_mfma_f32_16x16x32_bf16 v[8:11], v[170:173], v[194:197], v[8:11]
	v_mfma_f32_16x16x32_bf16 v[4:7], v[158:161], v[234:237], v[4:7]
	s_nop 0
	v_mfma_f32_16x16x32_bf16 v[4:7], v[162:165], v[238:241], v[4:7]
	v_mfma_f32_16x16x32_bf16 v[0:3], v[166:169], v[234:237], v[0:3]
	s_nop 0
	v_mfma_f32_16x16x32_bf16 v[0:3], v[170:173], v[238:241], v[0:3]
	s_setprio 0
	s_barrier
	s_bitcmp0_b32 s42, 0
	s_waitcnt vmcnt(15)
	v_mul_f32_e32 v128, 0x42800000, v128
	s_waitcnt vmcnt(14)
	v_mul_f32_e32 v132, 0x42800000, v132
	v_mul_f32_e32 v129, 0x42800000, v129
	v_mul_f32_e32 v133, 0x42800000, v133
	v_mul_f32_e32 v130, 0x42800000, v130
	v_mul_f32_e32 v134, 0x42800000, v134
	v_mul_f32_e32 v131, 0x42800000, v131
	v_mul_f32_e32 v135, 0x42800000, v135
	s_mov_b64 s[42:43], -1
	s_cbranch_scc0 .LBB0_598
	s_andn2_b64 vcc, exec, s[42:43]
	s_cbranch_vccnz .LBB0_594
	s_branch .LBB0_599

.LBB0_923:
	s_add_i32 s3, s94, 0x180
	s_add_i32 s4, s36, 0x180
	s_waitcnt lgkmcnt(0)
	s_barrier
	s_setprio 1
	v_mfma_scale_f32_16x16x128_f8f6f4 v[124:127], v[24:31], v[56:63], 0, v213, v213 op_sel_hi:[0,0,0]
	v_mfma_scale_f32_16x16x128_f8f6f4 v[120:123], v[16:23], v[56:63], 0, v213, v213 op_sel_hi:[0,0,0]
	v_mfma_scale_f32_16x16x128_f8f6f4 v[116:119], v[24:31], v[48:55], 0, v213, v213 op_sel_hi:[0,0,0]
	v_mfma_scale_f32_16x16x128_f8f6f4 v[112:115], v[16:23], v[48:55], 0, v213, v213 op_sel_hi:[0,0,0]
	v_mfma_scale_f32_16x16x128_f8f6f4 v[108:111], v[24:31], v[40:47], 0, v213, v213 op_sel_hi:[0,0,0]
	v_mfma_scale_f32_16x16x128_f8f6f4 v[104:107], v[16:23], v[40:47], 0, v213, v213 op_sel_hi:[0,0,0]
	v_mfma_scale_f32_16x16x128_f8f6f4 v[100:103], v[24:31], v[32:39], 0, v213, v213 op_sel_hi:[0,0,0]
	v_mfma_scale_f32_16x16x128_f8f6f4 v[96:99], v[16:23], v[32:39], 0, v213, v213 op_sel_hi:[0,0,0]
	s_setprio 0
	s_setprio 1
	v_mfma_scale_f32_16x16x128_f8f6f4 v[92:95], v[8:15], v[56:63], 0, v213, v213 op_sel_hi:[0,0,0]
	v_mfma_scale_f32_16x16x128_f8f6f4 v[88:91], v[0:7], v[56:63], 0, v213, v213 op_sel_hi:[0,0,0]
	v_mfma_scale_f32_16x16x128_f8f6f4 v[84:87], v[8:15], v[48:55], 0, v213, v213 op_sel_hi:[0,0,0]
	v_mfma_scale_f32_16x16x128_f8f6f4 v[80:83], v[0:7], v[48:55], 0, v213, v213 op_sel_hi:[0,0,0]
	v_mfma_scale_f32_16x16x128_f8f6f4 v[76:79], v[8:15], v[40:47], 0, v213, v213 op_sel_hi:[0,0,0]
	v_mfma_scale_f32_16x16x128_f8f6f4 v[72:75], v[0:7], v[40:47], 0, v213, v213 op_sel_hi:[0,0,0]
	v_mfma_scale_f32_16x16x128_f8f6f4 v[68:71], v[8:15], v[32:39], 0, v213, v213 op_sel_hi:[0,0,0]
	v_mfma_scale_f32_16x16x128_f8f6f4 v[64:67], v[0:7], v[32:39], 0, v213, v213 op_sel_hi:[0,0,0]
	s_setprio 0
	s_barrier
	ds_read_b128 v[24:27], v217 offset:0x8000
	ds_read_b128 v[28:31], v217 offset:0x8400
	ds_read_b128 v[16:19], v217 offset:0x8800
	ds_read_b128 v[20:23], v217 offset:0x8c00
	ds_read_b128 v[32:35], v216 offset:0x8000
	ds_read_b128 v[36:39], v216 offset:0x8400
	ds_read_b128 v[40:43], v216 offset:0x8800
	ds_read_b128 v[44:47], v216 offset:0x8c00
	ds_read_b128 v[48:51], v216 offset:0x9000
	ds_read_b128 v[52:55], v216 offset:0x9400
	ds_read_b128 v[56:59], v216 offset:0x9800
	ds_read_b128 v[60:63], v216 offset:0x9c00
	ds_read_b128 v[8:11], v217 offset:0xc000
	ds_read_b128 v[12:15], v217 offset:0xc400
	ds_read_b128 v[0:3], v217 offset:0xc800
	ds_read_b128 v[4:7], v217 offset:0xcc00
	s_mov_b32 m0, s76
	s_add_i32 s5, s94, 0x80100
	buffer_load_dwordx4 v214, s[12:15], s5 offen lds
	s_add_i32 s5, s94, 0xc0100
	s_mov_b32 m0, s77
	s_nop 0
	buffer_load_dwordx4 v214, s[12:15], s5 offen lds
	s_waitcnt vmcnt(10)
	s_waitcnt lgkmcnt(4)
	s_barrier
	s_setprio 1
	v_mfma_scale_f32_16x16x128_f8f6f4 v[188:191], v[24:31], v[32:39], v[188:191], v213, v213 op_sel_hi:[0,0,0]
	v_mfma_scale_f32_16x16x128_f8f6f4 v[184:187], v[16:23], v[32:39], v[184:187], v213, v213 op_sel_hi:[0,0,0]
	v_mfma_scale_f32_16x16x128_f8f6f4 v[180:183], v[24:31], v[40:47], v[180:183], v213, v213 op_sel_hi:[0,0,0]
	v_mfma_scale_f32_16x16x128_f8f6f4 v[176:179], v[16:23], v[40:47], v[176:179], v213, v213 op_sel_hi:[0,0,0]
	v_mfma_scale_f32_16x16x128_f8f6f4 v[172:175], v[24:31], v[48:55], v[172:175], v213, v213 op_sel_hi:[0,0,0]
	v_mfma_scale_f32_16x16x128_f8f6f4 v[168:171], v[16:23], v[48:55], v[168:171], v213, v213 op_sel_hi:[0,0,0]
	v_mfma_scale_f32_16x16x128_f8f6f4 v[164:167], v[24:31], v[56:63], v[164:167], v213, v213 op_sel_hi:[0,0,0]
	v_mfma_scale_f32_16x16x128_f8f6f4 v[160:163], v[16:23], v[56:63], v[160:163], v213, v213 op_sel_hi:[0,0,0]
	s_setprio 0
	s_setprio 1
	s_waitcnt lgkmcnt(2)
	v_mfma_scale_f32_16x16x128_f8f6f4 v[156:159], v[8:15], v[32:39], v[156:159], v213, v213 op_sel_hi:[0,0,0]
	s_waitcnt lgkmcnt(0)
	v_mfma_scale_f32_16x16x128_f8f6f4 v[152:155], v[0:7], v[32:39], v[152:155], v213, v213 op_sel_hi:[0,0,0]
	v_mfma_scale_f32_16x16x128_f8f6f4 v[148:151], v[8:15], v[40:47], v[148:151], v213, v213 op_sel_hi:[0,0,0]
	v_mfma_scale_f32_16x16x128_f8f6f4 v[144:147], v[0:7], v[40:47], v[144:147], v213, v213 op_sel_hi:[0,0,0]
	v_mfma_scale_f32_16x16x128_f8f6f4 v[140:143], v[8:15], v[48:55], v[140:143], v213, v213 op_sel_hi:[0,0,0]
	v_mfma_scale_f32_16x16x128_f8f6f4 v[136:139], v[0:7], v[48:55], v[136:139], v213, v213 op_sel_hi:[0,0,0]
	v_mfma_scale_f32_16x16x128_f8f6f4 v[132:135], v[8:15], v[56:63], v[132:135], v213, v213 op_sel_hi:[0,0,0]
	v_mfma_scale_f32_16x16x128_f8f6f4 v[128:131], v[0:7], v[56:63], v[128:131], v213, v213 op_sel_hi:[0,0,0]
	s_setprio 0
	s_barrier
	ds_read_b128 v[32:35], v216 offset:0xc000
	ds_read_b128 v[36:39], v216 offset:0xc400
	ds_read_b128 v[40:43], v216 offset:0xc800
	ds_read_b128 v[44:47], v216 offset:0xcc00
	ds_read_b128 v[48:51], v216 offset:0xd000
	ds_read_b128 v[52:55], v216 offset:0xd400
	ds_read_b128 v[56:59], v216 offset:0xd800
	ds_read_b128 v[60:63], v216 offset:0xdc00
	s_mov_b32 m0, s80
	s_mov_b32 s10, s14
	s_mov_b32 s11, s15
	buffer_load_dwordx4 v215, s[8:11], s4 offen lds
	s_add_i32 s4, s36, 0x80180
	s_mov_b32 m0, s81
	s_nop 0
	buffer_load_dwordx4 v215, s[8:11], s4 offen lds
	s_add_i32 s4, s36, 0x8180
	s_mov_b32 m0, s84
	s_nop 0
	buffer_load_dwordx4 v215, s[8:11], s4 offen lds
	s_add_i32 s4, s36, 0x88180
	s_mov_b32 m0, s85
	s_nop 0
	buffer_load_dwordx4 v215, s[8:11], s4 offen lds
	s_mov_b32 m0, s82
	s_nop 0
	buffer_load_dwordx4 v214, s[12:15], s3 offen lds
	s_add_i32 s3, s94, 0x40180
	s_mov_b32 m0, s83
	s_nop 0
	buffer_load_dwordx4 v214, s[12:15], s3 offen lds
	s_waitcnt vmcnt(8)
	s_waitcnt lgkmcnt(0)
	s_barrier
	s_setprio 1
	v_mfma_scale_f32_16x16x128_f8f6f4 v[124:127], v[24:31], v[32:39], v[124:127], v213, v213 op_sel_hi:[0,0,0]
	v_mfma_scale_f32_16x16x128_f8f6f4 v[120:123], v[16:23], v[32:39], v[120:123], v213, v213 op_sel_hi:[0,0,0]
	v_mfma_scale_f32_16x16x128_f8f6f4 v[116:119], v[24:31], v[40:47], v[116:119], v213, v213 op_sel_hi:[0,0,0]
	v_mfma_scale_f32_16x16x128_f8f6f4 v[112:115], v[16:23], v[40:47], v[112:115], v213, v213 op_sel_hi:[0,0,0]
	v_mfma_scale_f32_16x16x128_f8f6f4 v[108:111], v[24:31], v[48:55], v[108:111], v213, v213 op_sel_hi:[0,0,0]
	v_mfma_scale_f32_16x16x128_f8f6f4 v[104:107], v[16:23], v[48:55], v[104:107], v213, v213 op_sel_hi:[0,0,0]
	v_mfma_scale_f32_16x16x128_f8f6f4 v[100:103], v[24:31], v[56:63], v[100:103], v213, v213 op_sel_hi:[0,0,0]
	v_mfma_scale_f32_16x16x128_f8f6f4 v[96:99], v[16:23], v[56:63], v[96:99], v213, v213 op_sel_hi:[0,0,0]
	s_setprio 0
	s_setprio 1
	v_mfma_scale_f32_16x16x128_f8f6f4 v[92:95], v[8:15], v[32:39], v[92:95], v213, v213 op_sel_hi:[0,0,0]
	v_mfma_scale_f32_16x16x128_f8f6f4 v[88:91], v[0:7], v[32:39], v[88:91], v213, v213 op_sel_hi:[0,0,0]
	v_mfma_scale_f32_16x16x128_f8f6f4 v[84:87], v[8:15], v[40:47], v[84:87], v213, v213 op_sel_hi:[0,0,0]
	v_mfma_scale_f32_16x16x128_f8f6f4 v[80:83], v[0:7], v[40:47], v[80:83], v213, v213 op_sel_hi:[0,0,0]
	v_mfma_scale_f32_16x16x128_f8f6f4 v[76:79], v[8:15], v[48:55], v[76:79], v213, v213 op_sel_hi:[0,0,0]
	v_mfma_scale_f32_16x16x128_f8f6f4 v[72:75], v[0:7], v[48:55], v[72:75], v213, v213 op_sel_hi:[0,0,0]
	v_mfma_scale_f32_16x16x128_f8f6f4 v[68:71], v[8:15], v[56:63], v[68:71], v213, v213 op_sel_hi:[0,0,0]
	v_mfma_scale_f32_16x16x128_f8f6f4 v[64:67], v[0:7], v[56:63], v[64:67], v213, v213 op_sel_hi:[0,0,0]
	s_setprio 0
	s_barrier
	s_waitcnt vmcnt(14)
	v_mul_f32_e32 v0, 0x42800000, v196
	v_mul_f32_e32 v1, 0x42800000, v192
	v_mul_f32_e32 v2, 0x42800000, v197
	v_mul_f32_e32 v3, 0x42800000, v193
	v_mul_f32_e32 v4, 0x42800000, v198
	v_mul_f32_e32 v5, 0x42800000, v194
	v_mul_f32_e32 v6, 0x42800000, v199
	v_mul_f32_e32 v7, 0x42800000, v195
	v_cvt_pk_fp8_f32 v202, v1, v0
	v_cvt_pk_fp8_f32 v219, v3, v2
	v_cvt_pk_fp8_f32 v220, v5, v4
	v_cvt_pk_fp8_f32 v221, v7, v6
	s_add_i32 s61, s36, 0x200
	s_mov_b32 s33, 0
	s_mov_b32 s79, s66
	s_mov_b32 s90, s68
	s_branch .LBB0_926

.LBB0_926:
	v_mov_b32_e32 v40, v202
	v_mov_b32_e32 v41, v219
	v_mov_b32_e32 v42, v220
	v_mov_b32_e32 v43, v221
	s_add_i32 s4, s94, s33
	s_mov_b32 s64, s90
	s_add_i32 s90, s90, 1
	s_add_i32 s3, s4, 0x200
	s_add_i32 s5, s61, s33
	ds_read_b128 v[24:27], v217 offset:0
	ds_read_b128 v[28:31], v217 offset:0x400
	ds_read_b128 v[16:19], v217 offset:0x800
	ds_read_b128 v[20:23], v217 offset:0xc00
	ds_read_b128 v[46:49], v216 offset:0
	ds_read_b128 v[50:53], v216 offset:0x400
	ds_read_b128 v[54:57], v216 offset:0x800
	ds_read_b128 v[58:61], v216 offset:0xc00
	ds_read_b128 v[192:195], v216 offset:0x1000
	ds_read_b128 v[196:199], v216 offset:0x1400
	ds_read_b128 v[220:223], v216 offset:0x1800
	ds_read_b128 v[224:227], v216 offset:0x1c00
	ds_read_b128 v[8:11], v217 offset:0x4000
	ds_read_b128 v[12:15], v217 offset:0x4400
	ds_read_b128 v[0:3], v217 offset:0x4800
	ds_read_b128 v[4:7], v217 offset:0x4c00
	s_cmpk_eq_i32 s33, 0xe00
	s_cselect_b32 s65, s60, s3
	s_cselect_b32 s16, s95, s5
	s_add_i32 s3, s65, 0x80
	s_mov_b32 m0, s86
	s_add_i32 s5, s4, 0x80180
	buffer_load_dwordx4 v214, s[12:15], s5 offen lds
	s_add_i32 s4, s4, 0xc0180
	s_mov_b32 m0, s89
	s_add_i32 s17, s16, 0x80
	buffer_load_dwordx4 v214, s[12:15], s4 offen lds
	s_lshr_b32 s4, s90, 2
	s_mul_i32 s5, s4, s34
	s_add_i32 s36, s5, s2
	s_cmp_lt_i32 s4, s47
	s_cselect_b64 s[4:5], -1, 0
	s_and_b64 s[62:63], s[4:5], exec
	s_cselect_b32 s67, s36, 0
	s_ashr_i32 s62, s67, 7
	s_bfe_u32 s36, s90, 0x10001
	s_ashr_i32 s63, s62, 31
	s_or_b32 s78, s36, s87
	s_bfe_u32 s36, s67, 0x20005
	s_lshl_b64 vcc, s[62:63], 23
	s_add_u32 vcc_lo, s28, vcc_lo
	s_addc_u32 vcc_hi, s29, vcc_hi
	s_lshl_b32 s38, s36, 21
	s_add_u32 s38, vcc_lo, s38
	s_addc_u32 s39, vcc_hi, 0
	s_lshl_b32 s67, s67, 7
	s_and_b32 s67, s67, 0xf80
	s_lshl_b32 vcc_lo, s67, 2
	s_add_u32 vcc_lo, s38, vcc_lo
	v_and_or_b32 v202, s79, 2, v200
	s_addc_u32 vcc_hi, s39, 0
	v_lshl_or_b32 v44, s78, 5, v218
	v_lshlrev_b64 v[32:33], 14, v[202:203]
	v_lshl_add_u64 v[32:33], vcc, 0, v[32:33]
	v_lshlrev_b32_e32 v202, 2, v44
	v_lshl_add_u64 v[32:33], v[32:33], 0, v[202:203]
	s_movk_i32 s38, 0x4000
	v_add_co_u32_e32 v36, vcc, s38, v32
	s_nop 1
	v_addc_co_u32_e32 v37, vcc, 0, v33, vcc
	global_load_dwordx4 v[32:35], v[32:33], off nt
	s_nop 0
	global_load_dwordx4 v[36:39], v[36:37], off nt
	s_waitcnt vmcnt(10)
	s_waitcnt lgkmcnt(4)
	s_barrier
	s_setprio 1
	v_mfma_scale_f32_16x16x128_f8f6f4 v[188:191], v[24:31], v[46:53], v[188:191], v213, v213 op_sel_hi:[0,0,0]
	v_mfma_scale_f32_16x16x128_f8f6f4 v[184:187], v[16:23], v[46:53], v[184:187], v213, v213 op_sel_hi:[0,0,0]
	v_mfma_scale_f32_16x16x128_f8f6f4 v[180:183], v[24:31], v[54:61], v[180:183], v213, v213 op_sel_hi:[0,0,0]
	v_mfma_scale_f32_16x16x128_f8f6f4 v[176:179], v[16:23], v[54:61], v[176:179], v213, v213 op_sel_hi:[0,0,0]
	v_mfma_scale_f32_16x16x128_f8f6f4 v[172:175], v[24:31], v[192:199], v[172:175], v213, v213 op_sel_hi:[0,0,0]
	v_mfma_scale_f32_16x16x128_f8f6f4 v[168:171], v[16:23], v[192:199], v[168:171], v213, v213 op_sel_hi:[0,0,0]
	v_mfma_scale_f32_16x16x128_f8f6f4 v[164:167], v[24:31], v[220:227], v[164:167], v213, v213 op_sel_hi:[0,0,0]
	v_mfma_scale_f32_16x16x128_f8f6f4 v[160:163], v[16:23], v[220:227], v[160:163], v213, v213 op_sel_hi:[0,0,0]
	s_setprio 0
	s_setprio 1
	s_waitcnt lgkmcnt(2)
	v_mfma_scale_f32_16x16x128_f8f6f4 v[156:159], v[8:15], v[46:53], v[156:159], v213, v213 op_sel_hi:[0,0,0]
	s_waitcnt lgkmcnt(0)
	v_mfma_scale_f32_16x16x128_f8f6f4 v[152:155], v[0:7], v[46:53], v[152:155], v213, v213 op_sel_hi:[0,0,0]
	v_mfma_scale_f32_16x16x128_f8f6f4 v[148:151], v[8:15], v[54:61], v[148:151], v213, v213 op_sel_hi:[0,0,0]
	v_mfma_scale_f32_16x16x128_f8f6f4 v[144:147], v[0:7], v[54:61], v[144:147], v213, v213 op_sel_hi:[0,0,0]
	v_mfma_scale_f32_16x16x128_f8f6f4 v[140:143], v[8:15], v[192:199], v[140:143], v213, v213 op_sel_hi:[0,0,0]
	v_mfma_scale_f32_16x16x128_f8f6f4 v[136:139], v[0:7], v[192:199], v[136:139], v213, v213 op_sel_hi:[0,0,0]
	v_mfma_scale_f32_16x16x128_f8f6f4 v[132:135], v[8:15], v[220:227], v[132:135], v213, v213 op_sel_hi:[0,0,0]
	v_mfma_scale_f32_16x16x128_f8f6f4 v[128:131], v[0:7], v[220:227], v[128:131], v213, v213 op_sel_hi:[0,0,0]
	s_setprio 0
	s_barrier
	ds_read_b128 v[46:49], v216 offset:0x4000
	ds_read_b128 v[50:53], v216 offset:0x4400
	ds_read_b128 v[54:57], v216 offset:0x4800
	ds_read_b128 v[58:61], v216 offset:0x4c00
	ds_read_b128 v[192:195], v216 offset:0x5000
	ds_read_b128 v[196:199], v216 offset:0x5400
	ds_read_b128 v[220:223], v216 offset:0x5800
	ds_read_b128 v[224:227], v216 offset:0x5c00
	s_mov_b32 m0, s71
	s_nop 0
	buffer_load_dwordx4 v215, s[8:11], s16 offen lds
	s_add_i32 s38, s16, 0x80000
	s_mov_b32 m0, s72
	s_nop 0
	buffer_load_dwordx4 v215, s[8:11], s38 offen lds
	s_add_i32 s38, s16, 0x8000
	s_mov_b32 m0, s73
	s_nop 0
	buffer_load_dwordx4 v215, s[8:11], s38 offen lds
	s_add_i32 s38, s16, 0x88000
	s_mov_b32 m0, s74
	s_nop 0
	buffer_load_dwordx4 v215, s[8:11], s38 offen lds
	s_mov_b32 m0, s70
	s_add_i32 s38, s65, 0x40000
	buffer_load_dwordx4 v214, s[12:15], s65 offen lds
	s_mov_b32 m0, s75
	s_nop 0
	buffer_load_dwordx4 v214, s[12:15], s38 offen lds
	s_waitcnt vmcnt(10)
	s_waitcnt lgkmcnt(0)
	s_barrier
	s_setprio 1
	v_mfma_scale_f32_16x16x128_f8f6f4 v[124:127], v[24:31], v[46:53], v[124:127], v213, v213 op_sel_hi:[0,0,0]
	v_mfma_scale_f32_16x16x128_f8f6f4 v[120:123], v[16:23], v[46:53], v[120:123], v213, v213 op_sel_hi:[0,0,0]
	v_mfma_scale_f32_16x16x128_f8f6f4 v[116:119], v[24:31], v[54:61], v[116:119], v213, v213 op_sel_hi:[0,0,0]
	v_mfma_scale_f32_16x16x128_f8f6f4 v[112:115], v[16:23], v[54:61], v[112:115], v213, v213 op_sel_hi:[0,0,0]
	v_mfma_scale_f32_16x16x128_f8f6f4 v[108:111], v[24:31], v[192:199], v[108:111], v213, v213 op_sel_hi:[0,0,0]
	v_mfma_scale_f32_16x16x128_f8f6f4 v[104:107], v[16:23], v[192:199], v[104:107], v213, v213 op_sel_hi:[0,0,0]
	v_mfma_scale_f32_16x16x128_f8f6f4 v[100:103], v[24:31], v[220:227], v[100:103], v213, v213 op_sel_hi:[0,0,0]
	v_mfma_scale_f32_16x16x128_f8f6f4 v[96:99], v[16:23], v[220:227], v[96:99], v213, v213 op_sel_hi:[0,0,0]
	s_setprio 0
	s_setprio 1
	v_mfma_scale_f32_16x16x128_f8f6f4 v[92:95], v[8:15], v[46:53], v[92:95], v213, v213 op_sel_hi:[0,0,0]
	v_mfma_scale_f32_16x16x128_f8f6f4 v[88:91], v[0:7], v[46:53], v[88:91], v213, v213 op_sel_hi:[0,0,0]
	v_mfma_scale_f32_16x16x128_f8f6f4 v[84:87], v[8:15], v[54:61], v[84:87], v213, v213 op_sel_hi:[0,0,0]
	v_mfma_scale_f32_16x16x128_f8f6f4 v[80:83], v[0:7], v[54:61], v[80:83], v213, v213 op_sel_hi:[0,0,0]
	v_mfma_scale_f32_16x16x128_f8f6f4 v[76:79], v[8:15], v[192:199], v[76:79], v213, v213 op_sel_hi:[0,0,0]
	v_mfma_scale_f32_16x16x128_f8f6f4 v[72:75], v[0:7], v[192:199], v[72:75], v213, v213 op_sel_hi:[0,0,0]
	v_mfma_scale_f32_16x16x128_f8f6f4 v[68:71], v[8:15], v[220:227], v[68:71], v213, v213 op_sel_hi:[0,0,0]
	v_mfma_scale_f32_16x16x128_f8f6f4 v[64:67], v[0:7], v[220:227], v[64:67], v213, v213 op_sel_hi:[0,0,0]
	s_setprio 0
	s_barrier
	ds_read_b128 v[16:19], v217 offset:0x8000
	ds_read_b128 v[20:23], v217 offset:0x8400
	ds_read_b128 v[24:27], v217 offset:0x8800
	ds_read_b128 v[28:31], v217 offset:0x8c00
	ds_read_b128 v[46:49], v216 offset:0x8000
	ds_read_b128 v[50:53], v216 offset:0x8400
	ds_read_b128 v[54:57], v216 offset:0x8800
	ds_read_b128 v[58:61], v216 offset:0x8c00
	ds_read_b128 v[192:195], v216 offset:0x9000
	ds_read_b128 v[196:199], v216 offset:0x9400
	ds_read_b128 v[220:223], v216 offset:0x9800
	ds_read_b128 v[224:227], v216 offset:0x9c00
	ds_read_b128 v[8:11], v217 offset:0xc000
	ds_read_b128 v[12:15], v217 offset:0xc400
	ds_read_b128 v[0:3], v217 offset:0xc800
	ds_read_b128 v[4:7], v217 offset:0xcc00
	s_mov_b32 m0, s76
	s_add_i32 s38, s65, 0x80000
	buffer_load_dwordx4 v214, s[12:15], s38 offen lds
	s_add_i32 s38, s65, 0xc0000
	s_mov_b32 m0, s77
	s_nop 0
	buffer_load_dwordx4 v214, s[12:15], s38 offen lds
	s_waitcnt vmcnt(10)
	s_waitcnt lgkmcnt(4)
	s_barrier
	s_setprio 1
	v_mfma_scale_f32_16x16x128_f8f6f4 v[188:191], v[16:23], v[46:53], v[188:191], v213, v213 op_sel_hi:[0,0,0]
	v_mfma_scale_f32_16x16x128_f8f6f4 v[184:187], v[24:31], v[46:53], v[184:187], v213, v213 op_sel_hi:[0,0,0]
	v_mfma_scale_f32_16x16x128_f8f6f4 v[180:183], v[16:23], v[54:61], v[180:183], v213, v213 op_sel_hi:[0,0,0]
	v_mfma_scale_f32_16x16x128_f8f6f4 v[176:179], v[24:31], v[54:61], v[176:179], v213, v213 op_sel_hi:[0,0,0]
	v_mfma_scale_f32_16x16x128_f8f6f4 v[172:175], v[16:23], v[192:199], v[172:175], v213, v213 op_sel_hi:[0,0,0]
	v_mfma_scale_f32_16x16x128_f8f6f4 v[168:171], v[24:31], v[192:199], v[168:171], v213, v213 op_sel_hi:[0,0,0]
	v_mfma_scale_f32_16x16x128_f8f6f4 v[164:167], v[16:23], v[220:227], v[164:167], v213, v213 op_sel_hi:[0,0,0]
	v_mfma_scale_f32_16x16x128_f8f6f4 v[160:163], v[24:31], v[220:227], v[160:163], v213, v213 op_sel_hi:[0,0,0]
	s_setprio 0
	s_setprio 1
	s_waitcnt lgkmcnt(2)
	v_mfma_scale_f32_16x16x128_f8f6f4 v[156:159], v[8:15], v[46:53], v[156:159], v213, v213 op_sel_hi:[0,0,0]
	s_waitcnt lgkmcnt(0)
	v_mfma_scale_f32_16x16x128_f8f6f4 v[152:155], v[0:7], v[46:53], v[152:155], v213, v213 op_sel_hi:[0,0,0]
	v_mfma_scale_f32_16x16x128_f8f6f4 v[148:151], v[8:15], v[54:61], v[148:151], v213, v213 op_sel_hi:[0,0,0]
	v_mfma_scale_f32_16x16x128_f8f6f4 v[144:147], v[0:7], v[54:61], v[144:147], v213, v213 op_sel_hi:[0,0,0]
	v_mfma_scale_f32_16x16x128_f8f6f4 v[140:143], v[8:15], v[192:199], v[140:143], v213, v213 op_sel_hi:[0,0,0]
	v_mfma_scale_f32_16x16x128_f8f6f4 v[136:139], v[0:7], v[192:199], v[136:139], v213, v213 op_sel_hi:[0,0,0]
	v_mfma_scale_f32_16x16x128_f8f6f4 v[132:135], v[8:15], v[220:227], v[132:135], v213, v213 op_sel_hi:[0,0,0]
	v_mfma_scale_f32_16x16x128_f8f6f4 v[128:131], v[0:7], v[220:227], v[128:131], v213, v213 op_sel_hi:[0,0,0]
	s_setprio 0
	s_barrier
	ds_read_b128 v[46:49], v216 offset:0xc000
	ds_read_b128 v[50:53], v216 offset:0xc400
	ds_read_b128 v[54:57], v216 offset:0xc800
	ds_read_b128 v[58:61], v216 offset:0xcc00
	ds_read_b128 v[192:195], v216 offset:0xd000
	ds_read_b128 v[196:199], v216 offset:0xd400
	ds_read_b128 v[220:223], v216 offset:0xd800
	ds_read_b128 v[224:227], v216 offset:0xdc00
	s_mov_b32 m0, s80
	s_nop 0
	buffer_load_dwordx4 v215, s[8:11], s17 offen lds
	s_add_i32 s17, s16, 0x80080
	s_mov_b32 m0, s81
	s_add_i32 s65, s65, 0x40080
	buffer_load_dwordx4 v215, s[8:11], s17 offen lds
	s_add_i32 s17, s16, 0x8080
	s_mov_b32 m0, s84
	s_add_i32 s16, s16, 0x88080
	buffer_load_dwordx4 v215, s[8:11], s17 offen lds
	s_mov_b32 m0, s85
	s_nop 0
	buffer_load_dwordx4 v215, s[8:11], s16 offen lds
	s_mov_b32 m0, s82
	s_nop 0
	buffer_load_dwordx4 v214, s[12:15], s3 offen lds
	s_mov_b32 m0, s83
	s_nop 0
	buffer_load_dwordx4 v214, s[12:15], s65 offen lds
	s_waitcnt vmcnt(8)
	s_waitcnt lgkmcnt(0)
	s_barrier
	s_setprio 1
	v_mfma_scale_f32_16x16x128_f8f6f4 v[124:127], v[16:23], v[46:53], v[124:127], v213, v213 op_sel_hi:[0,0,0]
	v_mfma_scale_f32_16x16x128_f8f6f4 v[120:123], v[24:31], v[46:53], v[120:123], v213, v213 op_sel_hi:[0,0,0]
	v_mfma_scale_f32_16x16x128_f8f6f4 v[116:119], v[16:23], v[54:61], v[116:119], v213, v213 op_sel_hi:[0,0,0]
	v_mfma_scale_f32_16x16x128_f8f6f4 v[112:115], v[24:31], v[54:61], v[112:115], v213, v213 op_sel_hi:[0,0,0]
	v_mfma_scale_f32_16x16x128_f8f6f4 v[108:111], v[16:23], v[192:199], v[108:111], v213, v213 op_sel_hi:[0,0,0]
	v_mfma_scale_f32_16x16x128_f8f6f4 v[104:107], v[24:31], v[192:199], v[104:107], v213, v213 op_sel_hi:[0,0,0]
	v_mfma_scale_f32_16x16x128_f8f6f4 v[100:103], v[16:23], v[220:227], v[100:103], v213, v213 op_sel_hi:[0,0,0]
	v_mfma_scale_f32_16x16x128_f8f6f4 v[96:99], v[24:31], v[220:227], v[96:99], v213, v213 op_sel_hi:[0,0,0]
	s_setprio 0
	s_setprio 1
	v_mfma_scale_f32_16x16x128_f8f6f4 v[92:95], v[8:15], v[46:53], v[92:95], v213, v213 op_sel_hi:[0,0,0]
	v_mfma_scale_f32_16x16x128_f8f6f4 v[88:91], v[0:7], v[46:53], v[88:91], v213, v213 op_sel_hi:[0,0,0]
	v_mfma_scale_f32_16x16x128_f8f6f4 v[84:87], v[8:15], v[54:61], v[84:87], v213, v213 op_sel_hi:[0,0,0]
	v_mfma_scale_f32_16x16x128_f8f6f4 v[80:83], v[0:7], v[54:61], v[80:83], v213, v213 op_sel_hi:[0,0,0]
	v_mfma_scale_f32_16x16x128_f8f6f4 v[76:79], v[8:15], v[192:199], v[76:79], v213, v213 op_sel_hi:[0,0,0]
	v_mfma_scale_f32_16x16x128_f8f6f4 v[72:75], v[0:7], v[192:199], v[72:75], v213, v213 op_sel_hi:[0,0,0]
	v_mfma_scale_f32_16x16x128_f8f6f4 v[68:71], v[8:15], v[220:227], v[68:71], v213, v213 op_sel_hi:[0,0,0]
	v_mfma_scale_f32_16x16x128_f8f6f4 v[64:67], v[0:7], v[220:227], v[64:67], v213, v213 op_sel_hi:[0,0,0]
	s_setprio 0
	s_barrier
	s_bitcmp0_b32 s64, 0
	s_waitcnt vmcnt(15)
	v_mul_f32_e32 v0, 0x42800000, v32
	s_waitcnt vmcnt(14)
	v_mul_f32_e32 v4, 0x42800000, v36
	v_mul_f32_e32 v1, 0x42800000, v33
	v_mul_f32_e32 v5, 0x42800000, v37
	v_mul_f32_e32 v2, 0x42800000, v34
	v_mul_f32_e32 v6, 0x42800000, v38
	v_mul_f32_e32 v3, 0x42800000, v35
	v_mul_f32_e32 v7, 0x42800000, v39
	s_mov_b64 s[64:65], -1
	s_cbranch_scc0 .LBB0_929
	s_andn2_b64 vcc, exec, s[64:65]
	s_cbranch_vccnz .LBB0_925
	s_branch .LBB0_930

.LBB0_1228:
	s_add_i32 s28, s61, 0x180
	s_add_i32 s29, s60, 0x180
	s_waitcnt lgkmcnt(0)
	s_barrier
	s_setprio 1
	v_mfma_scale_f32_16x16x128_f8f6f4 v[128:131], v[24:31], v[56:63], 0, v201, v201 op_sel_hi:[0,0,0]
	v_mfma_scale_f32_16x16x128_f8f6f4 v[124:127], v[16:23], v[56:63], 0, v201, v201 op_sel_hi:[0,0,0]
	v_mfma_scale_f32_16x16x128_f8f6f4 v[120:123], v[24:31], v[48:55], 0, v201, v201 op_sel_hi:[0,0,0]
	v_mfma_scale_f32_16x16x128_f8f6f4 v[116:119], v[16:23], v[48:55], 0, v201, v201 op_sel_hi:[0,0,0]
	v_mfma_scale_f32_16x16x128_f8f6f4 v[112:115], v[24:31], v[40:47], 0, v201, v201 op_sel_hi:[0,0,0]
	v_mfma_scale_f32_16x16x128_f8f6f4 v[108:111], v[16:23], v[40:47], 0, v201, v201 op_sel_hi:[0,0,0]
	v_mfma_scale_f32_16x16x128_f8f6f4 v[104:107], v[24:31], v[32:39], 0, v201, v201 op_sel_hi:[0,0,0]
	v_mfma_scale_f32_16x16x128_f8f6f4 v[100:103], v[16:23], v[32:39], 0, v201, v201 op_sel_hi:[0,0,0]
	s_setprio 0
	s_setprio 1
	v_mfma_scale_f32_16x16x128_f8f6f4 v[96:99], v[8:15], v[56:63], 0, v201, v201 op_sel_hi:[0,0,0]
	v_mfma_scale_f32_16x16x128_f8f6f4 v[92:95], v[0:7], v[56:63], 0, v201, v201 op_sel_hi:[0,0,0]
	v_mfma_scale_f32_16x16x128_f8f6f4 v[88:91], v[8:15], v[48:55], 0, v201, v201 op_sel_hi:[0,0,0]
	v_mfma_scale_f32_16x16x128_f8f6f4 v[84:87], v[0:7], v[48:55], 0, v201, v201 op_sel_hi:[0,0,0]
	v_mfma_scale_f32_16x16x128_f8f6f4 v[80:83], v[8:15], v[40:47], 0, v201, v201 op_sel_hi:[0,0,0]
	v_mfma_scale_f32_16x16x128_f8f6f4 v[76:79], v[0:7], v[40:47], 0, v201, v201 op_sel_hi:[0,0,0]
	v_mfma_scale_f32_16x16x128_f8f6f4 v[72:75], v[8:15], v[32:39], 0, v201, v201 op_sel_hi:[0,0,0]
	v_mfma_scale_f32_16x16x128_f8f6f4 v[68:71], v[0:7], v[32:39], 0, v201, v201 op_sel_hi:[0,0,0]
	s_setprio 0
	s_barrier
	ds_read_b128 v[24:27], v205 offset:0x8000
	ds_read_b128 v[28:31], v205 offset:0x8400
	ds_read_b128 v[16:19], v205 offset:0x8800
	ds_read_b128 v[20:23], v205 offset:0x8c00
	ds_read_b128 v[32:35], v204 offset:0x8000
	ds_read_b128 v[36:39], v204 offset:0x8400
	ds_read_b128 v[40:43], v204 offset:0x8800
	ds_read_b128 v[44:47], v204 offset:0x8c00
	ds_read_b128 v[48:51], v204 offset:0x9000
	ds_read_b128 v[52:55], v204 offset:0x9400
	ds_read_b128 v[56:59], v204 offset:0x9800
	ds_read_b128 v[60:63], v204 offset:0x9c00
	ds_read_b128 v[8:11], v205 offset:0xc000
	ds_read_b128 v[12:15], v205 offset:0xc400
	ds_read_b128 v[0:3], v205 offset:0xc800
	ds_read_b128 v[4:7], v205 offset:0xcc00
	s_mov_b32 m0, s44
	s_nop 0
	buffer_load_dwordx4 v216, s[4:7], s33 offen lds
	s_mov_b32 m0, s45
	s_nop 0
	buffer_load_dwordx4 v215, s[4:7], s33 offen lds
	s_waitcnt vmcnt(8)
	s_waitcnt lgkmcnt(4)
	s_barrier
	s_setprio 1
	v_mfma_scale_f32_16x16x128_f8f6f4 v[192:195], v[24:31], v[32:39], v[192:195], v201, v201 op_sel_hi:[0,0,0]
	v_mfma_scale_f32_16x16x128_f8f6f4 v[188:191], v[16:23], v[32:39], v[188:191], v201, v201 op_sel_hi:[0,0,0]
	v_mfma_scale_f32_16x16x128_f8f6f4 v[184:187], v[24:31], v[40:47], v[184:187], v201, v201 op_sel_hi:[0,0,0]
	v_mfma_scale_f32_16x16x128_f8f6f4 v[180:183], v[16:23], v[40:47], v[180:183], v201, v201 op_sel_hi:[0,0,0]
	v_mfma_scale_f32_16x16x128_f8f6f4 v[176:179], v[24:31], v[48:55], v[176:179], v201, v201 op_sel_hi:[0,0,0]
	v_mfma_scale_f32_16x16x128_f8f6f4 v[172:175], v[16:23], v[48:55], v[172:175], v201, v201 op_sel_hi:[0,0,0]
	v_mfma_scale_f32_16x16x128_f8f6f4 v[168:171], v[24:31], v[56:63], v[168:171], v201, v201 op_sel_hi:[0,0,0]
	v_mfma_scale_f32_16x16x128_f8f6f4 v[164:167], v[16:23], v[56:63], v[164:167], v201, v201 op_sel_hi:[0,0,0]
	s_setprio 0
	s_setprio 1
	s_waitcnt lgkmcnt(2)
	v_mfma_scale_f32_16x16x128_f8f6f4 v[160:163], v[8:15], v[32:39], v[160:163], v201, v201 op_sel_hi:[0,0,0]
	s_waitcnt lgkmcnt(0)
	v_mfma_scale_f32_16x16x128_f8f6f4 v[156:159], v[0:7], v[32:39], v[156:159], v201, v201 op_sel_hi:[0,0,0]
	v_mfma_scale_f32_16x16x128_f8f6f4 v[152:155], v[8:15], v[40:47], v[152:155], v201, v201 op_sel_hi:[0,0,0]
	v_mfma_scale_f32_16x16x128_f8f6f4 v[148:151], v[0:7], v[40:47], v[148:151], v201, v201 op_sel_hi:[0,0,0]
	v_mfma_scale_f32_16x16x128_f8f6f4 v[144:147], v[8:15], v[48:55], v[144:147], v201, v201 op_sel_hi:[0,0,0]
	v_mfma_scale_f32_16x16x128_f8f6f4 v[140:143], v[0:7], v[48:55], v[140:143], v201, v201 op_sel_hi:[0,0,0]
	v_mfma_scale_f32_16x16x128_f8f6f4 v[136:139], v[8:15], v[56:63], v[136:139], v201, v201 op_sel_hi:[0,0,0]
	v_mfma_scale_f32_16x16x128_f8f6f4 v[132:135], v[0:7], v[56:63], v[132:135], v201, v201 op_sel_hi:[0,0,0]
	s_setprio 0
	s_barrier
	ds_read_b128 v[32:35], v204 offset:0xc000
	ds_read_b128 v[36:39], v204 offset:0xc400
	ds_read_b128 v[40:43], v204 offset:0xc800
	ds_read_b128 v[44:47], v204 offset:0xcc00
	ds_read_b128 v[48:51], v204 offset:0xd000
	ds_read_b128 v[52:55], v204 offset:0xd400
	ds_read_b128 v[56:59], v204 offset:0xd800
	ds_read_b128 v[60:63], v204 offset:0xdc00
	s_mov_b32 m0, s48
	s_mov_b32 s10, s6
	s_mov_b32 s11, s7
	buffer_load_dwordx4 v203, s[8:11], s29 offen lds
	s_add_i32 s29, s60, 0x80180
	s_mov_b32 m0, s49
	s_nop 0
	buffer_load_dwordx4 v203, s[8:11], s29 offen lds
	s_add_i32 s29, s60, 0x8180
	s_mov_b32 m0, s62
	s_nop 0
	buffer_load_dwordx4 v203, s[8:11], s29 offen lds
	s_add_i32 s29, s60, 0x88180
	s_mov_b32 m0, s63
	s_nop 0
	buffer_load_dwordx4 v203, s[8:11], s29 offen lds
	s_mov_b32 m0, s50
	s_nop 0
	buffer_load_dwordx4 v214, s[4:7], s28 offen lds
	s_mov_b32 m0, s51
	s_nop 0
	buffer_load_dwordx4 v217, s[4:7], s28 offen lds
	s_waitcnt vmcnt(8)
	s_waitcnt lgkmcnt(0)
	s_barrier
	s_setprio 1
	v_mfma_scale_f32_16x16x128_f8f6f4 v[128:131], v[24:31], v[32:39], v[128:131], v201, v201 op_sel_hi:[0,0,0]
	v_mfma_scale_f32_16x16x128_f8f6f4 v[124:127], v[16:23], v[32:39], v[124:127], v201, v201 op_sel_hi:[0,0,0]
	v_mfma_scale_f32_16x16x128_f8f6f4 v[120:123], v[24:31], v[40:47], v[120:123], v201, v201 op_sel_hi:[0,0,0]
	v_mfma_scale_f32_16x16x128_f8f6f4 v[116:119], v[16:23], v[40:47], v[116:119], v201, v201 op_sel_hi:[0,0,0]
	v_mfma_scale_f32_16x16x128_f8f6f4 v[112:115], v[24:31], v[48:55], v[112:115], v201, v201 op_sel_hi:[0,0,0]
	v_mfma_scale_f32_16x16x128_f8f6f4 v[108:111], v[16:23], v[48:55], v[108:111], v201, v201 op_sel_hi:[0,0,0]
	v_mfma_scale_f32_16x16x128_f8f6f4 v[104:107], v[24:31], v[56:63], v[104:107], v201, v201 op_sel_hi:[0,0,0]
	v_mfma_scale_f32_16x16x128_f8f6f4 v[100:103], v[16:23], v[56:63], v[100:103], v201, v201 op_sel_hi:[0,0,0]
	s_setprio 0
	s_setprio 1
	v_mfma_scale_f32_16x16x128_f8f6f4 v[96:99], v[8:15], v[32:39], v[96:99], v201, v201 op_sel_hi:[0,0,0]
	v_mfma_scale_f32_16x16x128_f8f6f4 v[92:95], v[0:7], v[32:39], v[92:95], v201, v201 op_sel_hi:[0,0,0]
	v_mfma_scale_f32_16x16x128_f8f6f4 v[88:91], v[8:15], v[40:47], v[88:91], v201, v201 op_sel_hi:[0,0,0]
	v_mfma_scale_f32_16x16x128_f8f6f4 v[84:87], v[0:7], v[40:47], v[84:87], v201, v201 op_sel_hi:[0,0,0]
	v_mfma_scale_f32_16x16x128_f8f6f4 v[80:83], v[8:15], v[48:55], v[80:83], v201, v201 op_sel_hi:[0,0,0]
	v_mfma_scale_f32_16x16x128_f8f6f4 v[76:79], v[0:7], v[48:55], v[76:79], v201, v201 op_sel_hi:[0,0,0]
	v_mfma_scale_f32_16x16x128_f8f6f4 v[72:75], v[8:15], v[56:63], v[72:75], v201, v201 op_sel_hi:[0,0,0]
	v_mfma_scale_f32_16x16x128_f8f6f4 v[68:71], v[0:7], v[56:63], v[68:71], v201, v201 op_sel_hi:[0,0,0]
	s_setprio 0
	s_barrier
	s_waitcnt vmcnt(16)
	v_mbcnt_lo_u32_b32 v0, -1, 0
	v_mbcnt_hi_u32_b32 v0, -1, v0
	s_add_i32 s29, s60, 0x200
	v_lshl_add_u32 v0, v0, 4, s37
	v_ashrrev_i32_e32 v1, 31, v0
	v_lshrrev_b32_e32 v1, 22, v1
	v_add_u32_e32 v1, v0, v1
	v_ashrrev_i32_e32 v1, 10, v1
	v_mul_i32_i24_e32 v2, 0x400, v1
	v_sub_u32_e32 v2, v0, v2
	v_lshrrev_b32_e32 v3, 4, v2
	v_bitop3_b32 v3, v3, v2, 32 bitop3:0x6c
	v_ashrrev_i32_e32 v2, 31, v2
	v_lshrrev_b32_e32 v2, 26, v2
	v_add_u32_e32 v2, v3, v2
	v_and_b32_e32 v2, 0xc0, v2
	v_add_u32_e32 v0, 0x2000, v0
	v_sub_u32_e32 v2, v3, v2
	v_ashrrev_i32_e32 v3, 31, v0
	v_lshrrev_b32_e32 v3, 22, v3
	v_add_u32_e32 v3, v0, v3
	v_ashrrev_i32_e32 v3, 10, v3
	v_mul_i32_i24_e32 v4, 0x400, v3
	v_sub_u32_e32 v0, v0, v4
	v_lshrrev_b32_e32 v4, 4, v0
	v_bitop3_b32 v4, v4, v0, 32 bitop3:0x6c
	v_ashrrev_i32_e32 v0, 31, v0
	v_lshrrev_b32_e32 v0, 26, v0
	v_add_u32_e32 v0, v4, v0
	v_and_b32_e32 v0, 0xffc0, v0
	v_sub_u32_e32 v0, v4, v0
	v_lshrrev_b16_e32 v4, 7, v0
	v_and_b32_e32 v4, 1, v4
	v_add_u16_e32 v0, v0, v4
	v_lshlrev_b32_e32 v1, 5, v1
	v_ashrrev_i16_sdwa v2, v202, sext(v2) dst_sel:DWORD dst_unused:UNUSED_PAD src0_sel:DWORD src1_sel:BYTE_0
	v_lshlrev_b32_e32 v3, 5, v3
	v_ashrrev_i16_sdwa v0, v202, sext(v0) dst_sel:DWORD dst_unused:UNUSED_PAD src0_sel:DWORD src1_sel:BYTE_0
	v_and_b32_e32 v1, 32, v1
	v_bfe_i32 v2, v2, 0, 16
	v_and_b32_e32 v3, 32, v3
	v_bfe_i32 v0, v0, 0, 16
	v_add_lshl_u32 v1, v1, v2, 1
	v_add_lshl_u32 v0, v3, v0, 1
	v_lshl_add_u32 v32, v231, 12, v1
	v_lshl_add_u32 v33, v228, 12, v0
	v_lshl_add_u32 v34, v229, 12, v1
	v_lshl_add_u32 v35, v230, 12, v0
	s_mov_b32 s33, 0
.LBB0_1229:
	s_add_i32 s66, s28, 0x80
	s_cmp_eq_u32 s33, 28
	s_cselect_b64 vcc, -1, 0
	ds_read_b128 v[16:19], v205 offset:0
	ds_read_b128 v[20:23], v205 offset:0x400
	ds_read_b128 v[24:27], v205 offset:0x800
	ds_read_b128 v[28:31], v205 offset:0xc00
	ds_read_b128 v[36:39], v204 offset:0
	ds_read_b128 v[40:43], v204 offset:0x400
	ds_read_b128 v[44:47], v204 offset:0x800
	ds_read_b128 v[48:51], v204 offset:0xc00
	ds_read_b128 v[52:55], v204 offset:0x1000
	ds_read_b128 v[56:59], v204 offset:0x1400
	ds_read_b128 v[228:231], v204 offset:0x1800
	ds_read_b128 v[232:235], v204 offset:0x1c00
	ds_read_b128 v[8:11], v205 offset:0x4000
	ds_read_b128 v[12:15], v205 offset:0x4400
	ds_read_b128 v[0:3], v205 offset:0x4800
	ds_read_b128 v[4:7], v205 offset:0x4c00
	s_and_b64 s[60:61], vcc, exec
	s_cselect_b32 s66, s72, s66
	s_cselect_b32 s61, s73, s29
	s_add_i32 s60, s66, 0x80
	s_mov_b32 m0, s65
	s_nop 0
	buffer_load_dwordx4 v216, s[4:7], s28 offen lds
	s_mov_b32 m0, s68
	s_nop 0
	buffer_load_dwordx4 v215, s[4:7], s28 offen lds
	s_waitcnt vmcnt(8)
	s_waitcnt lgkmcnt(4)
	s_barrier
	s_setprio 1
	v_mfma_scale_f32_16x16x128_f8f6f4 v[192:195], v[16:23], v[36:43], v[192:195], v201, v201 op_sel_hi:[0,0,0]
	v_mfma_scale_f32_16x16x128_f8f6f4 v[188:191], v[24:31], v[36:43], v[188:191], v201, v201 op_sel_hi:[0,0,0]
	v_mfma_scale_f32_16x16x128_f8f6f4 v[184:187], v[16:23], v[44:51], v[184:187], v201, v201 op_sel_hi:[0,0,0]
	v_mfma_scale_f32_16x16x128_f8f6f4 v[180:183], v[24:31], v[44:51], v[180:183], v201, v201 op_sel_hi:[0,0,0]
	v_mfma_scale_f32_16x16x128_f8f6f4 v[176:179], v[16:23], v[52:59], v[176:179], v201, v201 op_sel_hi:[0,0,0]
	v_mfma_scale_f32_16x16x128_f8f6f4 v[172:175], v[24:31], v[52:59], v[172:175], v201, v201 op_sel_hi:[0,0,0]
	v_mfma_scale_f32_16x16x128_f8f6f4 v[168:171], v[16:23], v[228:235], v[168:171], v201, v201 op_sel_hi:[0,0,0]
	v_mfma_scale_f32_16x16x128_f8f6f4 v[164:167], v[24:31], v[228:235], v[164:167], v201, v201 op_sel_hi:[0,0,0]
	s_setprio 0
	s_setprio 1
	s_waitcnt lgkmcnt(2)
	v_mfma_scale_f32_16x16x128_f8f6f4 v[160:163], v[8:15], v[36:43], v[160:163], v201, v201 op_sel_hi:[0,0,0]
	s_waitcnt lgkmcnt(0)
	v_mfma_scale_f32_16x16x128_f8f6f4 v[156:159], v[0:7], v[36:43], v[156:159], v201, v201 op_sel_hi:[0,0,0]
	v_mfma_scale_f32_16x16x128_f8f6f4 v[152:155], v[8:15], v[44:51], v[152:155], v201, v201 op_sel_hi:[0,0,0]
	v_mfma_scale_f32_16x16x128_f8f6f4 v[148:151], v[0:7], v[44:51], v[148:151], v201, v201 op_sel_hi:[0,0,0]
	v_mfma_scale_f32_16x16x128_f8f6f4 v[144:147], v[8:15], v[52:59], v[144:147], v201, v201 op_sel_hi:[0,0,0]
	v_mfma_scale_f32_16x16x128_f8f6f4 v[140:143], v[0:7], v[52:59], v[140:143], v201, v201 op_sel_hi:[0,0,0]
	v_mfma_scale_f32_16x16x128_f8f6f4 v[136:139], v[8:15], v[228:235], v[136:139], v201, v201 op_sel_hi:[0,0,0]
	v_mfma_scale_f32_16x16x128_f8f6f4 v[132:135], v[0:7], v[228:235], v[132:135], v201, v201 op_sel_hi:[0,0,0]
	s_setprio 0
	s_barrier
	ds_read_b128 v[36:39], v204 offset:0x4000
	ds_read_b128 v[40:43], v204 offset:0x4400
	ds_read_b128 v[44:47], v204 offset:0x4800
	ds_read_b128 v[48:51], v204 offset:0x4c00
	ds_read_b128 v[52:55], v204 offset:0x5000
	ds_read_b128 v[56:59], v204 offset:0x5400
	ds_read_b128 v[228:231], v204 offset:0x5800
	ds_read_b128 v[232:235], v204 offset:0x5c00
	s_mov_b32 m0, s39
	s_nop 0
	buffer_load_dwordx4 v203, s[8:11], s61 offen lds
	s_add_i32 s67, s61, 0x80000
	s_mov_b32 m0, s40
	v_cndmask_b32_e32 v60, v214, v32, vcc
	buffer_load_dwordx4 v203, s[8:11], s67 offen lds
	s_add_i32 s67, s61, 0x8000
	s_mov_b32 m0, s41
	v_cndmask_b32_e32 v61, v217, v33, vcc
	buffer_load_dwordx4 v203, s[8:11], s67 offen lds
	s_add_i32 s67, s61, 0x88000
	s_mov_b32 m0, s42
	s_nop 0
	buffer_load_dwordx4 v203, s[8:11], s67 offen lds
	s_mov_b32 m0, s38
	s_nop 0
	buffer_load_dwordx4 v60, s[4:7], s66 offen lds
	s_mov_b32 m0, s43
	s_nop 0
	buffer_load_dwordx4 v61, s[4:7], s66 offen lds
	s_waitcnt vmcnt(8)
	s_waitcnt lgkmcnt(0)
	s_barrier
	s_setprio 1
	v_mfma_scale_f32_16x16x128_f8f6f4 v[128:131], v[16:23], v[36:43], v[128:131], v201, v201 op_sel_hi:[0,0,0]
	v_mfma_scale_f32_16x16x128_f8f6f4 v[124:127], v[24:31], v[36:43], v[124:127], v201, v201 op_sel_hi:[0,0,0]
	v_mfma_scale_f32_16x16x128_f8f6f4 v[120:123], v[16:23], v[44:51], v[120:123], v201, v201 op_sel_hi:[0,0,0]
	v_mfma_scale_f32_16x16x128_f8f6f4 v[116:119], v[24:31], v[44:51], v[116:119], v201, v201 op_sel_hi:[0,0,0]
	v_mfma_scale_f32_16x16x128_f8f6f4 v[112:115], v[16:23], v[52:59], v[112:115], v201, v201 op_sel_hi:[0,0,0]
	v_mfma_scale_f32_16x16x128_f8f6f4 v[108:111], v[24:31], v[52:59], v[108:111], v201, v201 op_sel_hi:[0,0,0]
	v_mfma_scale_f32_16x16x128_f8f6f4 v[104:107], v[16:23], v[228:235], v[104:107], v201, v201 op_sel_hi:[0,0,0]
	v_mfma_scale_f32_16x16x128_f8f6f4 v[100:103], v[24:31], v[228:235], v[100:103], v201, v201 op_sel_hi:[0,0,0]
	s_setprio 0
	s_setprio 1
	v_mfma_scale_f32_16x16x128_f8f6f4 v[96:99], v[8:15], v[36:43], v[96:99], v201, v201 op_sel_hi:[0,0,0]
	v_mfma_scale_f32_16x16x128_f8f6f4 v[92:95], v[0:7], v[36:43], v[92:95], v201, v201 op_sel_hi:[0,0,0]
	v_mfma_scale_f32_16x16x128_f8f6f4 v[88:91], v[8:15], v[44:51], v[88:91], v201, v201 op_sel_hi:[0,0,0]
	v_mfma_scale_f32_16x16x128_f8f6f4 v[84:87], v[0:7], v[44:51], v[84:87], v201, v201 op_sel_hi:[0,0,0]
	v_mfma_scale_f32_16x16x128_f8f6f4 v[80:83], v[8:15], v[52:59], v[80:83], v201, v201 op_sel_hi:[0,0,0]
	v_mfma_scale_f32_16x16x128_f8f6f4 v[76:79], v[0:7], v[52:59], v[76:79], v201, v201 op_sel_hi:[0,0,0]
	v_mfma_scale_f32_16x16x128_f8f6f4 v[72:75], v[8:15], v[228:235], v[72:75], v201, v201 op_sel_hi:[0,0,0]
	v_mfma_scale_f32_16x16x128_f8f6f4 v[68:71], v[0:7], v[228:235], v[68:71], v201, v201 op_sel_hi:[0,0,0]
	s_setprio 0
	s_barrier
	ds_read_b128 v[24:27], v205 offset:0x8000
	ds_read_b128 v[28:31], v205 offset:0x8400
	ds_read_b128 v[16:19], v205 offset:0x8800
	ds_read_b128 v[20:23], v205 offset:0x8c00
	ds_read_b128 v[36:39], v204 offset:0x8000
	ds_read_b128 v[40:43], v204 offset:0x8400
	ds_read_b128 v[44:47], v204 offset:0x8800
	ds_read_b128 v[48:51], v204 offset:0x8c00
	ds_read_b128 v[52:55], v204 offset:0x9000
	ds_read_b128 v[56:59], v204 offset:0x9400
	ds_read_b128 v[228:231], v204 offset:0x9800
	ds_read_b128 v[232:235], v204 offset:0x9c00
	ds_read_b128 v[8:11], v205 offset:0xc000
	ds_read_b128 v[12:15], v205 offset:0xc400
	ds_read_b128 v[0:3], v205 offset:0xc800
	ds_read_b128 v[4:7], v205 offset:0xcc00
	s_mov_b32 m0, s44
	v_cndmask_b32_e32 v62, v216, v34, vcc
	buffer_load_dwordx4 v62, s[4:7], s66 offen lds
	v_cndmask_b32_e32 v62, v215, v35, vcc
	s_mov_b32 m0, s45
	s_nop 0
	buffer_load_dwordx4 v62, s[4:7], s66 offen lds
	s_waitcnt vmcnt(8)
	s_waitcnt lgkmcnt(4)
	s_barrier
	s_setprio 1
	v_mfma_scale_f32_16x16x128_f8f6f4 v[192:195], v[24:31], v[36:43], v[192:195], v201, v201 op_sel_hi:[0,0,0]
	v_mfma_scale_f32_16x16x128_f8f6f4 v[188:191], v[16:23], v[36:43], v[188:191], v201, v201 op_sel_hi:[0,0,0]
	v_mfma_scale_f32_16x16x128_f8f6f4 v[184:187], v[24:31], v[44:51], v[184:187], v201, v201 op_sel_hi:[0,0,0]
	v_mfma_scale_f32_16x16x128_f8f6f4 v[180:183], v[16:23], v[44:51], v[180:183], v201, v201 op_sel_hi:[0,0,0]
	v_mfma_scale_f32_16x16x128_f8f6f4 v[176:179], v[24:31], v[52:59], v[176:179], v201, v201 op_sel_hi:[0,0,0]
	v_mfma_scale_f32_16x16x128_f8f6f4 v[172:175], v[16:23], v[52:59], v[172:175], v201, v201 op_sel_hi:[0,0,0]
	v_mfma_scale_f32_16x16x128_f8f6f4 v[168:171], v[24:31], v[228:235], v[168:171], v201, v201 op_sel_hi:[0,0,0]
	v_mfma_scale_f32_16x16x128_f8f6f4 v[164:167], v[16:23], v[228:235], v[164:167], v201, v201 op_sel_hi:[0,0,0]
	s_setprio 0
	s_setprio 1
	s_waitcnt lgkmcnt(2)
	v_mfma_scale_f32_16x16x128_f8f6f4 v[160:163], v[8:15], v[36:43], v[160:163], v201, v201 op_sel_hi:[0,0,0]
	s_waitcnt lgkmcnt(0)
	v_mfma_scale_f32_16x16x128_f8f6f4 v[156:159], v[0:7], v[36:43], v[156:159], v201, v201 op_sel_hi:[0,0,0]
	v_mfma_scale_f32_16x16x128_f8f6f4 v[152:155], v[8:15], v[44:51], v[152:155], v201, v201 op_sel_hi:[0,0,0]
	v_mfma_scale_f32_16x16x128_f8f6f4 v[148:151], v[0:7], v[44:51], v[148:151], v201, v201 op_sel_hi:[0,0,0]
	v_mfma_scale_f32_16x16x128_f8f6f4 v[144:147], v[8:15], v[52:59], v[144:147], v201, v201 op_sel_hi:[0,0,0]
	v_mfma_scale_f32_16x16x128_f8f6f4 v[140:143], v[0:7], v[52:59], v[140:143], v201, v201 op_sel_hi:[0,0,0]
	v_mfma_scale_f32_16x16x128_f8f6f4 v[136:139], v[8:15], v[228:235], v[136:139], v201, v201 op_sel_hi:[0,0,0]
	v_mfma_scale_f32_16x16x128_f8f6f4 v[132:135], v[0:7], v[228:235], v[132:135], v201, v201 op_sel_hi:[0,0,0]
	s_setprio 0
	s_barrier
	ds_read_b128 v[36:39], v204 offset:0xc000
	ds_read_b128 v[40:43], v204 offset:0xc400
	ds_read_b128 v[44:47], v204 offset:0xc800
	ds_read_b128 v[48:51], v204 offset:0xcc00
	ds_read_b128 v[52:55], v204 offset:0xd000
	ds_read_b128 v[56:59], v204 offset:0xd400
	ds_read_b128 v[228:231], v204 offset:0xd800
	ds_read_b128 v[232:235], v204 offset:0xdc00
	s_mov_b32 m0, s48
	s_add_i32 s66, s61, 0x80
	buffer_load_dwordx4 v203, s[8:11], s66 offen lds
	s_add_i32 s66, s61, 0x80080
	s_mov_b32 m0, s49
	s_nop 0
	buffer_load_dwordx4 v203, s[8:11], s66 offen lds
	s_add_i32 s66, s61, 0x8080
	s_mov_b32 m0, s62
	s_add_i32 s61, s61, 0x88080
	buffer_load_dwordx4 v203, s[8:11], s66 offen lds
	s_mov_b32 m0, s63
	s_nop 0
	buffer_load_dwordx4 v203, s[8:11], s61 offen lds
	s_mov_b32 m0, s50
	s_nop 0
	buffer_load_dwordx4 v60, s[4:7], s60 offen lds
	s_mov_b32 m0, s51
	s_nop 0
	buffer_load_dwordx4 v61, s[4:7], s60 offen lds
	s_waitcnt vmcnt(8)
	s_waitcnt lgkmcnt(0)
	s_barrier
	s_setprio 1
	v_mfma_scale_f32_16x16x128_f8f6f4 v[128:131], v[24:31], v[36:43], v[128:131], v201, v201 op_sel_hi:[0,0,0]
	v_mfma_scale_f32_16x16x128_f8f6f4 v[124:127], v[16:23], v[36:43], v[124:127], v201, v201 op_sel_hi:[0,0,0]
	v_mfma_scale_f32_16x16x128_f8f6f4 v[120:123], v[24:31], v[44:51], v[120:123], v201, v201 op_sel_hi:[0,0,0]
	v_mfma_scale_f32_16x16x128_f8f6f4 v[116:119], v[16:23], v[44:51], v[116:119], v201, v201 op_sel_hi:[0,0,0]
	v_mfma_scale_f32_16x16x128_f8f6f4 v[112:115], v[24:31], v[52:59], v[112:115], v201, v201 op_sel_hi:[0,0,0]
	v_mfma_scale_f32_16x16x128_f8f6f4 v[108:111], v[16:23], v[52:59], v[108:111], v201, v201 op_sel_hi:[0,0,0]
	v_mfma_scale_f32_16x16x128_f8f6f4 v[104:107], v[24:31], v[228:235], v[104:107], v201, v201 op_sel_hi:[0,0,0]
	v_mfma_scale_f32_16x16x128_f8f6f4 v[100:103], v[16:23], v[228:235], v[100:103], v201, v201 op_sel_hi:[0,0,0]
	s_setprio 0
	s_setprio 1
	v_mfma_scale_f32_16x16x128_f8f6f4 v[96:99], v[8:15], v[36:43], v[96:99], v201, v201 op_sel_hi:[0,0,0]
	v_mfma_scale_f32_16x16x128_f8f6f4 v[92:95], v[0:7], v[36:43], v[92:95], v201, v201 op_sel_hi:[0,0,0]
	v_mfma_scale_f32_16x16x128_f8f6f4 v[88:91], v[8:15], v[44:51], v[88:91], v201, v201 op_sel_hi:[0,0,0]
	v_mfma_scale_f32_16x16x128_f8f6f4 v[84:87], v[0:7], v[44:51], v[84:87], v201, v201 op_sel_hi:[0,0,0]
	v_mfma_scale_f32_16x16x128_f8f6f4 v[80:83], v[8:15], v[52:59], v[80:83], v201, v201 op_sel_hi:[0,0,0]
	v_mfma_scale_f32_16x16x128_f8f6f4 v[76:79], v[0:7], v[52:59], v[76:79], v201, v201 op_sel_hi:[0,0,0]
	v_mfma_scale_f32_16x16x128_f8f6f4 v[72:75], v[8:15], v[228:235], v[72:75], v201, v201 op_sel_hi:[0,0,0]
	v_mfma_scale_f32_16x16x128_f8f6f4 v[68:71], v[0:7], v[228:235], v[68:71], v201, v201 op_sel_hi:[0,0,0]
	s_setprio 0
	s_barrier
	s_add_i32 s33, s33, 2
	s_addk_i32 s28, 0x100
	s_addk_i32 s29, 0x100
	s_cmp_gt_u32 s33, 29
	s_cbranch_scc0 .LBB0_1229
	s_and_b64 vcc, exec, s[18:19]
	s_cbranch_vccz .LBB0_1232
	s_barrier

.LBB0_1329:
	s_add_i32 s36, s89, 0x180
	s_add_i32 s37, s61, 0x180
	s_waitcnt lgkmcnt(0)
	s_barrier
	s_setprio 1
	v_mfma_scale_f32_16x16x128_f8f6f4 v[128:131], v[24:31], v[56:63], 0, v198, v198 op_sel_hi:[0,0,0]
	v_mfma_scale_f32_16x16x128_f8f6f4 v[124:127], v[16:23], v[56:63], 0, v198, v198 op_sel_hi:[0,0,0]
	v_mfma_scale_f32_16x16x128_f8f6f4 v[120:123], v[24:31], v[48:55], 0, v198, v198 op_sel_hi:[0,0,0]
	v_mfma_scale_f32_16x16x128_f8f6f4 v[116:119], v[16:23], v[48:55], 0, v198, v198 op_sel_hi:[0,0,0]
	v_mfma_scale_f32_16x16x128_f8f6f4 v[112:115], v[24:31], v[40:47], 0, v198, v198 op_sel_hi:[0,0,0]
	v_mfma_scale_f32_16x16x128_f8f6f4 v[108:111], v[16:23], v[40:47], 0, v198, v198 op_sel_hi:[0,0,0]
	v_mfma_scale_f32_16x16x128_f8f6f4 v[104:107], v[24:31], v[32:39], 0, v198, v198 op_sel_hi:[0,0,0]
	v_mfma_scale_f32_16x16x128_f8f6f4 v[100:103], v[16:23], v[32:39], 0, v198, v198 op_sel_hi:[0,0,0]
	s_setprio 0
	s_setprio 1
	v_mfma_scale_f32_16x16x128_f8f6f4 v[96:99], v[8:15], v[56:63], 0, v198, v198 op_sel_hi:[0,0,0]
	v_mfma_scale_f32_16x16x128_f8f6f4 v[92:95], v[0:7], v[56:63], 0, v198, v198 op_sel_hi:[0,0,0]
	v_mfma_scale_f32_16x16x128_f8f6f4 v[88:91], v[8:15], v[48:55], 0, v198, v198 op_sel_hi:[0,0,0]
	v_mfma_scale_f32_16x16x128_f8f6f4 v[84:87], v[0:7], v[48:55], 0, v198, v198 op_sel_hi:[0,0,0]
	v_mfma_scale_f32_16x16x128_f8f6f4 v[80:83], v[8:15], v[40:47], 0, v198, v198 op_sel_hi:[0,0,0]
	v_mfma_scale_f32_16x16x128_f8f6f4 v[76:79], v[0:7], v[40:47], 0, v198, v198 op_sel_hi:[0,0,0]
	v_mfma_scale_f32_16x16x128_f8f6f4 v[72:75], v[8:15], v[32:39], 0, v198, v198 op_sel_hi:[0,0,0]
	v_mfma_scale_f32_16x16x128_f8f6f4 v[68:71], v[0:7], v[32:39], 0, v198, v198 op_sel_hi:[0,0,0]
	s_setprio 0
	s_barrier
	ds_read_b128 v[24:27], v202 offset:0x8000
	ds_read_b128 v[28:31], v202 offset:0x8400
	ds_read_b128 v[16:19], v202 offset:0x8800
	ds_read_b128 v[20:23], v202 offset:0x8c00
	ds_read_b128 v[32:35], v201 offset:0x8000
	ds_read_b128 v[36:39], v201 offset:0x8400
	ds_read_b128 v[40:43], v201 offset:0x8800
	ds_read_b128 v[44:47], v201 offset:0x8c00
	ds_read_b128 v[48:51], v201 offset:0x9000
	ds_read_b128 v[52:55], v201 offset:0x9400
	ds_read_b128 v[56:59], v201 offset:0x9800
	ds_read_b128 v[60:63], v201 offset:0x9c00
	ds_read_b128 v[8:11], v202 offset:0xc000
	ds_read_b128 v[12:15], v202 offset:0xc400
	ds_read_b128 v[0:3], v202 offset:0xc800
	ds_read_b128 v[4:7], v202 offset:0xcc00
	s_mov_b32 m0, s50
	s_nop 0
	buffer_load_dwordx4 v207, s[4:7], s33 offen lds
	s_mov_b32 m0, s51
	s_nop 0
	buffer_load_dwordx4 v206, s[4:7], s33 offen lds
	s_waitcnt vmcnt(8)
	s_waitcnt lgkmcnt(4)
	s_barrier
	s_setprio 1
	v_mfma_scale_f32_16x16x128_f8f6f4 v[192:195], v[24:31], v[32:39], v[192:195], v198, v198 op_sel_hi:[0,0,0]
	v_mfma_scale_f32_16x16x128_f8f6f4 v[188:191], v[16:23], v[32:39], v[188:191], v198, v198 op_sel_hi:[0,0,0]
	v_mfma_scale_f32_16x16x128_f8f6f4 v[184:187], v[24:31], v[40:47], v[184:187], v198, v198 op_sel_hi:[0,0,0]
	v_mfma_scale_f32_16x16x128_f8f6f4 v[180:183], v[16:23], v[40:47], v[180:183], v198, v198 op_sel_hi:[0,0,0]
	v_mfma_scale_f32_16x16x128_f8f6f4 v[176:179], v[24:31], v[48:55], v[176:179], v198, v198 op_sel_hi:[0,0,0]
	v_mfma_scale_f32_16x16x128_f8f6f4 v[172:175], v[16:23], v[48:55], v[172:175], v198, v198 op_sel_hi:[0,0,0]
	v_mfma_scale_f32_16x16x128_f8f6f4 v[168:171], v[24:31], v[56:63], v[168:171], v198, v198 op_sel_hi:[0,0,0]
	v_mfma_scale_f32_16x16x128_f8f6f4 v[164:167], v[16:23], v[56:63], v[164:167], v198, v198 op_sel_hi:[0,0,0]
	s_setprio 0
	s_setprio 1
	s_waitcnt lgkmcnt(2)
	v_mfma_scale_f32_16x16x128_f8f6f4 v[160:163], v[8:15], v[32:39], v[160:163], v198, v198 op_sel_hi:[0,0,0]
	s_waitcnt lgkmcnt(0)
	v_mfma_scale_f32_16x16x128_f8f6f4 v[156:159], v[0:7], v[32:39], v[156:159], v198, v198 op_sel_hi:[0,0,0]
	v_mfma_scale_f32_16x16x128_f8f6f4 v[152:155], v[8:15], v[40:47], v[152:155], v198, v198 op_sel_hi:[0,0,0]
	v_mfma_scale_f32_16x16x128_f8f6f4 v[148:151], v[0:7], v[40:47], v[148:151], v198, v198 op_sel_hi:[0,0,0]
	v_mfma_scale_f32_16x16x128_f8f6f4 v[144:147], v[8:15], v[48:55], v[144:147], v198, v198 op_sel_hi:[0,0,0]
	v_mfma_scale_f32_16x16x128_f8f6f4 v[140:143], v[0:7], v[48:55], v[140:143], v198, v198 op_sel_hi:[0,0,0]
	v_mfma_scale_f32_16x16x128_f8f6f4 v[136:139], v[8:15], v[56:63], v[136:139], v198, v198 op_sel_hi:[0,0,0]
	v_mfma_scale_f32_16x16x128_f8f6f4 v[132:135], v[0:7], v[56:63], v[132:135], v198, v198 op_sel_hi:[0,0,0]
	s_setprio 0
	s_barrier
	ds_read_b128 v[32:35], v201 offset:0xc000
	ds_read_b128 v[36:39], v201 offset:0xc400
	ds_read_b128 v[40:43], v201 offset:0xc800
	ds_read_b128 v[44:47], v201 offset:0xcc00
	ds_read_b128 v[48:51], v201 offset:0xd000
	ds_read_b128 v[52:55], v201 offset:0xd400
	ds_read_b128 v[56:59], v201 offset:0xd800
	ds_read_b128 v[60:63], v201 offset:0xdc00
	s_mov_b32 m0, s64
	s_mov_b32 s10, s6
	s_mov_b32 s11, s7
	buffer_load_dwordx4 v200, s[8:11], s37 offen lds
	s_add_i32 s33, s61, 0x80180
	s_mov_b32 m0, s65
	s_nop 0
	buffer_load_dwordx4 v200, s[8:11], s33 offen lds
	s_add_i32 s33, s61, 0x8180
	s_mov_b32 m0, s70
	s_nop 0
	buffer_load_dwordx4 v200, s[8:11], s33 offen lds
	s_add_i32 s33, s61, 0x88180
	s_mov_b32 m0, s71
	s_nop 0
	buffer_load_dwordx4 v200, s[8:11], s33 offen lds
	s_mov_b32 m0, s68
	s_nop 0
	buffer_load_dwordx4 v205, s[4:7], s36 offen lds
	s_mov_b32 m0, s69
	s_nop 0
	buffer_load_dwordx4 v208, s[4:7], s36 offen lds
	s_waitcnt vmcnt(8)
	s_waitcnt lgkmcnt(0)
	s_barrier
	s_setprio 1
	v_mfma_scale_f32_16x16x128_f8f6f4 v[128:131], v[24:31], v[32:39], v[128:131], v198, v198 op_sel_hi:[0,0,0]
	v_mfma_scale_f32_16x16x128_f8f6f4 v[124:127], v[16:23], v[32:39], v[124:127], v198, v198 op_sel_hi:[0,0,0]
	v_mfma_scale_f32_16x16x128_f8f6f4 v[120:123], v[24:31], v[40:47], v[120:123], v198, v198 op_sel_hi:[0,0,0]
	v_mfma_scale_f32_16x16x128_f8f6f4 v[116:119], v[16:23], v[40:47], v[116:119], v198, v198 op_sel_hi:[0,0,0]
	v_mfma_scale_f32_16x16x128_f8f6f4 v[112:115], v[24:31], v[48:55], v[112:115], v198, v198 op_sel_hi:[0,0,0]
	v_mfma_scale_f32_16x16x128_f8f6f4 v[108:111], v[16:23], v[48:55], v[108:111], v198, v198 op_sel_hi:[0,0,0]
	v_mfma_scale_f32_16x16x128_f8f6f4 v[104:107], v[24:31], v[56:63], v[104:107], v198, v198 op_sel_hi:[0,0,0]
	v_mfma_scale_f32_16x16x128_f8f6f4 v[100:103], v[16:23], v[56:63], v[100:103], v198, v198 op_sel_hi:[0,0,0]
	s_setprio 0
	s_setprio 1
	v_mfma_scale_f32_16x16x128_f8f6f4 v[96:99], v[8:15], v[32:39], v[96:99], v198, v198 op_sel_hi:[0,0,0]
	v_mfma_scale_f32_16x16x128_f8f6f4 v[92:95], v[0:7], v[32:39], v[92:95], v198, v198 op_sel_hi:[0,0,0]
	v_mfma_scale_f32_16x16x128_f8f6f4 v[88:91], v[8:15], v[40:47], v[88:91], v198, v198 op_sel_hi:[0,0,0]
	v_mfma_scale_f32_16x16x128_f8f6f4 v[84:87], v[0:7], v[40:47], v[84:87], v198, v198 op_sel_hi:[0,0,0]
	v_mfma_scale_f32_16x16x128_f8f6f4 v[80:83], v[8:15], v[48:55], v[80:83], v198, v198 op_sel_hi:[0,0,0]
	v_mfma_scale_f32_16x16x128_f8f6f4 v[76:79], v[0:7], v[48:55], v[76:79], v198, v198 op_sel_hi:[0,0,0]
	v_mfma_scale_f32_16x16x128_f8f6f4 v[72:75], v[8:15], v[56:63], v[72:75], v198, v198 op_sel_hi:[0,0,0]
	v_mfma_scale_f32_16x16x128_f8f6f4 v[68:71], v[0:7], v[56:63], v[68:71], v198, v198 op_sel_hi:[0,0,0]
	s_setprio 0
	s_barrier
	s_waitcnt vmcnt(16)
	v_mbcnt_lo_u32_b32 v0, -1, 0
	v_mbcnt_hi_u32_b32 v0, -1, v0
	s_add_i32 s33, s61, 0x200
	v_lshl_add_u32 v0, v0, 4, s40
	v_ashrrev_i32_e32 v1, 31, v0
	v_lshrrev_b32_e32 v1, 22, v1
	v_add_u32_e32 v1, v0, v1
	v_ashrrev_i32_e32 v1, 10, v1
	v_mul_i32_i24_e32 v2, 0x400, v1
	v_sub_u32_e32 v2, v0, v2
	v_lshrrev_b32_e32 v3, 4, v2
	v_bitop3_b32 v3, v3, v2, 32 bitop3:0x6c
	v_ashrrev_i32_e32 v2, 31, v2
	v_lshrrev_b32_e32 v2, 26, v2
	v_add_u32_e32 v2, v3, v2
	v_and_b32_e32 v2, 0xc0, v2
	v_add_u32_e32 v0, 0x2000, v0
	v_sub_u32_e32 v2, v3, v2
	v_ashrrev_i32_e32 v3, 31, v0
	v_lshrrev_b32_e32 v3, 22, v3
	v_add_u32_e32 v3, v0, v3
	v_ashrrev_i32_e32 v3, 10, v3
	v_mul_i32_i24_e32 v4, 0x400, v3
	v_sub_u32_e32 v0, v0, v4
	v_lshrrev_b32_e32 v4, 4, v0
	v_bitop3_b32 v4, v4, v0, 32 bitop3:0x6c
	v_ashrrev_i32_e32 v0, 31, v0
	v_lshrrev_b32_e32 v0, 26, v0
	v_add_u32_e32 v0, v4, v0
	v_and_b32_e32 v0, 0xffc0, v0
	v_sub_u32_e32 v0, v4, v0
	v_lshrrev_b16_e32 v4, 7, v0
	v_and_b32_e32 v4, 1, v4
	v_add_u16_e32 v0, v0, v4
	v_lshlrev_b32_e32 v1, 5, v1
	v_ashrrev_i16_sdwa v2, v199, sext(v2) dst_sel:DWORD dst_unused:UNUSED_PAD src0_sel:DWORD src1_sel:BYTE_0
	v_lshlrev_b32_e32 v3, 5, v3
	v_ashrrev_i16_sdwa v0, v199, sext(v0) dst_sel:DWORD dst_unused:UNUSED_PAD src0_sel:DWORD src1_sel:BYTE_0
	v_and_b32_e32 v1, 32, v1
	v_bfe_i32 v2, v2, 0, 16
	v_and_b32_e32 v3, 32, v3
	v_bfe_i32 v0, v0, 0, 16
	v_add_lshl_u32 v1, v1, v2, 1
	v_add_lshl_u32 v0, v3, v0, 1
	v_lshl_add_u32 v32, v220, 12, v1
	v_lshl_add_u32 v33, v217, 12, v0
	v_lshl_add_u32 v34, v218, 12, v1
	v_lshl_add_u32 v35, v219, 12, v0
	s_mov_b32 s37, 0
.LBB0_1330:
	s_add_i32 s61, s36, 0x80
	s_cmp_eq_u32 s37, 28
	s_cselect_b64 vcc, -1, 0
	ds_read_b128 v[16:19], v202 offset:0
	ds_read_b128 v[20:23], v202 offset:0x400
	ds_read_b128 v[24:27], v202 offset:0x800
	ds_read_b128 v[28:31], v202 offset:0xc00
	ds_read_b128 v[36:39], v201 offset:0
	ds_read_b128 v[40:43], v201 offset:0x400
	ds_read_b128 v[44:47], v201 offset:0x800
	ds_read_b128 v[48:51], v201 offset:0xc00
	ds_read_b128 v[52:55], v201 offset:0x1000
	ds_read_b128 v[56:59], v201 offset:0x1400
	ds_read_b128 v[218:221], v201 offset:0x1800
	ds_read_b128 v[222:225], v201 offset:0x1c00
	ds_read_b128 v[8:11], v202 offset:0x4000
	ds_read_b128 v[12:15], v202 offset:0x4400
	ds_read_b128 v[0:3], v202 offset:0x4800
	ds_read_b128 v[4:7], v202 offset:0x4c00
	s_and_b64 s[66:67], vcc, exec
	s_cselect_b32 s67, s85, s61
	s_cselect_b32 s66, s86, s33
	s_add_i32 s61, s67, 0x80
	s_mov_b32 m0, s73
	s_nop 0
	buffer_load_dwordx4 v207, s[4:7], s36 offen lds
	s_mov_b32 m0, s74
	s_nop 0
	buffer_load_dwordx4 v206, s[4:7], s36 offen lds
	s_waitcnt vmcnt(8)
	s_waitcnt lgkmcnt(4)
	s_barrier
	s_setprio 1
	v_mfma_scale_f32_16x16x128_f8f6f4 v[192:195], v[16:23], v[36:43], v[192:195], v198, v198 op_sel_hi:[0,0,0]
	v_mfma_scale_f32_16x16x128_f8f6f4 v[188:191], v[24:31], v[36:43], v[188:191], v198, v198 op_sel_hi:[0,0,0]
	v_mfma_scale_f32_16x16x128_f8f6f4 v[184:187], v[16:23], v[44:51], v[184:187], v198, v198 op_sel_hi:[0,0,0]
	v_mfma_scale_f32_16x16x128_f8f6f4 v[180:183], v[24:31], v[44:51], v[180:183], v198, v198 op_sel_hi:[0,0,0]
	v_mfma_scale_f32_16x16x128_f8f6f4 v[176:179], v[16:23], v[52:59], v[176:179], v198, v198 op_sel_hi:[0,0,0]
	v_mfma_scale_f32_16x16x128_f8f6f4 v[172:175], v[24:31], v[52:59], v[172:175], v198, v198 op_sel_hi:[0,0,0]
	v_mfma_scale_f32_16x16x128_f8f6f4 v[168:171], v[16:23], v[218:225], v[168:171], v198, v198 op_sel_hi:[0,0,0]
	v_mfma_scale_f32_16x16x128_f8f6f4 v[164:167], v[24:31], v[218:225], v[164:167], v198, v198 op_sel_hi:[0,0,0]
	s_setprio 0
	s_setprio 1
	s_waitcnt lgkmcnt(2)
	v_mfma_scale_f32_16x16x128_f8f6f4 v[160:163], v[8:15], v[36:43], v[160:163], v198, v198 op_sel_hi:[0,0,0]
	s_waitcnt lgkmcnt(0)
	v_mfma_scale_f32_16x16x128_f8f6f4 v[156:159], v[0:7], v[36:43], v[156:159], v198, v198 op_sel_hi:[0,0,0]
	v_mfma_scale_f32_16x16x128_f8f6f4 v[152:155], v[8:15], v[44:51], v[152:155], v198, v198 op_sel_hi:[0,0,0]
	v_mfma_scale_f32_16x16x128_f8f6f4 v[148:151], v[0:7], v[44:51], v[148:151], v198, v198 op_sel_hi:[0,0,0]
	v_mfma_scale_f32_16x16x128_f8f6f4 v[144:147], v[8:15], v[52:59], v[144:147], v198, v198 op_sel_hi:[0,0,0]
	v_mfma_scale_f32_16x16x128_f8f6f4 v[140:143], v[0:7], v[52:59], v[140:143], v198, v198 op_sel_hi:[0,0,0]
	v_mfma_scale_f32_16x16x128_f8f6f4 v[136:139], v[8:15], v[218:225], v[136:139], v198, v198 op_sel_hi:[0,0,0]
	v_mfma_scale_f32_16x16x128_f8f6f4 v[132:135], v[0:7], v[218:225], v[132:135], v198, v198 op_sel_hi:[0,0,0]
	s_setprio 0
	s_barrier
	ds_read_b128 v[36:39], v201 offset:0x4000
	ds_read_b128 v[40:43], v201 offset:0x4400
	ds_read_b128 v[44:47], v201 offset:0x4800
	ds_read_b128 v[48:51], v201 offset:0x4c00
	ds_read_b128 v[52:55], v201 offset:0x5000
	ds_read_b128 v[56:59], v201 offset:0x5400
	ds_read_b128 v[218:221], v201 offset:0x5800
	ds_read_b128 v[222:225], v201 offset:0x5c00
	s_mov_b32 m0, s45
	s_nop 0
	buffer_load_dwordx4 v200, s[8:11], s66 offen lds
	s_add_i32 s89, s66, 0x80000
	s_mov_b32 m0, s46
	v_cndmask_b32_e32 v60, v205, v32, vcc
	buffer_load_dwordx4 v200, s[8:11], s89 offen lds
	s_add_i32 s89, s66, 0x8000
	s_mov_b32 m0, s47
	v_cndmask_b32_e32 v61, v208, v33, vcc
	buffer_load_dwordx4 v200, s[8:11], s89 offen lds
	s_add_i32 s89, s66, 0x88000
	s_mov_b32 m0, s48
	s_nop 0
	buffer_load_dwordx4 v200, s[8:11], s89 offen lds
	s_mov_b32 m0, s44
	s_nop 0
	buffer_load_dwordx4 v60, s[4:7], s67 offen lds
	s_mov_b32 m0, s49
	s_nop 0
	buffer_load_dwordx4 v61, s[4:7], s67 offen lds
	s_waitcnt vmcnt(8)
	s_waitcnt lgkmcnt(0)
	s_barrier
	s_setprio 1
	v_mfma_scale_f32_16x16x128_f8f6f4 v[128:131], v[16:23], v[36:43], v[128:131], v198, v198 op_sel_hi:[0,0,0]
	v_mfma_scale_f32_16x16x128_f8f6f4 v[124:127], v[24:31], v[36:43], v[124:127], v198, v198 op_sel_hi:[0,0,0]
	v_mfma_scale_f32_16x16x128_f8f6f4 v[120:123], v[16:23], v[44:51], v[120:123], v198, v198 op_sel_hi:[0,0,0]
	v_mfma_scale_f32_16x16x128_f8f6f4 v[116:119], v[24:31], v[44:51], v[116:119], v198, v198 op_sel_hi:[0,0,0]
	v_mfma_scale_f32_16x16x128_f8f6f4 v[112:115], v[16:23], v[52:59], v[112:115], v198, v198 op_sel_hi:[0,0,0]
	v_mfma_scale_f32_16x16x128_f8f6f4 v[108:111], v[24:31], v[52:59], v[108:111], v198, v198 op_sel_hi:[0,0,0]
	v_mfma_scale_f32_16x16x128_f8f6f4 v[104:107], v[16:23], v[218:225], v[104:107], v198, v198 op_sel_hi:[0,0,0]
	v_mfma_scale_f32_16x16x128_f8f6f4 v[100:103], v[24:31], v[218:225], v[100:103], v198, v198 op_sel_hi:[0,0,0]
	s_setprio 0
	s_setprio 1
	v_mfma_scale_f32_16x16x128_f8f6f4 v[96:99], v[8:15], v[36:43], v[96:99], v198, v198 op_sel_hi:[0,0,0]
	v_mfma_scale_f32_16x16x128_f8f6f4 v[92:95], v[0:7], v[36:43], v[92:95], v198, v198 op_sel_hi:[0,0,0]
	v_mfma_scale_f32_16x16x128_f8f6f4 v[88:91], v[8:15], v[44:51], v[88:91], v198, v198 op_sel_hi:[0,0,0]
	v_mfma_scale_f32_16x16x128_f8f6f4 v[84:87], v[0:7], v[44:51], v[84:87], v198, v198 op_sel_hi:[0,0,0]
	v_mfma_scale_f32_16x16x128_f8f6f4 v[80:83], v[8:15], v[52:59], v[80:83], v198, v198 op_sel_hi:[0,0,0]
	v_mfma_scale_f32_16x16x128_f8f6f4 v[76:79], v[0:7], v[52:59], v[76:79], v198, v198 op_sel_hi:[0,0,0]
	v_mfma_scale_f32_16x16x128_f8f6f4 v[72:75], v[8:15], v[218:225], v[72:75], v198, v198 op_sel_hi:[0,0,0]
	v_mfma_scale_f32_16x16x128_f8f6f4 v[68:71], v[0:7], v[218:225], v[68:71], v198, v198 op_sel_hi:[0,0,0]
	s_setprio 0
	s_barrier
	ds_read_b128 v[24:27], v202 offset:0x8000
	ds_read_b128 v[28:31], v202 offset:0x8400
	ds_read_b128 v[16:19], v202 offset:0x8800
	ds_read_b128 v[20:23], v202 offset:0x8c00
	ds_read_b128 v[36:39], v201 offset:0x8000
	ds_read_b128 v[40:43], v201 offset:0x8400
	ds_read_b128 v[44:47], v201 offset:0x8800
	ds_read_b128 v[48:51], v201 offset:0x8c00
	ds_read_b128 v[52:55], v201 offset:0x9000
	ds_read_b128 v[56:59], v201 offset:0x9400
	ds_read_b128 v[218:221], v201 offset:0x9800
	ds_read_b128 v[222:225], v201 offset:0x9c00
	ds_read_b128 v[8:11], v202 offset:0xc000
	ds_read_b128 v[12:15], v202 offset:0xc400
	ds_read_b128 v[0:3], v202 offset:0xc800
	ds_read_b128 v[4:7], v202 offset:0xcc00
	s_mov_b32 m0, s50
	v_cndmask_b32_e32 v62, v207, v34, vcc
	buffer_load_dwordx4 v62, s[4:7], s67 offen lds
	v_cndmask_b32_e32 v62, v206, v35, vcc
	s_mov_b32 m0, s51
	s_nop 0
	buffer_load_dwordx4 v62, s[4:7], s67 offen lds
	s_waitcnt vmcnt(8)
	s_waitcnt lgkmcnt(4)
	s_barrier
	s_setprio 1
	v_mfma_scale_f32_16x16x128_f8f6f4 v[192:195], v[24:31], v[36:43], v[192:195], v198, v198 op_sel_hi:[0,0,0]
	v_mfma_scale_f32_16x16x128_f8f6f4 v[188:191], v[16:23], v[36:43], v[188:191], v198, v198 op_sel_hi:[0,0,0]
	v_mfma_scale_f32_16x16x128_f8f6f4 v[184:187], v[24:31], v[44:51], v[184:187], v198, v198 op_sel_hi:[0,0,0]
	v_mfma_scale_f32_16x16x128_f8f6f4 v[180:183], v[16:23], v[44:51], v[180:183], v198, v198 op_sel_hi:[0,0,0]
	v_mfma_scale_f32_16x16x128_f8f6f4 v[176:179], v[24:31], v[52:59], v[176:179], v198, v198 op_sel_hi:[0,0,0]
	v_mfma_scale_f32_16x16x128_f8f6f4 v[172:175], v[16:23], v[52:59], v[172:175], v198, v198 op_sel_hi:[0,0,0]
	v_mfma_scale_f32_16x16x128_f8f6f4 v[168:171], v[24:31], v[218:225], v[168:171], v198, v198 op_sel_hi:[0,0,0]
	v_mfma_scale_f32_16x16x128_f8f6f4 v[164:167], v[16:23], v[218:225], v[164:167], v198, v198 op_sel_hi:[0,0,0]
	s_setprio 0
	s_setprio 1
	s_waitcnt lgkmcnt(2)
	v_mfma_scale_f32_16x16x128_f8f6f4 v[160:163], v[8:15], v[36:43], v[160:163], v198, v198 op_sel_hi:[0,0,0]
	s_waitcnt lgkmcnt(0)
	v_mfma_scale_f32_16x16x128_f8f6f4 v[156:159], v[0:7], v[36:43], v[156:159], v198, v198 op_sel_hi:[0,0,0]
	v_mfma_scale_f32_16x16x128_f8f6f4 v[152:155], v[8:15], v[44:51], v[152:155], v198, v198 op_sel_hi:[0,0,0]
	v_mfma_scale_f32_16x16x128_f8f6f4 v[148:151], v[0:7], v[44:51], v[148:151], v198, v198 op_sel_hi:[0,0,0]
	v_mfma_scale_f32_16x16x128_f8f6f4 v[144:147], v[8:15], v[52:59], v[144:147], v198, v198 op_sel_hi:[0,0,0]
	v_mfma_scale_f32_16x16x128_f8f6f4 v[140:143], v[0:7], v[52:59], v[140:143], v198, v198 op_sel_hi:[0,0,0]
	v_mfma_scale_f32_16x16x128_f8f6f4 v[136:139], v[8:15], v[218:225], v[136:139], v198, v198 op_sel_hi:[0,0,0]
	v_mfma_scale_f32_16x16x128_f8f6f4 v[132:135], v[0:7], v[218:225], v[132:135], v198, v198 op_sel_hi:[0,0,0]
	s_setprio 0
	s_barrier
	ds_read_b128 v[36:39], v201 offset:0xc000
	ds_read_b128 v[40:43], v201 offset:0xc400
	ds_read_b128 v[44:47], v201 offset:0xc800
	ds_read_b128 v[48:51], v201 offset:0xcc00
	ds_read_b128 v[52:55], v201 offset:0xd000
	ds_read_b128 v[56:59], v201 offset:0xd400
	ds_read_b128 v[218:221], v201 offset:0xd800
	ds_read_b128 v[222:225], v201 offset:0xdc00
	s_mov_b32 m0, s64
	s_add_i32 s67, s66, 0x80
	buffer_load_dwordx4 v200, s[8:11], s67 offen lds
	s_add_i32 s67, s66, 0x80080
	s_mov_b32 m0, s65
	s_nop 0
	buffer_load_dwordx4 v200, s[8:11], s67 offen lds
	s_add_i32 s67, s66, 0x8080
	s_mov_b32 m0, s70
	s_add_i32 s66, s66, 0x88080
	buffer_load_dwordx4 v200, s[8:11], s67 offen lds
	s_mov_b32 m0, s71
	s_nop 0
	buffer_load_dwordx4 v200, s[8:11], s66 offen lds
	s_mov_b32 m0, s68
	s_nop 0
	buffer_load_dwordx4 v60, s[4:7], s61 offen lds
	s_mov_b32 m0, s69
	s_nop 0
	buffer_load_dwordx4 v61, s[4:7], s61 offen lds
	s_waitcnt vmcnt(8)
	s_waitcnt lgkmcnt(0)
	s_barrier
	s_setprio 1
	v_mfma_scale_f32_16x16x128_f8f6f4 v[128:131], v[24:31], v[36:43], v[128:131], v198, v198 op_sel_hi:[0,0,0]
	v_mfma_scale_f32_16x16x128_f8f6f4 v[124:127], v[16:23], v[36:43], v[124:127], v198, v198 op_sel_hi:[0,0,0]
	v_mfma_scale_f32_16x16x128_f8f6f4 v[120:123], v[24:31], v[44:51], v[120:123], v198, v198 op_sel_hi:[0,0,0]
	v_mfma_scale_f32_16x16x128_f8f6f4 v[116:119], v[16:23], v[44:51], v[116:119], v198, v198 op_sel_hi:[0,0,0]
	v_mfma_scale_f32_16x16x128_f8f6f4 v[112:115], v[24:31], v[52:59], v[112:115], v198, v198 op_sel_hi:[0,0,0]
	v_mfma_scale_f32_16x16x128_f8f6f4 v[108:111], v[16:23], v[52:59], v[108:111], v198, v198 op_sel_hi:[0,0,0]
	v_mfma_scale_f32_16x16x128_f8f6f4 v[104:107], v[24:31], v[218:225], v[104:107], v198, v198 op_sel_hi:[0,0,0]
	v_mfma_scale_f32_16x16x128_f8f6f4 v[100:103], v[16:23], v[218:225], v[100:103], v198, v198 op_sel_hi:[0,0,0]
	s_setprio 0
	s_setprio 1
	v_mfma_scale_f32_16x16x128_f8f6f4 v[96:99], v[8:15], v[36:43], v[96:99], v198, v198 op_sel_hi:[0,0,0]
	v_mfma_scale_f32_16x16x128_f8f6f4 v[92:95], v[0:7], v[36:43], v[92:95], v198, v198 op_sel_hi:[0,0,0]
	v_mfma_scale_f32_16x16x128_f8f6f4 v[88:91], v[8:15], v[44:51], v[88:91], v198, v198 op_sel_hi:[0,0,0]
	v_mfma_scale_f32_16x16x128_f8f6f4 v[84:87], v[0:7], v[44:51], v[84:87], v198, v198 op_sel_hi:[0,0,0]
	v_mfma_scale_f32_16x16x128_f8f6f4 v[80:83], v[8:15], v[52:59], v[80:83], v198, v198 op_sel_hi:[0,0,0]
	v_mfma_scale_f32_16x16x128_f8f6f4 v[76:79], v[0:7], v[52:59], v[76:79], v198, v198 op_sel_hi:[0,0,0]
	v_mfma_scale_f32_16x16x128_f8f6f4 v[72:75], v[8:15], v[218:225], v[72:75], v198, v198 op_sel_hi:[0,0,0]
	v_mfma_scale_f32_16x16x128_f8f6f4 v[68:71], v[0:7], v[218:225], v[68:71], v198, v198 op_sel_hi:[0,0,0]
	s_setprio 0
	s_barrier
	s_add_i32 s37, s37, 2
	s_addk_i32 s36, 0x100
	s_addk_i32 s33, 0x100
	s_cmp_gt_u32 s37, 29
	s_cbranch_scc0 .LBB0_1330
	s_and_b64 vcc, exec, s[28:29]
	s_cbranch_vccz .LBB0_1333
	s_barrier

.LBB0_1369:
	s_add_i32 s33, s88, 0x180
	s_add_i32 s40, s89, 0x180
	s_waitcnt lgkmcnt(0)
	s_barrier
	s_setprio 1
	v_mfma_scale_f32_16x16x128_f8f6f4 v[128:131], v[24:31], v[56:63], 0, v235, v235 op_sel_hi:[0,0,0]
	v_mfma_scale_f32_16x16x128_f8f6f4 v[124:127], v[16:23], v[56:63], 0, v235, v235 op_sel_hi:[0,0,0]
	v_mfma_scale_f32_16x16x128_f8f6f4 v[120:123], v[24:31], v[48:55], 0, v235, v235 op_sel_hi:[0,0,0]
	v_mfma_scale_f32_16x16x128_f8f6f4 v[116:119], v[16:23], v[48:55], 0, v235, v235 op_sel_hi:[0,0,0]
	v_mfma_scale_f32_16x16x128_f8f6f4 v[112:115], v[24:31], v[40:47], 0, v235, v235 op_sel_hi:[0,0,0]
	v_mfma_scale_f32_16x16x128_f8f6f4 v[108:111], v[16:23], v[40:47], 0, v235, v235 op_sel_hi:[0,0,0]
	v_mfma_scale_f32_16x16x128_f8f6f4 v[104:107], v[24:31], v[32:39], 0, v235, v235 op_sel_hi:[0,0,0]
	v_mfma_scale_f32_16x16x128_f8f6f4 v[100:103], v[16:23], v[32:39], 0, v235, v235 op_sel_hi:[0,0,0]
	s_setprio 0
	s_setprio 1
	v_mfma_scale_f32_16x16x128_f8f6f4 v[96:99], v[8:15], v[56:63], 0, v235, v235 op_sel_hi:[0,0,0]
	v_mfma_scale_f32_16x16x128_f8f6f4 v[92:95], v[0:7], v[56:63], 0, v235, v235 op_sel_hi:[0,0,0]
	v_mfma_scale_f32_16x16x128_f8f6f4 v[88:91], v[8:15], v[48:55], 0, v235, v235 op_sel_hi:[0,0,0]
	v_mfma_scale_f32_16x16x128_f8f6f4 v[84:87], v[0:7], v[48:55], 0, v235, v235 op_sel_hi:[0,0,0]
	v_mfma_scale_f32_16x16x128_f8f6f4 v[80:83], v[8:15], v[40:47], 0, v235, v235 op_sel_hi:[0,0,0]
	v_mfma_scale_f32_16x16x128_f8f6f4 v[76:79], v[0:7], v[40:47], 0, v235, v235 op_sel_hi:[0,0,0]
	v_mfma_scale_f32_16x16x128_f8f6f4 v[72:75], v[8:15], v[32:39], 0, v235, v235 op_sel_hi:[0,0,0]
	v_mfma_scale_f32_16x16x128_f8f6f4 v[68:71], v[0:7], v[32:39], 0, v235, v235 op_sel_hi:[0,0,0]
	s_setprio 0
	s_barrier
	ds_read_b128 v[16:19], v233 offset:0x8000
	ds_read_b128 v[20:23], v233 offset:0x8400
	ds_read_b128 v[24:27], v233 offset:0x8800
	ds_read_b128 v[28:31], v233 offset:0x8c00
	ds_read_b128 v[32:35], v232 offset:0x8000
	ds_read_b128 v[36:39], v232 offset:0x8400
	ds_read_b128 v[40:43], v232 offset:0x8800
	ds_read_b128 v[44:47], v232 offset:0x8c00
	ds_read_b128 v[48:51], v232 offset:0x9000
	ds_read_b128 v[52:55], v232 offset:0x9400
	ds_read_b128 v[56:59], v232 offset:0x9800
	ds_read_b128 v[60:63], v232 offset:0x9c00
	ds_read_b128 v[8:11], v233 offset:0xc000
	ds_read_b128 v[12:15], v233 offset:0xc400
	ds_read_b128 v[0:3], v233 offset:0xc800
	ds_read_b128 v[4:7], v233 offset:0xcc00
	s_mov_b32 m0, s62
	s_add_i32 s10, s88, 0x10100
	buffer_load_dwordx4 v230, s[4:7], s10 offen lds
	s_add_i32 s10, s88, 0x18100
	s_mov_b32 m0, s63
	s_nop 0
	buffer_load_dwordx4 v230, s[4:7], s10 offen lds
	s_waitcnt vmcnt(8)
	s_waitcnt lgkmcnt(4)
	s_barrier
	s_setprio 1
	v_mfma_scale_f32_16x16x128_f8f6f4 v[192:195], v[16:23], v[32:39], v[192:195], v235, v235 op_sel_hi:[0,0,0]
	v_mfma_scale_f32_16x16x128_f8f6f4 v[188:191], v[24:31], v[32:39], v[188:191], v235, v235 op_sel_hi:[0,0,0]
	v_mfma_scale_f32_16x16x128_f8f6f4 v[184:187], v[16:23], v[40:47], v[184:187], v235, v235 op_sel_hi:[0,0,0]
	v_mfma_scale_f32_16x16x128_f8f6f4 v[180:183], v[24:31], v[40:47], v[180:183], v235, v235 op_sel_hi:[0,0,0]
	v_mfma_scale_f32_16x16x128_f8f6f4 v[176:179], v[16:23], v[48:55], v[176:179], v235, v235 op_sel_hi:[0,0,0]
	v_mfma_scale_f32_16x16x128_f8f6f4 v[172:175], v[24:31], v[48:55], v[172:175], v235, v235 op_sel_hi:[0,0,0]
	v_mfma_scale_f32_16x16x128_f8f6f4 v[168:171], v[16:23], v[56:63], v[168:171], v235, v235 op_sel_hi:[0,0,0]
	v_mfma_scale_f32_16x16x128_f8f6f4 v[164:167], v[24:31], v[56:63], v[164:167], v235, v235 op_sel_hi:[0,0,0]
	s_setprio 0
	s_setprio 1
	s_waitcnt lgkmcnt(2)
	v_mfma_scale_f32_16x16x128_f8f6f4 v[160:163], v[8:15], v[32:39], v[160:163], v235, v235 op_sel_hi:[0,0,0]
	s_waitcnt lgkmcnt(0)
	v_mfma_scale_f32_16x16x128_f8f6f4 v[156:159], v[0:7], v[32:39], v[156:159], v235, v235 op_sel_hi:[0,0,0]
	v_mfma_scale_f32_16x16x128_f8f6f4 v[152:155], v[8:15], v[40:47], v[152:155], v235, v235 op_sel_hi:[0,0,0]
	v_mfma_scale_f32_16x16x128_f8f6f4 v[148:151], v[0:7], v[40:47], v[148:151], v235, v235 op_sel_hi:[0,0,0]
	v_mfma_scale_f32_16x16x128_f8f6f4 v[144:147], v[8:15], v[48:55], v[144:147], v235, v235 op_sel_hi:[0,0,0]
	v_mfma_scale_f32_16x16x128_f8f6f4 v[140:143], v[0:7], v[48:55], v[140:143], v235, v235 op_sel_hi:[0,0,0]
	v_mfma_scale_f32_16x16x128_f8f6f4 v[136:139], v[8:15], v[56:63], v[136:139], v235, v235 op_sel_hi:[0,0,0]
	v_mfma_scale_f32_16x16x128_f8f6f4 v[132:135], v[0:7], v[56:63], v[132:135], v235, v235 op_sel_hi:[0,0,0]
	s_setprio 0
	s_barrier
	ds_read_b128 v[32:35], v232 offset:0xc000
	ds_read_b128 v[36:39], v232 offset:0xc400
	ds_read_b128 v[40:43], v232 offset:0xc800
	ds_read_b128 v[44:47], v232 offset:0xcc00
	ds_read_b128 v[48:51], v232 offset:0xd000
	ds_read_b128 v[52:55], v232 offset:0xd400
	ds_read_b128 v[56:59], v232 offset:0xd800
	ds_read_b128 v[60:63], v232 offset:0xdc00
	s_mov_b32 m0, s64
	s_mov_b32 s10, s6
	s_mov_b32 s11, s7
	buffer_load_dwordx4 v231, s[8:11], s40 offen lds
	s_add_i32 s40, s89, 0x10180
	s_mov_b32 m0, s65
	s_nop 0
	buffer_load_dwordx4 v231, s[8:11], s40 offen lds
	s_add_i32 s40, s89, 0x1180
	s_mov_b32 m0, s70
	s_nop 0
	buffer_load_dwordx4 v231, s[8:11], s40 offen lds
	s_add_i32 s40, s89, 0x11180
	s_mov_b32 m0, s71
	s_nop 0
	buffer_load_dwordx4 v231, s[8:11], s40 offen lds
	s_mov_b32 m0, s68
	s_nop 0
	buffer_load_dwordx4 v230, s[4:7], s33 offen lds
	s_add_i32 s33, s88, 0x8180
	s_mov_b32 m0, s69
	s_nop 0
	buffer_load_dwordx4 v230, s[4:7], s33 offen lds
	s_waitcnt vmcnt(8)
	s_waitcnt lgkmcnt(0)
	s_barrier
	s_setprio 1
	v_mfma_scale_f32_16x16x128_f8f6f4 v[128:131], v[16:23], v[32:39], v[128:131], v235, v235 op_sel_hi:[0,0,0]
	v_mfma_scale_f32_16x16x128_f8f6f4 v[124:127], v[24:31], v[32:39], v[124:127], v235, v235 op_sel_hi:[0,0,0]
	v_mfma_scale_f32_16x16x128_f8f6f4 v[120:123], v[16:23], v[40:47], v[120:123], v235, v235 op_sel_hi:[0,0,0]
	v_mfma_scale_f32_16x16x128_f8f6f4 v[116:119], v[24:31], v[40:47], v[116:119], v235, v235 op_sel_hi:[0,0,0]
	v_mfma_scale_f32_16x16x128_f8f6f4 v[112:115], v[16:23], v[48:55], v[112:115], v235, v235 op_sel_hi:[0,0,0]
	v_mfma_scale_f32_16x16x128_f8f6f4 v[108:111], v[24:31], v[48:55], v[108:111], v235, v235 op_sel_hi:[0,0,0]
	v_mfma_scale_f32_16x16x128_f8f6f4 v[104:107], v[16:23], v[56:63], v[104:107], v235, v235 op_sel_hi:[0,0,0]
	v_mfma_scale_f32_16x16x128_f8f6f4 v[100:103], v[24:31], v[56:63], v[100:103], v235, v235 op_sel_hi:[0,0,0]
	s_setprio 0
	s_setprio 1
	v_mfma_scale_f32_16x16x128_f8f6f4 v[96:99], v[8:15], v[32:39], v[96:99], v235, v235 op_sel_hi:[0,0,0]
	v_mfma_scale_f32_16x16x128_f8f6f4 v[92:95], v[0:7], v[32:39], v[92:95], v235, v235 op_sel_hi:[0,0,0]
	v_mfma_scale_f32_16x16x128_f8f6f4 v[88:91], v[8:15], v[40:47], v[88:91], v235, v235 op_sel_hi:[0,0,0]
	v_mfma_scale_f32_16x16x128_f8f6f4 v[84:87], v[0:7], v[40:47], v[84:87], v235, v235 op_sel_hi:[0,0,0]
	v_mfma_scale_f32_16x16x128_f8f6f4 v[80:83], v[8:15], v[48:55], v[80:83], v235, v235 op_sel_hi:[0,0,0]
	v_mfma_scale_f32_16x16x128_f8f6f4 v[76:79], v[0:7], v[48:55], v[76:79], v235, v235 op_sel_hi:[0,0,0]
	v_mfma_scale_f32_16x16x128_f8f6f4 v[72:75], v[8:15], v[56:63], v[72:75], v235, v235 op_sel_hi:[0,0,0]
	v_mfma_scale_f32_16x16x128_f8f6f4 v[68:71], v[0:7], v[56:63], v[68:71], v235, v235 op_sel_hi:[0,0,0]
	s_setprio 0
	s_barrier
	ds_read_b128 v[16:19], v233 offset:0
	ds_read_b128 v[20:23], v233 offset:0x400
	ds_read_b128 v[24:27], v233 offset:0x800
	ds_read_b128 v[28:31], v233 offset:0xc00
	ds_read_b128 v[32:35], v232 offset:0
	ds_read_b128 v[36:39], v232 offset:0x400
	ds_read_b128 v[40:43], v232 offset:0x800
	ds_read_b128 v[44:47], v232 offset:0xc00
	ds_read_b128 v[48:51], v232 offset:0x1000
	ds_read_b128 v[52:55], v232 offset:0x1400
	ds_read_b128 v[56:59], v232 offset:0x1800
	ds_read_b128 v[60:63], v232 offset:0x1c00
	ds_read_b128 v[8:11], v233 offset:0x4000
	ds_read_b128 v[12:15], v233 offset:0x4400
	ds_read_b128 v[0:3], v233 offset:0x4800
	ds_read_b128 v[4:7], v233 offset:0x4c00
	s_add_i32 s33, s85, 0x80
	s_mov_b32 m0, s74
	s_add_i32 s40, s88, 0x10180
	buffer_load_dwordx4 v230, s[4:7], s40 offen lds
	s_add_i32 s40, s88, 0x18180
	s_mov_b32 m0, s76
	s_nop 0
	buffer_load_dwordx4 v230, s[4:7], s40 offen lds
	s_waitcnt vmcnt(8)
	s_waitcnt lgkmcnt(4)
	s_barrier
	s_setprio 1
	v_mfma_scale_f32_16x16x128_f8f6f4 v[192:195], v[16:23], v[32:39], v[192:195], v235, v235 op_sel_hi:[0,0,0]
	v_mfma_scale_f32_16x16x128_f8f6f4 v[188:191], v[24:31], v[32:39], v[188:191], v235, v235 op_sel_hi:[0,0,0]
	v_mfma_scale_f32_16x16x128_f8f6f4 v[184:187], v[16:23], v[40:47], v[184:187], v235, v235 op_sel_hi:[0,0,0]
	v_mfma_scale_f32_16x16x128_f8f6f4 v[180:183], v[24:31], v[40:47], v[180:183], v235, v235 op_sel_hi:[0,0,0]
	v_mfma_scale_f32_16x16x128_f8f6f4 v[176:179], v[16:23], v[48:55], v[176:179], v235, v235 op_sel_hi:[0,0,0]
	v_mfma_scale_f32_16x16x128_f8f6f4 v[172:175], v[24:31], v[48:55], v[172:175], v235, v235 op_sel_hi:[0,0,0]
	v_mfma_scale_f32_16x16x128_f8f6f4 v[168:171], v[16:23], v[56:63], v[168:171], v235, v235 op_sel_hi:[0,0,0]
	v_mfma_scale_f32_16x16x128_f8f6f4 v[164:167], v[24:31], v[56:63], v[164:167], v235, v235 op_sel_hi:[0,0,0]
	s_setprio 0
	s_setprio 1
	s_waitcnt lgkmcnt(2)
	v_mfma_scale_f32_16x16x128_f8f6f4 v[160:163], v[8:15], v[32:39], v[160:163], v235, v235 op_sel_hi:[0,0,0]
	s_waitcnt lgkmcnt(0)
	v_mfma_scale_f32_16x16x128_f8f6f4 v[156:159], v[0:7], v[32:39], v[156:159], v235, v235 op_sel_hi:[0,0,0]
	v_mfma_scale_f32_16x16x128_f8f6f4 v[152:155], v[8:15], v[40:47], v[152:155], v235, v235 op_sel_hi:[0,0,0]
	v_mfma_scale_f32_16x16x128_f8f6f4 v[148:151], v[0:7], v[40:47], v[148:151], v235, v235 op_sel_hi:[0,0,0]
	v_mfma_scale_f32_16x16x128_f8f6f4 v[144:147], v[8:15], v[48:55], v[144:147], v235, v235 op_sel_hi:[0,0,0]
	v_mfma_scale_f32_16x16x128_f8f6f4 v[140:143], v[0:7], v[48:55], v[140:143], v235, v235 op_sel_hi:[0,0,0]
	v_mfma_scale_f32_16x16x128_f8f6f4 v[136:139], v[8:15], v[56:63], v[136:139], v235, v235 op_sel_hi:[0,0,0]
	v_mfma_scale_f32_16x16x128_f8f6f4 v[132:135], v[0:7], v[56:63], v[132:135], v235, v235 op_sel_hi:[0,0,0]
	s_setprio 0
	s_barrier
	ds_read_b128 v[32:35], v232 offset:0x4000
	ds_read_b128 v[36:39], v232 offset:0x4400
	ds_read_b128 v[40:43], v232 offset:0x4800
	ds_read_b128 v[44:47], v232 offset:0x4c00
	ds_read_b128 v[48:51], v232 offset:0x5000
	ds_read_b128 v[52:55], v232 offset:0x5400
	ds_read_b128 v[56:59], v232 offset:0x5800
	ds_read_b128 v[60:63], v232 offset:0x5c00
	s_mov_b32 m0, s46
	s_nop 0
	buffer_load_dwordx4 v231, s[8:11], s86 offen lds
	s_add_i32 s40, s86, 0x10000
	s_mov_b32 m0, s47
	s_nop 0
	buffer_load_dwordx4 v231, s[8:11], s40 offen lds
	s_add_i32 s40, s86, 0x1000
	s_mov_b32 m0, s49
	s_nop 0
	buffer_load_dwordx4 v231, s[8:11], s40 offen lds
	s_add_i32 s40, s86, 0x11000
	s_mov_b32 m0, s50
	s_nop 0
	buffer_load_dwordx4 v231, s[8:11], s40 offen lds
	s_mov_b32 m0, s48
	s_add_i32 s40, s85, 0x8000
	buffer_load_dwordx4 v230, s[4:7], s85 offen lds
	s_mov_b32 m0, s51
	s_nop 0
	buffer_load_dwordx4 v230, s[4:7], s40 offen lds
	s_waitcnt vmcnt(8)
	s_waitcnt lgkmcnt(0)
	s_barrier
	s_setprio 1
	v_mfma_scale_f32_16x16x128_f8f6f4 v[128:131], v[16:23], v[32:39], v[128:131], v235, v235 op_sel_hi:[0,0,0]
	v_mfma_scale_f32_16x16x128_f8f6f4 v[124:127], v[24:31], v[32:39], v[124:127], v235, v235 op_sel_hi:[0,0,0]
	v_mfma_scale_f32_16x16x128_f8f6f4 v[120:123], v[16:23], v[40:47], v[120:123], v235, v235 op_sel_hi:[0,0,0]
	v_mfma_scale_f32_16x16x128_f8f6f4 v[116:119], v[24:31], v[40:47], v[116:119], v235, v235 op_sel_hi:[0,0,0]
	v_mfma_scale_f32_16x16x128_f8f6f4 v[112:115], v[16:23], v[48:55], v[112:115], v235, v235 op_sel_hi:[0,0,0]
	v_mfma_scale_f32_16x16x128_f8f6f4 v[108:111], v[24:31], v[48:55], v[108:111], v235, v235 op_sel_hi:[0,0,0]
	v_mfma_scale_f32_16x16x128_f8f6f4 v[104:107], v[16:23], v[56:63], v[104:107], v235, v235 op_sel_hi:[0,0,0]
	v_mfma_scale_f32_16x16x128_f8f6f4 v[100:103], v[24:31], v[56:63], v[100:103], v235, v235 op_sel_hi:[0,0,0]
	s_setprio 0
	s_setprio 1
	v_mfma_scale_f32_16x16x128_f8f6f4 v[96:99], v[8:15], v[32:39], v[96:99], v235, v235 op_sel_hi:[0,0,0]
	v_mfma_scale_f32_16x16x128_f8f6f4 v[92:95], v[0:7], v[32:39], v[92:95], v235, v235 op_sel_hi:[0,0,0]
	v_mfma_scale_f32_16x16x128_f8f6f4 v[88:91], v[8:15], v[40:47], v[88:91], v235, v235 op_sel_hi:[0,0,0]
	v_mfma_scale_f32_16x16x128_f8f6f4 v[84:87], v[0:7], v[40:47], v[84:87], v235, v235 op_sel_hi:[0,0,0]
	v_mfma_scale_f32_16x16x128_f8f6f4 v[80:83], v[8:15], v[48:55], v[80:83], v235, v235 op_sel_hi:[0,0,0]
	v_mfma_scale_f32_16x16x128_f8f6f4 v[76:79], v[0:7], v[48:55], v[76:79], v235, v235 op_sel_hi:[0,0,0]
	v_mfma_scale_f32_16x16x128_f8f6f4 v[72:75], v[8:15], v[56:63], v[72:75], v235, v235 op_sel_hi:[0,0,0]
	v_mfma_scale_f32_16x16x128_f8f6f4 v[68:71], v[0:7], v[56:63], v[68:71], v235, v235 op_sel_hi:[0,0,0]
	s_setprio 0
	s_barrier
	ds_read_b128 v[16:19], v233 offset:0x8000
	ds_read_b128 v[20:23], v233 offset:0x8400
	ds_read_b128 v[24:27], v233 offset:0x8800
	ds_read_b128 v[28:31], v233 offset:0x8c00
	ds_read_b128 v[32:35], v232 offset:0x8000
	ds_read_b128 v[36:39], v232 offset:0x8400
	ds_read_b128 v[40:43], v232 offset:0x8800
	ds_read_b128 v[44:47], v232 offset:0x8c00
	ds_read_b128 v[48:51], v232 offset:0x9000
	ds_read_b128 v[52:55], v232 offset:0x9400
	ds_read_b128 v[56:59], v232 offset:0x9800
	ds_read_b128 v[60:63], v232 offset:0x9c00
	ds_read_b128 v[8:11], v233 offset:0xc000
	ds_read_b128 v[12:15], v233 offset:0xc400
	ds_read_b128 v[0:3], v233 offset:0xc800
	ds_read_b128 v[4:7], v233 offset:0xcc00
	s_mov_b32 m0, s62
	s_add_i32 s40, s85, 0x10000
	buffer_load_dwordx4 v230, s[4:7], s40 offen lds
	s_add_i32 s40, s85, 0x18000
	s_mov_b32 m0, s63
	s_nop 0
	buffer_load_dwordx4 v230, s[4:7], s40 offen lds
	s_waitcnt vmcnt(8)
	s_waitcnt lgkmcnt(4)
	s_barrier
	s_setprio 1
	v_mfma_scale_f32_16x16x128_f8f6f4 v[192:195], v[16:23], v[32:39], v[192:195], v235, v235 op_sel_hi:[0,0,0]
	v_mfma_scale_f32_16x16x128_f8f6f4 v[188:191], v[24:31], v[32:39], v[188:191], v235, v235 op_sel_hi:[0,0,0]
	v_mfma_scale_f32_16x16x128_f8f6f4 v[184:187], v[16:23], v[40:47], v[184:187], v235, v235 op_sel_hi:[0,0,0]
	v_mfma_scale_f32_16x16x128_f8f6f4 v[180:183], v[24:31], v[40:47], v[180:183], v235, v235 op_sel_hi:[0,0,0]
	v_mfma_scale_f32_16x16x128_f8f6f4 v[176:179], v[16:23], v[48:55], v[176:179], v235, v235 op_sel_hi:[0,0,0]
	v_mfma_scale_f32_16x16x128_f8f6f4 v[172:175], v[24:31], v[48:55], v[172:175], v235, v235 op_sel_hi:[0,0,0]
	v_mfma_scale_f32_16x16x128_f8f6f4 v[168:171], v[16:23], v[56:63], v[168:171], v235, v235 op_sel_hi:[0,0,0]
	v_mfma_scale_f32_16x16x128_f8f6f4 v[164:167], v[24:31], v[56:63], v[164:167], v235, v235 op_sel_hi:[0,0,0]
	s_setprio 0
	s_setprio 1
	s_waitcnt lgkmcnt(2)
	v_mfma_scale_f32_16x16x128_f8f6f4 v[160:163], v[8:15], v[32:39], v[160:163], v235, v235 op_sel_hi:[0,0,0]
	s_waitcnt lgkmcnt(0)
	v_mfma_scale_f32_16x16x128_f8f6f4 v[156:159], v[0:7], v[32:39], v[156:159], v235, v235 op_sel_hi:[0,0,0]
	v_mfma_scale_f32_16x16x128_f8f6f4 v[152:155], v[8:15], v[40:47], v[152:155], v235, v235 op_sel_hi:[0,0,0]
	v_mfma_scale_f32_16x16x128_f8f6f4 v[148:151], v[0:7], v[40:47], v[148:151], v235, v235 op_sel_hi:[0,0,0]
	v_mfma_scale_f32_16x16x128_f8f6f4 v[144:147], v[8:15], v[48:55], v[144:147], v235, v235 op_sel_hi:[0,0,0]
	v_mfma_scale_f32_16x16x128_f8f6f4 v[140:143], v[0:7], v[48:55], v[140:143], v235, v235 op_sel_hi:[0,0,0]
	v_mfma_scale_f32_16x16x128_f8f6f4 v[136:139], v[8:15], v[56:63], v[136:139], v235, v235 op_sel_hi:[0,0,0]
	v_mfma_scale_f32_16x16x128_f8f6f4 v[132:135], v[0:7], v[56:63], v[132:135], v235, v235 op_sel_hi:[0,0,0]
	s_setprio 0
	s_barrier
	ds_read_b128 v[32:35], v232 offset:0xc000
	ds_read_b128 v[36:39], v232 offset:0xc400
	ds_read_b128 v[40:43], v232 offset:0xc800
	ds_read_b128 v[44:47], v232 offset:0xcc00
	ds_read_b128 v[48:51], v232 offset:0xd000
	ds_read_b128 v[52:55], v232 offset:0xd400
	ds_read_b128 v[56:59], v232 offset:0xd800
	ds_read_b128 v[60:63], v232 offset:0xdc00
	s_mov_b32 m0, s64
	s_add_i32 s40, s86, 0x80
	buffer_load_dwordx4 v231, s[8:11], s40 offen lds
	s_add_i32 s40, s86, 0x10080
	s_mov_b32 m0, s65
	s_nop 0
	buffer_load_dwordx4 v231, s[8:11], s40 offen lds
	s_add_i32 s40, s86, 0x1080
	s_mov_b32 m0, s70
	s_nop 0
	buffer_load_dwordx4 v231, s[8:11], s40 offen lds
	s_add_i32 s40, s86, 0x11080
	s_mov_b32 m0, s71
	s_nop 0
	buffer_load_dwordx4 v231, s[8:11], s40 offen lds
	s_mov_b32 m0, s68
	s_add_i32 s10, s85, 0x8080
	buffer_load_dwordx4 v230, s[4:7], s33 offen lds
	s_mov_b32 m0, s69
	s_nop 0
	buffer_load_dwordx4 v230, s[4:7], s10 offen lds
	s_waitcnt vmcnt(8)
	s_waitcnt lgkmcnt(0)
	s_barrier
	s_setprio 1
	v_mfma_scale_f32_16x16x128_f8f6f4 v[128:131], v[16:23], v[32:39], v[128:131], v235, v235 op_sel_hi:[0,0,0]
	v_mfma_scale_f32_16x16x128_f8f6f4 v[124:127], v[24:31], v[32:39], v[124:127], v235, v235 op_sel_hi:[0,0,0]
	v_mfma_scale_f32_16x16x128_f8f6f4 v[120:123], v[16:23], v[40:47], v[120:123], v235, v235 op_sel_hi:[0,0,0]
	v_mfma_scale_f32_16x16x128_f8f6f4 v[116:119], v[24:31], v[40:47], v[116:119], v235, v235 op_sel_hi:[0,0,0]
	v_mfma_scale_f32_16x16x128_f8f6f4 v[112:115], v[16:23], v[48:55], v[112:115], v235, v235 op_sel_hi:[0,0,0]
	v_mfma_scale_f32_16x16x128_f8f6f4 v[108:111], v[24:31], v[48:55], v[108:111], v235, v235 op_sel_hi:[0,0,0]
	v_mfma_scale_f32_16x16x128_f8f6f4 v[104:107], v[16:23], v[56:63], v[104:107], v235, v235 op_sel_hi:[0,0,0]
	v_mfma_scale_f32_16x16x128_f8f6f4 v[100:103], v[24:31], v[56:63], v[100:103], v235, v235 op_sel_hi:[0,0,0]
	s_setprio 0
	s_setprio 1
	v_mfma_scale_f32_16x16x128_f8f6f4 v[96:99], v[8:15], v[32:39], v[96:99], v235, v235 op_sel_hi:[0,0,0]
	v_mfma_scale_f32_16x16x128_f8f6f4 v[92:95], v[0:7], v[32:39], v[92:95], v235, v235 op_sel_hi:[0,0,0]
	v_mfma_scale_f32_16x16x128_f8f6f4 v[88:91], v[8:15], v[40:47], v[88:91], v235, v235 op_sel_hi:[0,0,0]
	v_mfma_scale_f32_16x16x128_f8f6f4 v[84:87], v[0:7], v[40:47], v[84:87], v235, v235 op_sel_hi:[0,0,0]
	v_mfma_scale_f32_16x16x128_f8f6f4 v[80:83], v[8:15], v[48:55], v[80:83], v235, v235 op_sel_hi:[0,0,0]
	v_mfma_scale_f32_16x16x128_f8f6f4 v[76:79], v[0:7], v[48:55], v[76:79], v235, v235 op_sel_hi:[0,0,0]
	v_mfma_scale_f32_16x16x128_f8f6f4 v[72:75], v[8:15], v[56:63], v[72:75], v235, v235 op_sel_hi:[0,0,0]
	v_mfma_scale_f32_16x16x128_f8f6f4 v[68:71], v[0:7], v[56:63], v[68:71], v235, v235 op_sel_hi:[0,0,0]
	s_setprio 0
	s_barrier
	s_andn2_b64 vcc, exec, s[20:21]
	s_cbranch_vccnz .LBB0_1371
	s_barrier

.LBB0_1452:
	s_add_i32 s33, s80, 0x180
	s_add_i32 s36, s81, 0x180
	s_waitcnt lgkmcnt(0)
	s_barrier
	s_setprio 1
	v_mfma_scale_f32_16x16x128_f8f6f4 v[128:131], v[24:31], v[56:63], 0, v235, v235 op_sel_hi:[0,0,0]
	v_mfma_scale_f32_16x16x128_f8f6f4 v[124:127], v[16:23], v[56:63], 0, v235, v235 op_sel_hi:[0,0,0]
	v_mfma_scale_f32_16x16x128_f8f6f4 v[120:123], v[24:31], v[48:55], 0, v235, v235 op_sel_hi:[0,0,0]
	v_mfma_scale_f32_16x16x128_f8f6f4 v[116:119], v[16:23], v[48:55], 0, v235, v235 op_sel_hi:[0,0,0]
	v_mfma_scale_f32_16x16x128_f8f6f4 v[112:115], v[24:31], v[40:47], 0, v235, v235 op_sel_hi:[0,0,0]
	v_mfma_scale_f32_16x16x128_f8f6f4 v[108:111], v[16:23], v[40:47], 0, v235, v235 op_sel_hi:[0,0,0]
	v_mfma_scale_f32_16x16x128_f8f6f4 v[104:107], v[24:31], v[32:39], 0, v235, v235 op_sel_hi:[0,0,0]
	v_mfma_scale_f32_16x16x128_f8f6f4 v[100:103], v[16:23], v[32:39], 0, v235, v235 op_sel_hi:[0,0,0]
	s_setprio 0
	s_setprio 1
	v_mfma_scale_f32_16x16x128_f8f6f4 v[96:99], v[8:15], v[56:63], 0, v235, v235 op_sel_hi:[0,0,0]
	v_mfma_scale_f32_16x16x128_f8f6f4 v[92:95], v[0:7], v[56:63], 0, v235, v235 op_sel_hi:[0,0,0]
	v_mfma_scale_f32_16x16x128_f8f6f4 v[88:91], v[8:15], v[48:55], 0, v235, v235 op_sel_hi:[0,0,0]
	v_mfma_scale_f32_16x16x128_f8f6f4 v[84:87], v[0:7], v[48:55], 0, v235, v235 op_sel_hi:[0,0,0]
	v_mfma_scale_f32_16x16x128_f8f6f4 v[80:83], v[8:15], v[40:47], 0, v235, v235 op_sel_hi:[0,0,0]
	v_mfma_scale_f32_16x16x128_f8f6f4 v[76:79], v[0:7], v[40:47], 0, v235, v235 op_sel_hi:[0,0,0]
	v_mfma_scale_f32_16x16x128_f8f6f4 v[72:75], v[8:15], v[32:39], 0, v235, v235 op_sel_hi:[0,0,0]
	v_mfma_scale_f32_16x16x128_f8f6f4 v[68:71], v[0:7], v[32:39], 0, v235, v235 op_sel_hi:[0,0,0]
	s_setprio 0
	s_barrier
	ds_read_b128 v[16:19], v233 offset:0x8000
	ds_read_b128 v[20:23], v233 offset:0x8400
	ds_read_b128 v[24:27], v233 offset:0x8800
	ds_read_b128 v[28:31], v233 offset:0x8c00
	ds_read_b128 v[32:35], v232 offset:0x8000
	ds_read_b128 v[36:39], v232 offset:0x8400
	ds_read_b128 v[40:43], v232 offset:0x8800
	ds_read_b128 v[44:47], v232 offset:0x8c00
	ds_read_b128 v[48:51], v232 offset:0x9000
	ds_read_b128 v[52:55], v232 offset:0x9400
	ds_read_b128 v[56:59], v232 offset:0x9800
	ds_read_b128 v[60:63], v232 offset:0x9c00
	ds_read_b128 v[8:11], v233 offset:0xc000
	ds_read_b128 v[12:15], v233 offset:0xc400
	ds_read_b128 v[0:3], v233 offset:0xc800
	ds_read_b128 v[4:7], v233 offset:0xcc00
	s_mov_b32 m0, s62
	s_add_i32 s10, s80, 0x10100
	buffer_load_dwordx4 v230, s[4:7], s10 offen lds
	s_add_i32 s10, s80, 0x18100
	s_mov_b32 m0, s63
	s_nop 0
	buffer_load_dwordx4 v230, s[4:7], s10 offen lds
	s_waitcnt vmcnt(8)
	s_waitcnt lgkmcnt(4)
	s_barrier
	s_setprio 1
	v_mfma_scale_f32_16x16x128_f8f6f4 v[192:195], v[16:23], v[32:39], v[192:195], v235, v235 op_sel_hi:[0,0,0]
	v_mfma_scale_f32_16x16x128_f8f6f4 v[188:191], v[24:31], v[32:39], v[188:191], v235, v235 op_sel_hi:[0,0,0]
	v_mfma_scale_f32_16x16x128_f8f6f4 v[184:187], v[16:23], v[40:47], v[184:187], v235, v235 op_sel_hi:[0,0,0]
	v_mfma_scale_f32_16x16x128_f8f6f4 v[180:183], v[24:31], v[40:47], v[180:183], v235, v235 op_sel_hi:[0,0,0]
	v_mfma_scale_f32_16x16x128_f8f6f4 v[176:179], v[16:23], v[48:55], v[176:179], v235, v235 op_sel_hi:[0,0,0]
	v_mfma_scale_f32_16x16x128_f8f6f4 v[172:175], v[24:31], v[48:55], v[172:175], v235, v235 op_sel_hi:[0,0,0]
	v_mfma_scale_f32_16x16x128_f8f6f4 v[168:171], v[16:23], v[56:63], v[168:171], v235, v235 op_sel_hi:[0,0,0]
	v_mfma_scale_f32_16x16x128_f8f6f4 v[164:167], v[24:31], v[56:63], v[164:167], v235, v235 op_sel_hi:[0,0,0]
	s_setprio 0
	s_setprio 1
	s_waitcnt lgkmcnt(2)
	v_mfma_scale_f32_16x16x128_f8f6f4 v[160:163], v[8:15], v[32:39], v[160:163], v235, v235 op_sel_hi:[0,0,0]
	s_waitcnt lgkmcnt(0)
	v_mfma_scale_f32_16x16x128_f8f6f4 v[156:159], v[0:7], v[32:39], v[156:159], v235, v235 op_sel_hi:[0,0,0]
	v_mfma_scale_f32_16x16x128_f8f6f4 v[152:155], v[8:15], v[40:47], v[152:155], v235, v235 op_sel_hi:[0,0,0]
	v_mfma_scale_f32_16x16x128_f8f6f4 v[148:151], v[0:7], v[40:47], v[148:151], v235, v235 op_sel_hi:[0,0,0]
	v_mfma_scale_f32_16x16x128_f8f6f4 v[144:147], v[8:15], v[48:55], v[144:147], v235, v235 op_sel_hi:[0,0,0]
	v_mfma_scale_f32_16x16x128_f8f6f4 v[140:143], v[0:7], v[48:55], v[140:143], v235, v235 op_sel_hi:[0,0,0]
	v_mfma_scale_f32_16x16x128_f8f6f4 v[136:139], v[8:15], v[56:63], v[136:139], v235, v235 op_sel_hi:[0,0,0]
	v_mfma_scale_f32_16x16x128_f8f6f4 v[132:135], v[0:7], v[56:63], v[132:135], v235, v235 op_sel_hi:[0,0,0]
	s_setprio 0
	s_barrier
	ds_read_b128 v[32:35], v232 offset:0xc000
	ds_read_b128 v[36:39], v232 offset:0xc400
	ds_read_b128 v[40:43], v232 offset:0xc800
	ds_read_b128 v[44:47], v232 offset:0xcc00
	ds_read_b128 v[48:51], v232 offset:0xd000
	ds_read_b128 v[52:55], v232 offset:0xd400
	ds_read_b128 v[56:59], v232 offset:0xd800
	ds_read_b128 v[60:63], v232 offset:0xdc00
	s_mov_b32 m0, s64
	s_mov_b32 s10, s6
	s_mov_b32 s11, s7
	buffer_load_dwordx4 v231, s[8:11], s36 offen lds
	s_add_i32 s36, s81, 0x10180
	s_mov_b32 m0, s65
	s_nop 0
	buffer_load_dwordx4 v231, s[8:11], s36 offen lds
	s_add_i32 s36, s81, 0x1180
	s_mov_b32 m0, s70
	s_nop 0
	buffer_load_dwordx4 v231, s[8:11], s36 offen lds
	s_add_i32 s36, s81, 0x11180
	s_mov_b32 m0, s71
	s_nop 0
	buffer_load_dwordx4 v231, s[8:11], s36 offen lds
	s_mov_b32 m0, s68
	s_nop 0
	buffer_load_dwordx4 v230, s[4:7], s33 offen lds
	s_add_i32 s33, s80, 0x8180
	s_mov_b32 m0, s69
	s_nop 0
	buffer_load_dwordx4 v230, s[4:7], s33 offen lds
	s_waitcnt vmcnt(8)
	s_waitcnt lgkmcnt(0)
	s_barrier
	s_setprio 1
	v_mfma_scale_f32_16x16x128_f8f6f4 v[128:131], v[16:23], v[32:39], v[128:131], v235, v235 op_sel_hi:[0,0,0]
	v_mfma_scale_f32_16x16x128_f8f6f4 v[124:127], v[24:31], v[32:39], v[124:127], v235, v235 op_sel_hi:[0,0,0]
	v_mfma_scale_f32_16x16x128_f8f6f4 v[120:123], v[16:23], v[40:47], v[120:123], v235, v235 op_sel_hi:[0,0,0]
	v_mfma_scale_f32_16x16x128_f8f6f4 v[116:119], v[24:31], v[40:47], v[116:119], v235, v235 op_sel_hi:[0,0,0]
	v_mfma_scale_f32_16x16x128_f8f6f4 v[112:115], v[16:23], v[48:55], v[112:115], v235, v235 op_sel_hi:[0,0,0]
	v_mfma_scale_f32_16x16x128_f8f6f4 v[108:111], v[24:31], v[48:55], v[108:111], v235, v235 op_sel_hi:[0,0,0]
	v_mfma_scale_f32_16x16x128_f8f6f4 v[104:107], v[16:23], v[56:63], v[104:107], v235, v235 op_sel_hi:[0,0,0]
	v_mfma_scale_f32_16x16x128_f8f6f4 v[100:103], v[24:31], v[56:63], v[100:103], v235, v235 op_sel_hi:[0,0,0]
	s_setprio 0
	s_setprio 1
	v_mfma_scale_f32_16x16x128_f8f6f4 v[96:99], v[8:15], v[32:39], v[96:99], v235, v235 op_sel_hi:[0,0,0]
	v_mfma_scale_f32_16x16x128_f8f6f4 v[92:95], v[0:7], v[32:39], v[92:95], v235, v235 op_sel_hi:[0,0,0]
	v_mfma_scale_f32_16x16x128_f8f6f4 v[88:91], v[8:15], v[40:47], v[88:91], v235, v235 op_sel_hi:[0,0,0]
	v_mfma_scale_f32_16x16x128_f8f6f4 v[84:87], v[0:7], v[40:47], v[84:87], v235, v235 op_sel_hi:[0,0,0]
	v_mfma_scale_f32_16x16x128_f8f6f4 v[80:83], v[8:15], v[48:55], v[80:83], v235, v235 op_sel_hi:[0,0,0]
	v_mfma_scale_f32_16x16x128_f8f6f4 v[76:79], v[0:7], v[48:55], v[76:79], v235, v235 op_sel_hi:[0,0,0]
	v_mfma_scale_f32_16x16x128_f8f6f4 v[72:75], v[8:15], v[56:63], v[72:75], v235, v235 op_sel_hi:[0,0,0]
	v_mfma_scale_f32_16x16x128_f8f6f4 v[68:71], v[0:7], v[56:63], v[68:71], v235, v235 op_sel_hi:[0,0,0]
	s_setprio 0
	s_barrier
	ds_read_b128 v[16:19], v233 offset:0
	ds_read_b128 v[20:23], v233 offset:0x400
	ds_read_b128 v[24:27], v233 offset:0x800
	ds_read_b128 v[28:31], v233 offset:0xc00
	ds_read_b128 v[32:35], v232 offset:0
	ds_read_b128 v[36:39], v232 offset:0x400
	ds_read_b128 v[40:43], v232 offset:0x800
	ds_read_b128 v[44:47], v232 offset:0xc00
	ds_read_b128 v[48:51], v232 offset:0x1000
	ds_read_b128 v[52:55], v232 offset:0x1400
	ds_read_b128 v[56:59], v232 offset:0x1800
	ds_read_b128 v[60:63], v232 offset:0x1c00
	ds_read_b128 v[8:11], v233 offset:0x4000
	ds_read_b128 v[12:15], v233 offset:0x4400
	ds_read_b128 v[0:3], v233 offset:0x4800
	ds_read_b128 v[4:7], v233 offset:0x4c00
	s_add_i32 s33, s43, 0x80
	s_mov_b32 m0, s74
	s_add_i32 s36, s80, 0x10180
	buffer_load_dwordx4 v230, s[4:7], s36 offen lds
	s_add_i32 s36, s80, 0x18180
	s_mov_b32 m0, s76
	s_nop 0
	buffer_load_dwordx4 v230, s[4:7], s36 offen lds
	s_waitcnt vmcnt(8)
	s_waitcnt lgkmcnt(4)
	s_barrier
	s_setprio 1
	v_mfma_scale_f32_16x16x128_f8f6f4 v[192:195], v[16:23], v[32:39], v[192:195], v235, v235 op_sel_hi:[0,0,0]
	v_mfma_scale_f32_16x16x128_f8f6f4 v[188:191], v[24:31], v[32:39], v[188:191], v235, v235 op_sel_hi:[0,0,0]
	v_mfma_scale_f32_16x16x128_f8f6f4 v[184:187], v[16:23], v[40:47], v[184:187], v235, v235 op_sel_hi:[0,0,0]
	v_mfma_scale_f32_16x16x128_f8f6f4 v[180:183], v[24:31], v[40:47], v[180:183], v235, v235 op_sel_hi:[0,0,0]
	v_mfma_scale_f32_16x16x128_f8f6f4 v[176:179], v[16:23], v[48:55], v[176:179], v235, v235 op_sel_hi:[0,0,0]
	v_mfma_scale_f32_16x16x128_f8f6f4 v[172:175], v[24:31], v[48:55], v[172:175], v235, v235 op_sel_hi:[0,0,0]
	v_mfma_scale_f32_16x16x128_f8f6f4 v[168:171], v[16:23], v[56:63], v[168:171], v235, v235 op_sel_hi:[0,0,0]
	v_mfma_scale_f32_16x16x128_f8f6f4 v[164:167], v[24:31], v[56:63], v[164:167], v235, v235 op_sel_hi:[0,0,0]
	s_setprio 0
	s_setprio 1
	s_waitcnt lgkmcnt(2)
	v_mfma_scale_f32_16x16x128_f8f6f4 v[160:163], v[8:15], v[32:39], v[160:163], v235, v235 op_sel_hi:[0,0,0]
	s_waitcnt lgkmcnt(0)
	v_mfma_scale_f32_16x16x128_f8f6f4 v[156:159], v[0:7], v[32:39], v[156:159], v235, v235 op_sel_hi:[0,0,0]
	v_mfma_scale_f32_16x16x128_f8f6f4 v[152:155], v[8:15], v[40:47], v[152:155], v235, v235 op_sel_hi:[0,0,0]
	v_mfma_scale_f32_16x16x128_f8f6f4 v[148:151], v[0:7], v[40:47], v[148:151], v235, v235 op_sel_hi:[0,0,0]
	v_mfma_scale_f32_16x16x128_f8f6f4 v[144:147], v[8:15], v[48:55], v[144:147], v235, v235 op_sel_hi:[0,0,0]
	v_mfma_scale_f32_16x16x128_f8f6f4 v[140:143], v[0:7], v[48:55], v[140:143], v235, v235 op_sel_hi:[0,0,0]
	v_mfma_scale_f32_16x16x128_f8f6f4 v[136:139], v[8:15], v[56:63], v[136:139], v235, v235 op_sel_hi:[0,0,0]
	v_mfma_scale_f32_16x16x128_f8f6f4 v[132:135], v[0:7], v[56:63], v[132:135], v235, v235 op_sel_hi:[0,0,0]
	s_setprio 0
	s_barrier
	ds_read_b128 v[32:35], v232 offset:0x4000
	ds_read_b128 v[36:39], v232 offset:0x4400
	ds_read_b128 v[40:43], v232 offset:0x4800
	ds_read_b128 v[44:47], v232 offset:0x4c00
	ds_read_b128 v[48:51], v232 offset:0x5000
	ds_read_b128 v[52:55], v232 offset:0x5400
	ds_read_b128 v[56:59], v232 offset:0x5800
	ds_read_b128 v[60:63], v232 offset:0x5c00
	s_mov_b32 m0, s46
	s_nop 0
	buffer_load_dwordx4 v231, s[8:11], s78 offen lds
	s_add_i32 s36, s78, 0x10000
	s_mov_b32 m0, s47
	s_nop 0
	buffer_load_dwordx4 v231, s[8:11], s36 offen lds
	s_add_i32 s36, s78, 0x1000
	s_mov_b32 m0, s49
	s_nop 0
	buffer_load_dwordx4 v231, s[8:11], s36 offen lds
	s_add_i32 s36, s78, 0x11000
	s_mov_b32 m0, s50
	s_nop 0
	buffer_load_dwordx4 v231, s[8:11], s36 offen lds
	s_mov_b32 m0, s48
	s_add_i32 s36, s43, 0x8000
	buffer_load_dwordx4 v230, s[4:7], s43 offen lds
	s_mov_b32 m0, s51
	s_nop 0
	buffer_load_dwordx4 v230, s[4:7], s36 offen lds
	s_waitcnt vmcnt(8)
	s_waitcnt lgkmcnt(0)
	s_barrier
	s_setprio 1
	v_mfma_scale_f32_16x16x128_f8f6f4 v[128:131], v[16:23], v[32:39], v[128:131], v235, v235 op_sel_hi:[0,0,0]
	v_mfma_scale_f32_16x16x128_f8f6f4 v[124:127], v[24:31], v[32:39], v[124:127], v235, v235 op_sel_hi:[0,0,0]
	v_mfma_scale_f32_16x16x128_f8f6f4 v[120:123], v[16:23], v[40:47], v[120:123], v235, v235 op_sel_hi:[0,0,0]
	v_mfma_scale_f32_16x16x128_f8f6f4 v[116:119], v[24:31], v[40:47], v[116:119], v235, v235 op_sel_hi:[0,0,0]
	v_mfma_scale_f32_16x16x128_f8f6f4 v[112:115], v[16:23], v[48:55], v[112:115], v235, v235 op_sel_hi:[0,0,0]
	v_mfma_scale_f32_16x16x128_f8f6f4 v[108:111], v[24:31], v[48:55], v[108:111], v235, v235 op_sel_hi:[0,0,0]
	v_mfma_scale_f32_16x16x128_f8f6f4 v[104:107], v[16:23], v[56:63], v[104:107], v235, v235 op_sel_hi:[0,0,0]
	v_mfma_scale_f32_16x16x128_f8f6f4 v[100:103], v[24:31], v[56:63], v[100:103], v235, v235 op_sel_hi:[0,0,0]
	s_setprio 0
	s_setprio 1
	v_mfma_scale_f32_16x16x128_f8f6f4 v[96:99], v[8:15], v[32:39], v[96:99], v235, v235 op_sel_hi:[0,0,0]
	v_mfma_scale_f32_16x16x128_f8f6f4 v[92:95], v[0:7], v[32:39], v[92:95], v235, v235 op_sel_hi:[0,0,0]
	v_mfma_scale_f32_16x16x128_f8f6f4 v[88:91], v[8:15], v[40:47], v[88:91], v235, v235 op_sel_hi:[0,0,0]
	v_mfma_scale_f32_16x16x128_f8f6f4 v[84:87], v[0:7], v[40:47], v[84:87], v235, v235 op_sel_hi:[0,0,0]
	v_mfma_scale_f32_16x16x128_f8f6f4 v[80:83], v[8:15], v[48:55], v[80:83], v235, v235 op_sel_hi:[0,0,0]
	v_mfma_scale_f32_16x16x128_f8f6f4 v[76:79], v[0:7], v[48:55], v[76:79], v235, v235 op_sel_hi:[0,0,0]
	v_mfma_scale_f32_16x16x128_f8f6f4 v[72:75], v[8:15], v[56:63], v[72:75], v235, v235 op_sel_hi:[0,0,0]
	v_mfma_scale_f32_16x16x128_f8f6f4 v[68:71], v[0:7], v[56:63], v[68:71], v235, v235 op_sel_hi:[0,0,0]
	s_setprio 0
	s_barrier
	ds_read_b128 v[16:19], v233 offset:0x8000
	ds_read_b128 v[20:23], v233 offset:0x8400
	ds_read_b128 v[24:27], v233 offset:0x8800
	ds_read_b128 v[28:31], v233 offset:0x8c00
	ds_read_b128 v[32:35], v232 offset:0x8000
	ds_read_b128 v[36:39], v232 offset:0x8400
	ds_read_b128 v[40:43], v232 offset:0x8800
	ds_read_b128 v[44:47], v232 offset:0x8c00
	ds_read_b128 v[48:51], v232 offset:0x9000
	ds_read_b128 v[52:55], v232 offset:0x9400
	ds_read_b128 v[56:59], v232 offset:0x9800
	ds_read_b128 v[60:63], v232 offset:0x9c00
	ds_read_b128 v[8:11], v233 offset:0xc000
	ds_read_b128 v[12:15], v233 offset:0xc400
	ds_read_b128 v[0:3], v233 offset:0xc800
	ds_read_b128 v[4:7], v233 offset:0xcc00
	s_mov_b32 m0, s62
	s_add_i32 s36, s43, 0x10000
	buffer_load_dwordx4 v230, s[4:7], s36 offen lds
	s_add_i32 s36, s43, 0x18000
	s_mov_b32 m0, s63
	s_nop 0
	buffer_load_dwordx4 v230, s[4:7], s36 offen lds
	s_waitcnt vmcnt(8)
	s_waitcnt lgkmcnt(4)
	s_barrier
	s_setprio 1
	v_mfma_scale_f32_16x16x128_f8f6f4 v[192:195], v[16:23], v[32:39], v[192:195], v235, v235 op_sel_hi:[0,0,0]
	v_mfma_scale_f32_16x16x128_f8f6f4 v[188:191], v[24:31], v[32:39], v[188:191], v235, v235 op_sel_hi:[0,0,0]
	v_mfma_scale_f32_16x16x128_f8f6f4 v[184:187], v[16:23], v[40:47], v[184:187], v235, v235 op_sel_hi:[0,0,0]
	v_mfma_scale_f32_16x16x128_f8f6f4 v[180:183], v[24:31], v[40:47], v[180:183], v235, v235 op_sel_hi:[0,0,0]
	v_mfma_scale_f32_16x16x128_f8f6f4 v[176:179], v[16:23], v[48:55], v[176:179], v235, v235 op_sel_hi:[0,0,0]
	v_mfma_scale_f32_16x16x128_f8f6f4 v[172:175], v[24:31], v[48:55], v[172:175], v235, v235 op_sel_hi:[0,0,0]
	v_mfma_scale_f32_16x16x128_f8f6f4 v[168:171], v[16:23], v[56:63], v[168:171], v235, v235 op_sel_hi:[0,0,0]
	v_mfma_scale_f32_16x16x128_f8f6f4 v[164:167], v[24:31], v[56:63], v[164:167], v235, v235 op_sel_hi:[0,0,0]
	s_setprio 0
	s_setprio 1
	s_waitcnt lgkmcnt(2)
	v_mfma_scale_f32_16x16x128_f8f6f4 v[160:163], v[8:15], v[32:39], v[160:163], v235, v235 op_sel_hi:[0,0,0]
	s_waitcnt lgkmcnt(0)
	v_mfma_scale_f32_16x16x128_f8f6f4 v[156:159], v[0:7], v[32:39], v[156:159], v235, v235 op_sel_hi:[0,0,0]
	v_mfma_scale_f32_16x16x128_f8f6f4 v[152:155], v[8:15], v[40:47], v[152:155], v235, v235 op_sel_hi:[0,0,0]
	v_mfma_scale_f32_16x16x128_f8f6f4 v[148:151], v[0:7], v[40:47], v[148:151], v235, v235 op_sel_hi:[0,0,0]
	v_mfma_scale_f32_16x16x128_f8f6f4 v[144:147], v[8:15], v[48:55], v[144:147], v235, v235 op_sel_hi:[0,0,0]
	v_mfma_scale_f32_16x16x128_f8f6f4 v[140:143], v[0:7], v[48:55], v[140:143], v235, v235 op_sel_hi:[0,0,0]
	v_mfma_scale_f32_16x16x128_f8f6f4 v[136:139], v[8:15], v[56:63], v[136:139], v235, v235 op_sel_hi:[0,0,0]
	v_mfma_scale_f32_16x16x128_f8f6f4 v[132:135], v[0:7], v[56:63], v[132:135], v235, v235 op_sel_hi:[0,0,0]
	s_setprio 0
	s_barrier
	ds_read_b128 v[32:35], v232 offset:0xc000
	ds_read_b128 v[36:39], v232 offset:0xc400
	ds_read_b128 v[40:43], v232 offset:0xc800
	ds_read_b128 v[44:47], v232 offset:0xcc00
	ds_read_b128 v[48:51], v232 offset:0xd000
	ds_read_b128 v[52:55], v232 offset:0xd400
	ds_read_b128 v[56:59], v232 offset:0xd800
	ds_read_b128 v[60:63], v232 offset:0xdc00
	s_mov_b32 m0, s64
	s_add_i32 s36, s78, 0x80
	buffer_load_dwordx4 v231, s[8:11], s36 offen lds
	s_add_i32 s36, s78, 0x10080
	s_mov_b32 m0, s65
	s_nop 0
	buffer_load_dwordx4 v231, s[8:11], s36 offen lds
	s_add_i32 s36, s78, 0x1080
	s_mov_b32 m0, s70
	s_nop 0
	buffer_load_dwordx4 v231, s[8:11], s36 offen lds
	s_add_i32 s36, s78, 0x11080
	s_mov_b32 m0, s71
	s_nop 0
	buffer_load_dwordx4 v231, s[8:11], s36 offen lds
	s_mov_b32 m0, s68
	s_add_i32 s10, s43, 0x8080
	buffer_load_dwordx4 v230, s[4:7], s33 offen lds
	s_mov_b32 m0, s69
	s_nop 0
	buffer_load_dwordx4 v230, s[4:7], s10 offen lds
	s_waitcnt vmcnt(8)
	s_waitcnt lgkmcnt(0)
	s_barrier
	s_setprio 1
	v_mfma_scale_f32_16x16x128_f8f6f4 v[128:131], v[16:23], v[32:39], v[128:131], v235, v235 op_sel_hi:[0,0,0]
	v_mfma_scale_f32_16x16x128_f8f6f4 v[124:127], v[24:31], v[32:39], v[124:127], v235, v235 op_sel_hi:[0,0,0]
	v_mfma_scale_f32_16x16x128_f8f6f4 v[120:123], v[16:23], v[40:47], v[120:123], v235, v235 op_sel_hi:[0,0,0]
	v_mfma_scale_f32_16x16x128_f8f6f4 v[116:119], v[24:31], v[40:47], v[116:119], v235, v235 op_sel_hi:[0,0,0]
	v_mfma_scale_f32_16x16x128_f8f6f4 v[112:115], v[16:23], v[48:55], v[112:115], v235, v235 op_sel_hi:[0,0,0]
	v_mfma_scale_f32_16x16x128_f8f6f4 v[108:111], v[24:31], v[48:55], v[108:111], v235, v235 op_sel_hi:[0,0,0]
	v_mfma_scale_f32_16x16x128_f8f6f4 v[104:107], v[16:23], v[56:63], v[104:107], v235, v235 op_sel_hi:[0,0,0]
	v_mfma_scale_f32_16x16x128_f8f6f4 v[100:103], v[24:31], v[56:63], v[100:103], v235, v235 op_sel_hi:[0,0,0]
	s_setprio 0
	s_setprio 1
	v_mfma_scale_f32_16x16x128_f8f6f4 v[96:99], v[8:15], v[32:39], v[96:99], v235, v235 op_sel_hi:[0,0,0]
	v_mfma_scale_f32_16x16x128_f8f6f4 v[92:95], v[0:7], v[32:39], v[92:95], v235, v235 op_sel_hi:[0,0,0]
	v_mfma_scale_f32_16x16x128_f8f6f4 v[88:91], v[8:15], v[40:47], v[88:91], v235, v235 op_sel_hi:[0,0,0]
	v_mfma_scale_f32_16x16x128_f8f6f4 v[84:87], v[0:7], v[40:47], v[84:87], v235, v235 op_sel_hi:[0,0,0]
	v_mfma_scale_f32_16x16x128_f8f6f4 v[80:83], v[8:15], v[48:55], v[80:83], v235, v235 op_sel_hi:[0,0,0]
	v_mfma_scale_f32_16x16x128_f8f6f4 v[76:79], v[0:7], v[48:55], v[76:79], v235, v235 op_sel_hi:[0,0,0]
	v_mfma_scale_f32_16x16x128_f8f6f4 v[72:75], v[8:15], v[56:63], v[72:75], v235, v235 op_sel_hi:[0,0,0]
	v_mfma_scale_f32_16x16x128_f8f6f4 v[68:71], v[0:7], v[56:63], v[68:71], v235, v235 op_sel_hi:[0,0,0]
	s_setprio 0
	s_barrier
	s_andn2_b64 vcc, exec, s[20:21]
	s_cbranch_vccnz .LBB0_1454
	s_barrier
